# packed-f32 epilogues for P16 and P5, packed FMAs in the router phase P14
# speedup vs baseline: 1.0089x; 1.0057x over previous
; __device__ __forceinline__ unsigned cvt_pk_bf16(float lo, float hi) { unsigned r; asm volatile("v_cvt_pk_bf16_f32 %0, %1, %2" : "=v"(r) : "v"(lo), "v"(hi)); return r; }
; __device__ __forceinline__ float fast_sigmoid(float x) { return __builtin_amdgcn_rcpf(1.0f + fast_exp(-x)); }
; #define NEXT_ROW(roff, m, LD) do { roff += (size_t)((m) == 3 ? 80 : 16) * (LD); asm volatile("" : "+v"(roff) :: "memory"); } while (0)
;     __device__ __forceinline__ void operator()(Acc& acc, const Unit& u, int wr, int wc, int fr, int fq, LAS unsigned char* le, int wid, int lane, int& cpm) const {
;     ...
;         size_t roff = (size_t)(row0 + wr * 64 + fr) * DFF + u.pn * 128 + wc * 32 + fq * 8;
; #pragma unroll
;         for (int ai = 0; ai < 2; ++ai)
; #pragma unroll
;             for (int m = 0; m < 4; ++m) { const int rt = ai * 128 + wr * 64 + m * 16 + fr; const float rs = S[rt] * pscale;
;                 const f32x4 ga = acc[ai][0][m][0] * rs, gb = acc[ai][0][m][1] * rs, ua = acc[ai][1][m][0] * rs, ub = acc[ai][1][m][1] * rs; f32x4 ha, hb;
; #pragma unroll
;                 for (int j = 0; j < 4; ++j) { ha[j] = ga[j] * fast_sigmoid(ga[j]) * ua[j]; hb[j] = gb[j] * fast_sigmoid(gb[j]) * ub[j]; }
;                 u32x4 w; w.x = cvt_pk_bf16(ha[0], ha[1]); w.y = cvt_pk_bf16(ha[2], ha[3]); w.z = cvt_pk_bf16(hb[0], hb[1]); w.w = cvt_pk_bf16(hb[2], hb[3]);
;                 ST_NT((u32x4*)(out + roff), w);
;                 NEXT_ROW(roff, m, DFF); }
.LBB0_1255:
	ds_read_b32 v200, v193
	ds_read_b32 v201, v193 offset:64
	ds_read_b32 v202, v193 offset:128
	ds_read_b32 v203, v193 offset:192
	ds_read_b32 v204, v193 offset:512
	ds_read_b32 v205, v193 offset:576
	ds_read_b32 v206, v193 offset:640
	ds_read_b32 v207, v193 offset:704
	s_lshl_b32 s10, s28, 7
	s_ashr_i32 s11, s10, 31
	v_add_u32_e32 v15, s30, v190
	s_movk_i32 s3, 0x1c00
	v_lshl_add_u64 v[18:19], v[172:173], 0, s[10:11]
	v_mad_i64_i32 v[18:19], s[10:11], v15, s3, v[18:19]
	v_lshl_add_u64 v[20:21], v[18:19], 1, s[12:13]
	s_waitcnt lgkmcnt(0)
	v_mul_f32_e32 v8, 0x3a000000, v200
	v_pk_mul_f32 v[216:217], v[156:157], v[152:153]
	v_pk_mul_f32 v[218:219], v[158:159], v[154:155]
	v_pk_mul_f32 v[220:221], v[144:145], v[148:149]
	v_pk_mul_f32 v[222:223], v[146:147], v[150:151]
	v_mul_f32_e32 v10, 0xbfb8aa3b, v8
	v_mul_f32_e32 v12, v8, v8
	v_pk_mul_f32 v[208:209], v[156:157], v[10:11] op_sel_hi:[1,0]
	v_pk_mul_f32 v[210:211], v[158:159], v[10:11] op_sel_hi:[1,0]
	v_pk_mul_f32 v[212:213], v[144:145], v[10:11] op_sel_hi:[1,0]
	v_pk_mul_f32 v[214:215], v[146:147], v[10:11] op_sel_hi:[1,0]
	v_rcp_f32_e32 v12, v12
	v_exp_f32_e32 v208, v208
	v_exp_f32_e32 v209, v209
	v_exp_f32_e32 v210, v210
	v_exp_f32_e32 v211, v211
	v_exp_f32_e32 v212, v212
	v_exp_f32_e32 v213, v213
	v_exp_f32_e32 v214, v214
	v_exp_f32_e32 v215, v215
	v_pk_fma_f32 v[208:209], v[208:209], v[12:13], v[12:13] op_sel_hi:[1,0,0]
	v_pk_fma_f32 v[210:211], v[210:211], v[12:13], v[12:13] op_sel_hi:[1,0,0]
	v_pk_fma_f32 v[212:213], v[212:213], v[12:13], v[12:13] op_sel_hi:[1,0,0]
	v_pk_fma_f32 v[214:215], v[214:215], v[12:13], v[12:13] op_sel_hi:[1,0,0]
	v_rcp_f32_e32 v208, v208
	v_rcp_f32_e32 v209, v209
	v_rcp_f32_e32 v210, v210
	v_rcp_f32_e32 v211, v211
	v_rcp_f32_e32 v212, v212
	v_rcp_f32_e32 v213, v213
	v_rcp_f32_e32 v214, v214
	v_rcp_f32_e32 v215, v215
	v_pk_mul_f32 v[216:217], v[216:217], v[208:209]
	v_pk_mul_f32 v[218:219], v[218:219], v[210:211]
	v_pk_mul_f32 v[220:221], v[220:221], v[212:213]
	v_pk_mul_f32 v[222:223], v[222:223], v[214:215]
	v_cvt_pk_bf16_f32 v0, v216, v217
	v_cvt_pk_bf16_f32 v1, v218, v219
	v_cvt_pk_bf16_f32 v2, v220, v221
	v_cvt_pk_bf16_f32 v3, v222, v223
	s_nop 0
	global_store_dwordx4 v[20:21], v[0:3], off
	v_lshl_add_u64 v[20:21], s[16:17], 1, v[20:21]
	v_mul_f32_e32 v8, 0x3a000000, v201
	v_pk_mul_f32 v[216:217], v[140:141], v[136:137]
	v_pk_mul_f32 v[218:219], v[142:143], v[138:139]
	v_pk_mul_f32 v[220:221], v[132:133], v[128:129]
	v_pk_mul_f32 v[222:223], v[134:135], v[130:131]
	v_mul_f32_e32 v10, 0xbfb8aa3b, v8
	v_mul_f32_e32 v12, v8, v8
	v_pk_mul_f32 v[208:209], v[140:141], v[10:11] op_sel_hi:[1,0]
	v_pk_mul_f32 v[210:211], v[142:143], v[10:11] op_sel_hi:[1,0]
	v_pk_mul_f32 v[212:213], v[132:133], v[10:11] op_sel_hi:[1,0]
	v_pk_mul_f32 v[214:215], v[134:135], v[10:11] op_sel_hi:[1,0]
	v_rcp_f32_e32 v12, v12
	v_exp_f32_e32 v208, v208
	v_exp_f32_e32 v209, v209
	v_exp_f32_e32 v210, v210
	v_exp_f32_e32 v211, v211
	v_exp_f32_e32 v212, v212
	v_exp_f32_e32 v213, v213
	v_exp_f32_e32 v214, v214
	v_exp_f32_e32 v215, v215
	v_pk_fma_f32 v[208:209], v[208:209], v[12:13], v[12:13] op_sel_hi:[1,0,0]
	v_pk_fma_f32 v[210:211], v[210:211], v[12:13], v[12:13] op_sel_hi:[1,0,0]
	v_pk_fma_f32 v[212:213], v[212:213], v[12:13], v[12:13] op_sel_hi:[1,0,0]
	v_pk_fma_f32 v[214:215], v[214:215], v[12:13], v[12:13] op_sel_hi:[1,0,0]
	v_rcp_f32_e32 v208, v208
	v_rcp_f32_e32 v209, v209
	v_rcp_f32_e32 v210, v210
	v_rcp_f32_e32 v211, v211
	v_rcp_f32_e32 v212, v212
	v_rcp_f32_e32 v213, v213
	v_rcp_f32_e32 v214, v214
	v_rcp_f32_e32 v215, v215
	v_pk_mul_f32 v[216:217], v[216:217], v[208:209]
	v_pk_mul_f32 v[218:219], v[218:219], v[210:211]
	v_pk_mul_f32 v[220:221], v[220:221], v[212:213]
	v_pk_mul_f32 v[222:223], v[222:223], v[214:215]
	v_cvt_pk_bf16_f32 v0, v216, v217
	v_cvt_pk_bf16_f32 v1, v218, v219
	v_cvt_pk_bf16_f32 v2, v220, v221
	v_cvt_pk_bf16_f32 v3, v222, v223
	s_nop 0
	global_store_dwordx4 v[20:21], v[0:3], off
	v_lshl_add_u64 v[20:21], s[16:17], 1, v[20:21]
	v_mul_f32_e32 v8, 0x3a000000, v202
	v_pk_mul_f32 v[216:217], v[124:125], v[120:121]
	v_pk_mul_f32 v[218:219], v[126:127], v[122:123]
	v_pk_mul_f32 v[220:221], v[116:117], v[112:113]
	v_pk_mul_f32 v[222:223], v[118:119], v[114:115]
	v_mul_f32_e32 v10, 0xbfb8aa3b, v8
	v_mul_f32_e32 v12, v8, v8
	v_pk_mul_f32 v[208:209], v[124:125], v[10:11] op_sel_hi:[1,0]
	v_pk_mul_f32 v[210:211], v[126:127], v[10:11] op_sel_hi:[1,0]
	v_pk_mul_f32 v[212:213], v[116:117], v[10:11] op_sel_hi:[1,0]
	v_pk_mul_f32 v[214:215], v[118:119], v[10:11] op_sel_hi:[1,0]
	v_rcp_f32_e32 v12, v12
	v_exp_f32_e32 v208, v208
	v_exp_f32_e32 v209, v209
	v_exp_f32_e32 v210, v210
	v_exp_f32_e32 v211, v211
	v_exp_f32_e32 v212, v212
	v_exp_f32_e32 v213, v213
	v_exp_f32_e32 v214, v214
	v_exp_f32_e32 v215, v215
	v_pk_fma_f32 v[208:209], v[208:209], v[12:13], v[12:13] op_sel_hi:[1,0,0]
	v_pk_fma_f32 v[210:211], v[210:211], v[12:13], v[12:13] op_sel_hi:[1,0,0]
	v_pk_fma_f32 v[212:213], v[212:213], v[12:13], v[12:13] op_sel_hi:[1,0,0]
	v_pk_fma_f32 v[214:215], v[214:215], v[12:13], v[12:13] op_sel_hi:[1,0,0]
	v_rcp_f32_e32 v208, v208
	v_rcp_f32_e32 v209, v209
	v_rcp_f32_e32 v210, v210
	v_rcp_f32_e32 v211, v211
	v_rcp_f32_e32 v212, v212
	v_rcp_f32_e32 v213, v213
	v_rcp_f32_e32 v214, v214
	v_rcp_f32_e32 v215, v215
	v_pk_mul_f32 v[216:217], v[216:217], v[208:209]
	v_pk_mul_f32 v[218:219], v[218:219], v[210:211]
	v_pk_mul_f32 v[220:221], v[220:221], v[212:213]
	v_pk_mul_f32 v[222:223], v[222:223], v[214:215]
	v_cvt_pk_bf16_f32 v0, v216, v217
	v_cvt_pk_bf16_f32 v1, v218, v219
	v_cvt_pk_bf16_f32 v2, v220, v221
	v_cvt_pk_bf16_f32 v3, v222, v223
	s_nop 0
; __device__ __forceinline__ unsigned cvt_pk_bf16(float lo, float hi) { unsigned r; asm volatile("v_cvt_pk_bf16_f32 %0, %1, %2" : "=v"(r) : "v"(lo), "v"(hi)); return r; }
; __device__ __forceinline__ float fast_sigmoid(float x) { return __builtin_amdgcn_rcpf(1.0f + fast_exp(-x)); }
; #define NEXT_ROW(roff, m, LD) do { roff += (size_t)((m) == 3 ? 80 : 16) * (LD); asm volatile("" : "+v"(roff) :: "memory"); } while (0)
;     __device__ __forceinline__ void operator()(Acc& acc, const Unit& u, int wr, int wc, int fr, int fq, LAS unsigned char* le, int wid, int lane, int& cpm) const {
;     ...
;             for (int m = 0; m < 4; ++m) { const int rt = ai * 128 + wr * 64 + m * 16 + fr; const float rs = S[rt] * pscale;
;                 const f32x4 ga = acc[ai][0][m][0] * rs, gb = acc[ai][0][m][1] * rs, ua = acc[ai][1][m][0] * rs, ub = acc[ai][1][m][1] * rs; f32x4 ha, hb;
; #pragma unroll
;                 for (int j = 0; j < 4; ++j) { ha[j] = ga[j] * fast_sigmoid(ga[j]) * ua[j]; hb[j] = gb[j] * fast_sigmoid(gb[j]) * ub[j]; }
;                 u32x4 w; w.x = cvt_pk_bf16(ha[0], ha[1]); w.y = cvt_pk_bf16(ha[2], ha[3]); w.z = cvt_pk_bf16(hb[0], hb[1]); w.w = cvt_pk_bf16(hb[2], hb[3]);
;                 ST_NT((u32x4*)(out + roff), w);
;                 NEXT_ROW(roff, m, DFF); }
	global_store_dwordx4 v[20:21], v[0:3], off
	v_lshl_add_u64 v[20:21], s[16:17], 1, v[20:21]
	v_mul_f32_e32 v8, 0x3a000000, v203
	v_pk_mul_f32 v[216:217], v[108:109], v[104:105]
	v_pk_mul_f32 v[218:219], v[110:111], v[106:107]
	v_pk_mul_f32 v[220:221], v[100:101], v[96:97]
	v_pk_mul_f32 v[222:223], v[102:103], v[98:99]
	v_mul_f32_e32 v10, 0xbfb8aa3b, v8
	v_mul_f32_e32 v12, v8, v8
	v_pk_mul_f32 v[208:209], v[108:109], v[10:11] op_sel_hi:[1,0]
	v_pk_mul_f32 v[210:211], v[110:111], v[10:11] op_sel_hi:[1,0]
	v_pk_mul_f32 v[212:213], v[100:101], v[10:11] op_sel_hi:[1,0]
	v_pk_mul_f32 v[214:215], v[102:103], v[10:11] op_sel_hi:[1,0]
	v_rcp_f32_e32 v12, v12
	v_exp_f32_e32 v208, v208
	v_exp_f32_e32 v209, v209
	v_exp_f32_e32 v210, v210
	v_exp_f32_e32 v211, v211
	v_exp_f32_e32 v212, v212
	v_exp_f32_e32 v213, v213
	v_exp_f32_e32 v214, v214
	v_exp_f32_e32 v215, v215
	v_pk_fma_f32 v[208:209], v[208:209], v[12:13], v[12:13] op_sel_hi:[1,0,0]
	v_pk_fma_f32 v[210:211], v[210:211], v[12:13], v[12:13] op_sel_hi:[1,0,0]
	v_pk_fma_f32 v[212:213], v[212:213], v[12:13], v[12:13] op_sel_hi:[1,0,0]
	v_pk_fma_f32 v[214:215], v[214:215], v[12:13], v[12:13] op_sel_hi:[1,0,0]
	v_rcp_f32_e32 v208, v208
	v_rcp_f32_e32 v209, v209
	v_rcp_f32_e32 v210, v210
	v_rcp_f32_e32 v211, v211
	v_rcp_f32_e32 v212, v212
	v_rcp_f32_e32 v213, v213
	v_rcp_f32_e32 v214, v214
	v_rcp_f32_e32 v215, v215
	v_pk_mul_f32 v[216:217], v[216:217], v[208:209]
	v_pk_mul_f32 v[218:219], v[218:219], v[210:211]
	v_pk_mul_f32 v[220:221], v[220:221], v[212:213]
	v_pk_mul_f32 v[222:223], v[222:223], v[214:215]
	v_cvt_pk_bf16_f32 v0, v216, v217
	v_cvt_pk_bf16_f32 v1, v218, v219
	v_cvt_pk_bf16_f32 v2, v220, v221
	v_cvt_pk_bf16_f32 v3, v222, v223
	s_nop 0
	global_store_dwordx4 v[20:21], v[0:3], off
	v_lshl_add_u64 v[20:21], s[18:19], 1, v[20:21]
	v_mul_f32_e32 v8, 0x3a000000, v204
	v_pk_mul_f32 v[216:217], v[92:93], v[88:89]
	v_pk_mul_f32 v[218:219], v[94:95], v[90:91]
	v_pk_mul_f32 v[220:221], v[84:85], v[80:81]
	v_pk_mul_f32 v[222:223], v[86:87], v[82:83]
	v_mul_f32_e32 v10, 0xbfb8aa3b, v8
	v_mul_f32_e32 v12, v8, v8
	v_pk_mul_f32 v[208:209], v[92:93], v[10:11] op_sel_hi:[1,0]
	v_pk_mul_f32 v[210:211], v[94:95], v[10:11] op_sel_hi:[1,0]
	v_pk_mul_f32 v[212:213], v[84:85], v[10:11] op_sel_hi:[1,0]
	v_pk_mul_f32 v[214:215], v[86:87], v[10:11] op_sel_hi:[1,0]
	v_rcp_f32_e32 v12, v12
	v_exp_f32_e32 v208, v208
	v_exp_f32_e32 v209, v209
	v_exp_f32_e32 v210, v210
	v_exp_f32_e32 v211, v211
	v_exp_f32_e32 v212, v212
	v_exp_f32_e32 v213, v213
	v_exp_f32_e32 v214, v214
	v_exp_f32_e32 v215, v215
	v_pk_fma_f32 v[208:209], v[208:209], v[12:13], v[12:13] op_sel_hi:[1,0,0]
	v_pk_fma_f32 v[210:211], v[210:211], v[12:13], v[12:13] op_sel_hi:[1,0,0]
	v_pk_fma_f32 v[212:213], v[212:213], v[12:13], v[12:13] op_sel_hi:[1,0,0]
	v_pk_fma_f32 v[214:215], v[214:215], v[12:13], v[12:13] op_sel_hi:[1,0,0]
	v_rcp_f32_e32 v208, v208
	v_rcp_f32_e32 v209, v209
	v_rcp_f32_e32 v210, v210
	v_rcp_f32_e32 v211, v211
	v_rcp_f32_e32 v212, v212
	v_rcp_f32_e32 v213, v213
	v_rcp_f32_e32 v214, v214
	v_rcp_f32_e32 v215, v215
	v_pk_mul_f32 v[216:217], v[216:217], v[208:209]
	v_pk_mul_f32 v[218:219], v[218:219], v[210:211]
	v_pk_mul_f32 v[220:221], v[220:221], v[212:213]
	v_pk_mul_f32 v[222:223], v[222:223], v[214:215]
	v_cvt_pk_bf16_f32 v0, v216, v217
	v_cvt_pk_bf16_f32 v1, v218, v219
	v_cvt_pk_bf16_f32 v2, v220, v221
	v_cvt_pk_bf16_f32 v3, v222, v223
	s_nop 0
	global_store_dwordx4 v[20:21], v[0:3], off
	v_lshl_add_u64 v[20:21], s[16:17], 1, v[20:21]
	v_mul_f32_e32 v8, 0x3a000000, v205
	v_pk_mul_f32 v[216:217], v[76:77], v[72:73]
	v_pk_mul_f32 v[218:219], v[78:79], v[74:75]
	v_pk_mul_f32 v[220:221], v[68:69], v[64:65]
	v_pk_mul_f32 v[222:223], v[70:71], v[66:67]
	v_mul_f32_e32 v10, 0xbfb8aa3b, v8
	v_mul_f32_e32 v12, v8, v8
	v_pk_mul_f32 v[208:209], v[76:77], v[10:11] op_sel_hi:[1,0]
	v_pk_mul_f32 v[210:211], v[78:79], v[10:11] op_sel_hi:[1,0]
	v_pk_mul_f32 v[212:213], v[68:69], v[10:11] op_sel_hi:[1,0]
	v_pk_mul_f32 v[214:215], v[70:71], v[10:11] op_sel_hi:[1,0]
	v_rcp_f32_e32 v12, v12
	v_exp_f32_e32 v208, v208
	v_exp_f32_e32 v209, v209
	v_exp_f32_e32 v210, v210
	v_exp_f32_e32 v211, v211
	v_exp_f32_e32 v212, v212
	v_exp_f32_e32 v213, v213
	v_exp_f32_e32 v214, v214
	v_exp_f32_e32 v215, v215
	v_pk_fma_f32 v[208:209], v[208:209], v[12:13], v[12:13] op_sel_hi:[1,0,0]
; __device__ __forceinline__ unsigned cvt_pk_bf16(float lo, float hi) { unsigned r; asm volatile("v_cvt_pk_bf16_f32 %0, %1, %2" : "=v"(r) : "v"(lo), "v"(hi)); return r; }
; __device__ __forceinline__ float fast_sigmoid(float x) { return __builtin_amdgcn_rcpf(1.0f + fast_exp(-x)); }
; #define PG8_BAR __builtin_amdgcn_s_barrier()
; #define PG8_ACC_INIT(unit) do { if constexpr (Epi::ACC_INIT) { E.init(acc, unit, wr, wc, fr, fq); } else { \
;         _Pragma("unroll") for (int a = 0; a < 2; ++a) _Pragma("unroll") for (int b = 0; b < 2; ++b) _Pragma("unroll") for (int m = 0; m < 4; ++m) _Pragma("unroll") for (int n = 0; n < 2; ++n) acc[a][b][m][n] = (f32x4){0.f, 0.f, 0.f, 0.f}; } } while (0)
; #define NEXT_ROW(roff, m, LD) do { roff += (size_t)((m) == 3 ? 80 : 16) * (LD); asm volatile("" : "+v"(roff) :: "memory"); } while (0)
; template <class Epi, class Sched, class Prob>
; __device__ __forceinline__ void gemm_phase(LAS unsigned char* lds, LAS unsigned char* lds_epi, const Prob g, const Sched& S, const Epi& E, int wid) {
;     ...
;         if (!has_next) break;
;         PG8_ACC_INIT(nxt);
;         cur = nxt; cA = nA; cB = nB; ++ui;
;         if (wr == 1) PG8_BAR;
;     __device__ __forceinline__ void operator()(Acc& acc, const Unit& u, int wr, int wc, int fr, int fq, LAS unsigned char* le, int wid, int lane, int& cpm) const {
;     ...
;             for (int m = 0; m < 4; ++m) { const int rt = ai * 128 + wr * 64 + m * 16 + fr; const float rs = S[rt] * pscale;
;                 const f32x4 ga = acc[ai][0][m][0] * rs, gb = acc[ai][0][m][1] * rs, ua = acc[ai][1][m][0] * rs, ub = acc[ai][1][m][1] * rs; f32x4 ha, hb;
; #pragma unroll
;                 for (int j = 0; j < 4; ++j) { ha[j] = ga[j] * fast_sigmoid(ga[j]) * ua[j]; hb[j] = gb[j] * fast_sigmoid(gb[j]) * ub[j]; }
;                 u32x4 w; w.x = cvt_pk_bf16(ha[0], ha[1]); w.y = cvt_pk_bf16(ha[2], ha[3]); w.z = cvt_pk_bf16(hb[0], hb[1]); w.w = cvt_pk_bf16(hb[2], hb[3]);
;                 ST_NT((u32x4*)(out + roff), w);
;                 NEXT_ROW(roff, m, DFF); }
	v_pk_fma_f32 v[210:211], v[210:211], v[12:13], v[12:13] op_sel_hi:[1,0,0]
	v_pk_fma_f32 v[212:213], v[212:213], v[12:13], v[12:13] op_sel_hi:[1,0,0]
	v_pk_fma_f32 v[214:215], v[214:215], v[12:13], v[12:13] op_sel_hi:[1,0,0]
	v_rcp_f32_e32 v208, v208
	v_rcp_f32_e32 v209, v209
	v_rcp_f32_e32 v210, v210
	v_rcp_f32_e32 v211, v211
	v_rcp_f32_e32 v212, v212
	v_rcp_f32_e32 v213, v213
	v_rcp_f32_e32 v214, v214
	v_rcp_f32_e32 v215, v215
	v_pk_mul_f32 v[216:217], v[216:217], v[208:209]
	v_pk_mul_f32 v[218:219], v[218:219], v[210:211]
	v_pk_mul_f32 v[220:221], v[220:221], v[212:213]
	v_pk_mul_f32 v[222:223], v[222:223], v[214:215]
	v_cvt_pk_bf16_f32 v0, v216, v217
	v_cvt_pk_bf16_f32 v1, v218, v219
	v_cvt_pk_bf16_f32 v2, v220, v221
	v_cvt_pk_bf16_f32 v3, v222, v223
	s_nop 0
	global_store_dwordx4 v[20:21], v[0:3], off
	v_lshl_add_u64 v[20:21], s[16:17], 1, v[20:21]
	v_mul_f32_e32 v8, 0x3a000000, v206
	v_pk_mul_f32 v[216:217], v[60:61], v[56:57]
	v_pk_mul_f32 v[218:219], v[62:63], v[58:59]
	v_pk_mul_f32 v[220:221], v[52:53], v[48:49]
	v_pk_mul_f32 v[222:223], v[54:55], v[50:51]
	v_mul_f32_e32 v10, 0xbfb8aa3b, v8
	v_mul_f32_e32 v12, v8, v8
	v_pk_mul_f32 v[208:209], v[60:61], v[10:11] op_sel_hi:[1,0]
	v_pk_mul_f32 v[210:211], v[62:63], v[10:11] op_sel_hi:[1,0]
	v_pk_mul_f32 v[212:213], v[52:53], v[10:11] op_sel_hi:[1,0]
	v_pk_mul_f32 v[214:215], v[54:55], v[10:11] op_sel_hi:[1,0]
	v_rcp_f32_e32 v12, v12
	v_exp_f32_e32 v208, v208
	v_exp_f32_e32 v209, v209
	v_exp_f32_e32 v210, v210
	v_exp_f32_e32 v211, v211
	v_exp_f32_e32 v212, v212
	v_exp_f32_e32 v213, v213
	v_exp_f32_e32 v214, v214
	v_exp_f32_e32 v215, v215
	v_pk_fma_f32 v[208:209], v[208:209], v[12:13], v[12:13] op_sel_hi:[1,0,0]
	v_pk_fma_f32 v[210:211], v[210:211], v[12:13], v[12:13] op_sel_hi:[1,0,0]
	v_pk_fma_f32 v[212:213], v[212:213], v[12:13], v[12:13] op_sel_hi:[1,0,0]
	v_pk_fma_f32 v[214:215], v[214:215], v[12:13], v[12:13] op_sel_hi:[1,0,0]
	v_rcp_f32_e32 v208, v208
	v_rcp_f32_e32 v209, v209
	v_rcp_f32_e32 v210, v210
	v_rcp_f32_e32 v211, v211
	v_rcp_f32_e32 v212, v212
	v_rcp_f32_e32 v213, v213
	v_rcp_f32_e32 v214, v214
	v_rcp_f32_e32 v215, v215
	v_pk_mul_f32 v[216:217], v[216:217], v[208:209]
	v_pk_mul_f32 v[218:219], v[218:219], v[210:211]
	v_pk_mul_f32 v[220:221], v[220:221], v[212:213]
	v_pk_mul_f32 v[222:223], v[222:223], v[214:215]
	v_cvt_pk_bf16_f32 v0, v216, v217
	v_cvt_pk_bf16_f32 v1, v218, v219
	v_cvt_pk_bf16_f32 v2, v220, v221
	v_cvt_pk_bf16_f32 v3, v222, v223
	s_nop 0
	global_store_dwordx4 v[20:21], v[0:3], off
	v_lshl_add_u64 v[20:21], s[16:17], 1, v[20:21]
	v_mul_f32_e32 v8, 0x3a000000, v207
	v_pk_mul_f32 v[216:217], v[44:45], v[40:41]
	v_pk_mul_f32 v[218:219], v[46:47], v[42:43]
	v_pk_mul_f32 v[220:221], v[36:37], v[32:33]
	v_pk_mul_f32 v[222:223], v[38:39], v[34:35]
	v_mul_f32_e32 v10, 0xbfb8aa3b, v8
	v_mul_f32_e32 v12, v8, v8
	v_pk_mul_f32 v[208:209], v[44:45], v[10:11] op_sel_hi:[1,0]
	v_pk_mul_f32 v[210:211], v[46:47], v[10:11] op_sel_hi:[1,0]
	v_pk_mul_f32 v[212:213], v[36:37], v[10:11] op_sel_hi:[1,0]
	v_pk_mul_f32 v[214:215], v[38:39], v[10:11] op_sel_hi:[1,0]
	v_rcp_f32_e32 v12, v12
	v_exp_f32_e32 v208, v208
	v_exp_f32_e32 v209, v209
	v_exp_f32_e32 v210, v210
	v_exp_f32_e32 v211, v211
	v_exp_f32_e32 v212, v212
	v_exp_f32_e32 v213, v213
	v_exp_f32_e32 v214, v214
	v_exp_f32_e32 v215, v215
	v_pk_fma_f32 v[208:209], v[208:209], v[12:13], v[12:13] op_sel_hi:[1,0,0]
	v_pk_fma_f32 v[210:211], v[210:211], v[12:13], v[12:13] op_sel_hi:[1,0,0]
	v_pk_fma_f32 v[212:213], v[212:213], v[12:13], v[12:13] op_sel_hi:[1,0,0]
	v_pk_fma_f32 v[214:215], v[214:215], v[12:13], v[12:13] op_sel_hi:[1,0,0]
	v_rcp_f32_e32 v208, v208
	v_rcp_f32_e32 v209, v209
	v_rcp_f32_e32 v210, v210
	v_rcp_f32_e32 v211, v211
	v_rcp_f32_e32 v212, v212
	v_rcp_f32_e32 v213, v213
	v_rcp_f32_e32 v214, v214
	v_rcp_f32_e32 v215, v215
	v_pk_mul_f32 v[216:217], v[216:217], v[208:209]
	v_pk_mul_f32 v[218:219], v[218:219], v[210:211]
	v_pk_mul_f32 v[220:221], v[220:221], v[212:213]
	v_pk_mul_f32 v[222:223], v[222:223], v[214:215]
	v_cvt_pk_bf16_f32 v0, v216, v217
	v_cvt_pk_bf16_f32 v1, v218, v219
	v_cvt_pk_bf16_f32 v2, v220, v221
	v_cvt_pk_bf16_f32 v3, v222, v223
	s_nop 0
	global_store_dwordx4 v[20:21], v[0:3], off
	s_andn2_b64 vcc, exec, s[22:23]
	s_mov_b64 s[10:11], -1
	s_cbranch_vccnz .LBB0_1243
	s_and_b64 vcc, exec, s[6:7]
	s_cbranch_vccnz .LBB0_1242
	s_barrier
	s_branch .LBB0_1242

; #define LAS __attribute__((address_space(3)))
; __global__ void __launch_bounds__(NTHR, 2) fwd_kernel(Args args) {
;     ...
;         LAS float* Rg = (LAS float*)ring;
;         LAS int* lcnt = (LAS int*)lepi;
;         for (int i = tid; i < DM * 8; i += NTHR) { const int k = i >> 3, e = i & 7; Rg[e * DM + k] = od_ffn_norm[k] * od_router[i]; }
;         for (int c = wg; c < T / 64; c += G) {
;             if (tid < 8) lcnt[tid] = 0;
;             __syncthreads();
;             const int t0 = c * 64 + wave * 8;
;             float acc[8][8], ssq[8];
; #pragma unroll
;             for (int q = 0; q < 8; ++q) { ssq[q] = 0.f;
; #pragma unroll
;                 for (int e = 0; e < 8; ++e) acc[q][e] = 0.f; }
.LBB0_1812:
	v_readlane_b32 s0, v254, 0
	v_readlane_b32 s1, v254, 1
	s_cmp_lt_i32 s0, 15
	s_cselect_b64 s[0:1], -1, 0
	s_and_b64 s[2:3], s[0:1], s[2:3]
	s_andn2_b64 vcc, exec, s[2:3]
	s_lshl_b32 s33, s85, 3
	s_cbranch_vccnz .LBB0_1851
	v_mbcnt_lo_u32_b32 v210, -1, 0
	v_mbcnt_hi_u32_b32 v210, -1, v210
	s_load_dwordx4 s[4:7], s[94:95], 0xb0
	s_load_dwordx2 s[8:9], s[94:95], 0xe0
	v_add_u32_e32 v211, s91, v210
	v_lshlrev_b32_e32 v208, 4, v210
	v_lshlrev_b32_e32 v212, 5, v211
	v_lshlrev_b32_e32 v213, 2, v211
	v_lshrrev_b32_e32 v214, 3, v211
	v_lshlrev_b32_e32 v214, 4, v214
	v_and_b32_e32 v215, 7, v211
	v_lshl_add_u32 v214, v215, 11, v214
	v_add_u32_e32 v216, 0x4000, v212
	v_add_u32_e32 v217, 0x8000, v212
	v_add_u32_e32 v218, 0xc000, v212
	v_add_u32_e32 v219, 0x1000, v213
	s_waitcnt lgkmcnt(0)
	global_load_dwordx4 v[64:67], v212, s[6:7]
	global_load_dwordx4 v[68:71], v212, s[6:7] offset:16
	global_load_dwordx4 v[72:75], v216, s[6:7]
	global_load_dwordx4 v[76:79], v216, s[6:7] offset:16
	global_load_dwordx4 v[80:83], v217, s[6:7]
	global_load_dwordx4 v[84:87], v217, s[6:7] offset:16
	global_load_dwordx4 v[88:91], v218, s[6:7]
	global_load_dwordx4 v[92:95], v218, s[6:7] offset:16
	global_load_dword v96, v213, s[4:5]
	global_load_dword v97, v213, s[4:5] offset:2048
	global_load_dword v98, v219, s[4:5]
	global_load_dword v99, v219, s[4:5] offset:2048
	s_add_u32 s10, s8, 0x35000000
	s_addc_u32 s11, s9, 0
	s_mov_b32 s15, 0xffff0000
	s_mov_b32 s63, 0xf800000
	s_mov_b32 s65, 0x3fb8aa3b
	s_mov_b32 s66, 0xc2ce8ed0
	s_mov_b32 s67, 0x42b17218
	v_mov_b32_e32 v220, 0
	v_mov_b32_e32 v221, 1
	v_mov_b32_e32 v222, 0x358637bd
	v_mov_b32_e32 v223, 0x260
	v_mov_b32_e32 v224, 0xff800000
	v_mov_b32_e32 v225, 0x7f800000
	v_mov_b32_e32 v226, 0x362000
	v_mov_b32_e32 v227, 0x372000
	v_mov_b32_e32 v228, 0x352000
	s_mov_b32 s20, 0x20000
	v_lshl_add_u32 v229, v211, 2, s20
	s_waitcnt vmcnt(0)
	v_mul_f32_e32 v64, v64, v96
	v_mul_f32_e32 v65, v65, v96
	v_mul_f32_e32 v66, v66, v96
	v_mul_f32_e32 v67, v67, v96
	v_mul_f32_e32 v68, v68, v96
	v_mul_f32_e32 v69, v69, v96
	v_mul_f32_e32 v70, v70, v96
	v_mul_f32_e32 v71, v71, v96
	v_mul_f32_e32 v72, v72, v97
	v_mul_f32_e32 v73, v73, v97
	v_mul_f32_e32 v74, v74, v97
	v_mul_f32_e32 v75, v75, v97
	v_mul_f32_e32 v76, v76, v97
	v_mul_f32_e32 v77, v77, v97
	v_mul_f32_e32 v78, v78, v97
	v_mul_f32_e32 v79, v79, v97
	v_mul_f32_e32 v80, v80, v98
	v_mul_f32_e32 v81, v81, v98
	v_mul_f32_e32 v82, v82, v98
	v_mul_f32_e32 v83, v83, v98
	v_mul_f32_e32 v84, v84, v98
	v_mul_f32_e32 v85, v85, v98
	v_mul_f32_e32 v86, v86, v98
	v_mul_f32_e32 v87, v87, v98
	v_mul_f32_e32 v88, v88, v99
	v_mul_f32_e32 v89, v89, v99
	v_mul_f32_e32 v90, v90, v99
	v_mul_f32_e32 v91, v91, v99
	v_mul_f32_e32 v92, v92, v99
	v_mul_f32_e32 v93, v93, v99
	v_mul_f32_e32 v94, v94, v99
	v_mul_f32_e32 v95, v95, v99
	ds_write_b128 v214, v[64:67] offset:0
	ds_write_b128 v214, v[68:71] offset:1024
	ds_write_b128 v214, v[72:75] offset:16384
	ds_write_b128 v214, v[76:79] offset:17408
	ds_write_b128 v214, v[80:83] offset:32768
	ds_write_b128 v214, v[84:87] offset:33792
	ds_write_b128 v214, v[88:91] offset:49152
	ds_write_b128 v214, v[92:95] offset:50176
	s_mov_b32 s12, s93
.Lr14_chunk:
	s_waitcnt vmcnt(0)
	v_cmp_gt_u32_e32 vcc, 8, v211
	s_and_saveexec_b64 s[2:3], vcc
	ds_write_b32 v229, v220
	s_mov_b64 exec, s[2:3]
	s_lshl_b32 s13, s12, 6
	s_add_i32 s13, s13, s33
	s_lshl_b32 s14, s13, 12
	s_add_u32 s40, s10, s14
	s_addc_u32 s41, s11, 0
	s_add_u32 s42, s40, 0x1000
	s_addc_u32 s43, s41, 0
	s_add_u32 s44, s42, 0x1000
	s_addc_u32 s45, s43, 0
	s_add_u32 s46, s44, 0x1000
	s_addc_u32 s47, s45, 0
	s_add_u32 s48, s46, 0x1000
	s_addc_u32 s49, s47, 0
	s_add_u32 s50, s48, 0x1000
	s_addc_u32 s51, s49, 0
	s_add_u32 s52, s50, 0x1000
	s_addc_u32 s53, s51, 0
	s_add_u32 s54, s52, 0x1000
	s_addc_u32 s55, s53, 0
	global_load_dwordx4 v[64:67], v208, s[40:41] offset:0
	global_load_dwordx4 v[68:71], v208, s[42:43] offset:0
	global_load_dwordx4 v[72:75], v208, s[44:45] offset:0
	global_load_dwordx4 v[76:79], v208, s[46:47] offset:0
	global_load_dwordx4 v[80:83], v208, s[48:49] offset:0
	global_load_dwordx4 v[84:87], v208, s[50:51] offset:0
	global_load_dwordx4 v[88:91], v208, s[52:53] offset:0
	global_load_dwordx4 v[92:95], v208, s[54:55] offset:0
	global_load_dwordx4 v[96:99], v208, s[40:41] offset:1024
	global_load_dwordx4 v[100:103], v208, s[42:43] offset:1024
	global_load_dwordx4 v[104:107], v208, s[44:45] offset:1024
	global_load_dwordx4 v[108:111], v208, s[46:47] offset:1024
	global_load_dwordx4 v[112:115], v208, s[48:49] offset:1024
	global_load_dwordx4 v[116:119], v208, s[50:51] offset:1024
	global_load_dwordx4 v[120:123], v208, s[52:53] offset:1024
	global_load_dwordx4 v[124:127], v208, s[54:55] offset:1024
	v_mov_b32_e32 v0, 0
	v_mov_b32_e32 v1, 0
	v_mov_b32_e32 v2, 0
	v_mov_b32_e32 v3, 0
	v_mov_b32_e32 v4, 0
	v_mov_b32_e32 v5, 0
	v_mov_b32_e32 v6, 0
	v_mov_b32_e32 v7, 0
	v_mov_b32_e32 v8, 0
	v_mov_b32_e32 v9, 0
	v_mov_b32_e32 v10, 0
	v_mov_b32_e32 v11, 0
	v_mov_b32_e32 v12, 0
	v_mov_b32_e32 v13, 0
	v_mov_b32_e32 v14, 0
	v_mov_b32_e32 v15, 0
	v_mov_b32_e32 v16, 0
	v_mov_b32_e32 v17, 0
	v_mov_b32_e32 v18, 0
	v_mov_b32_e32 v19, 0
	v_mov_b32_e32 v20, 0
	v_mov_b32_e32 v21, 0
	v_mov_b32_e32 v22, 0
	v_mov_b32_e32 v23, 0
	v_mov_b32_e32 v24, 0
	v_mov_b32_e32 v25, 0
	v_mov_b32_e32 v26, 0
	v_mov_b32_e32 v27, 0
	v_mov_b32_e32 v28, 0
	v_mov_b32_e32 v29, 0
	v_mov_b32_e32 v30, 0
	v_mov_b32_e32 v31, 0
	v_mov_b32_e32 v32, 0
	v_mov_b32_e32 v33, 0
	v_mov_b32_e32 v34, 0
	v_mov_b32_e32 v35, 0
	v_mov_b32_e32 v36, 0
	v_mov_b32_e32 v37, 0
	v_mov_b32_e32 v38, 0
	v_mov_b32_e32 v39, 0
	v_mov_b32_e32 v40, 0
	v_mov_b32_e32 v41, 0
	v_mov_b32_e32 v42, 0
	v_mov_b32_e32 v43, 0
	v_mov_b32_e32 v44, 0
	v_mov_b32_e32 v45, 0
	v_mov_b32_e32 v46, 0
	v_mov_b32_e32 v47, 0
	v_mov_b32_e32 v48, 0
	v_mov_b32_e32 v49, 0
	v_mov_b32_e32 v50, 0
	v_mov_b32_e32 v51, 0
	v_mov_b32_e32 v52, 0
	v_mov_b32_e32 v53, 0
	v_mov_b32_e32 v54, 0
	v_mov_b32_e32 v55, 0
	v_mov_b32_e32 v56, 0
	v_mov_b32_e32 v57, 0
	v_mov_b32_e32 v58, 0
	v_mov_b32_e32 v59, 0
	v_mov_b32_e32 v60, 0
	v_mov_b32_e32 v61, 0
	v_mov_b32_e32 v62, 0
	v_mov_b32_e32 v63, 0
	v_mov_b32_e32 v192, 0
	v_mov_b32_e32 v193, 0
	v_mov_b32_e32 v194, 0
	v_mov_b32_e32 v195, 0
	v_mov_b32_e32 v196, 0
	v_mov_b32_e32 v197, 0
	v_mov_b32_e32 v198, 0
	v_mov_b32_e32 v199, 0
	v_mov_b32_e32 v200, 0
	v_mov_b32_e32 v201, 0
	v_mov_b32_e32 v202, 0
	v_mov_b32_e32 v203, 0
	v_mov_b32_e32 v204, 0
	v_mov_b32_e32 v205, 0
	v_mov_b32_e32 v206, 0
	v_mov_b32_e32 v207, 0
	s_waitcnt lgkmcnt(0)
	s_barrier
; #define LAS __attribute__((address_space(3)))
; __global__ void __launch_bounds__(NTHR, 2) fwd_kernel(Args args) {
;     ...
;             for (int i = 0; i < 16; ++i) { const int k = 2 * lane + 128 * i; f32x2 rv[8]; unsigned xw[8];
; #pragma unroll
;                 for (int e = 0; e < 8; ++e) rv[e] = *(const LAS f32x2*)(Rg + e * DM + k);
; #pragma unroll
;                 for (int q = 0; q < 8; ++q) xw[q] = *(const unsigned*)(XB + (size_t)(t0 + q) * DM + k);
; #pragma unroll
;                 for (int q = 0; q < 8; ++q) { const float x0 = bflo(xw[q]), x1 = bfhi(xw[q]); ssq[q] += x0 * x0 + x1 * x1;
; #pragma unroll
;                     for (int e = 0; e < 8; ++e) acc[q][e] += x0 * rv[e].x + x1 * rv[e].y; } }
	ds_read_b128 v[128:131], v208 offset:0
	ds_read_b128 v[132:135], v208 offset:1024
	ds_read_b128 v[136:139], v208 offset:2048
	ds_read_b128 v[140:143], v208 offset:3072
	ds_read_b128 v[144:147], v208 offset:4096
	ds_read_b128 v[148:151], v208 offset:5120
	ds_read_b128 v[152:155], v208 offset:6144
	ds_read_b128 v[156:159], v208 offset:7168
	ds_read_b128 v[160:163], v208 offset:8192
	ds_read_b128 v[164:167], v208 offset:9216
	ds_read_b128 v[168:171], v208 offset:10240
	ds_read_b128 v[172:175], v208 offset:11264
	ds_read_b128 v[176:179], v208 offset:12288
	ds_read_b128 v[180:183], v208 offset:13312
	ds_read_b128 v[184:187], v208 offset:14336
	ds_read_b128 v[188:191], v208 offset:15360
	s_waitcnt vmcnt(8)
	s_waitcnt lgkmcnt(0)
	v_lshlrev_b32_e32 v232, 16, v64
	v_and_b32_e32 v233, s15, v64
	v_lshlrev_b32_e32 v234, 16, v65
	v_and_b32_e32 v235, s15, v65
	v_lshlrev_b32_e32 v236, 16, v66
	v_and_b32_e32 v237, s15, v66
	v_lshlrev_b32_e32 v238, 16, v67
	v_and_b32_e32 v239, s15, v67
	v_pk_fma_f32 v[192:193], v[232:233], v[232:233], v[192:193]
	v_pk_fma_f32 v[192:193], v[234:235], v[234:235], v[192:193]
	v_pk_fma_f32 v[192:193], v[236:237], v[236:237], v[192:193]
	v_pk_fma_f32 v[192:193], v[238:239], v[238:239], v[192:193]
	v_pk_fma_f32 v[0:1], v[232:233], v[128:129], v[0:1] op_sel_hi:[0,1,1]
	v_pk_fma_f32 v[2:3], v[232:233], v[130:131], v[2:3] op_sel_hi:[0,1,1]
	v_pk_fma_f32 v[4:5], v[232:233], v[132:133], v[4:5] op_sel_hi:[0,1,1]
	v_pk_fma_f32 v[6:7], v[232:233], v[134:135], v[6:7] op_sel_hi:[0,1,1]
	v_pk_fma_f32 v[0:1], v[232:233], v[136:137], v[0:1] op_sel:[1,0,0] op_sel_hi:[1,1,1]
	v_pk_fma_f32 v[2:3], v[232:233], v[138:139], v[2:3] op_sel:[1,0,0] op_sel_hi:[1,1,1]
	v_pk_fma_f32 v[4:5], v[232:233], v[140:141], v[4:5] op_sel:[1,0,0] op_sel_hi:[1,1,1]
	v_pk_fma_f32 v[6:7], v[232:233], v[142:143], v[6:7] op_sel:[1,0,0] op_sel_hi:[1,1,1]
	v_pk_fma_f32 v[0:1], v[234:235], v[144:145], v[0:1] op_sel_hi:[0,1,1]
	v_pk_fma_f32 v[2:3], v[234:235], v[146:147], v[2:3] op_sel_hi:[0,1,1]
	v_pk_fma_f32 v[4:5], v[234:235], v[148:149], v[4:5] op_sel_hi:[0,1,1]
	v_pk_fma_f32 v[6:7], v[234:235], v[150:151], v[6:7] op_sel_hi:[0,1,1]
	v_pk_fma_f32 v[0:1], v[234:235], v[152:153], v[0:1] op_sel:[1,0,0] op_sel_hi:[1,1,1]
	v_pk_fma_f32 v[2:3], v[234:235], v[154:155], v[2:3] op_sel:[1,0,0] op_sel_hi:[1,1,1]
	v_pk_fma_f32 v[4:5], v[234:235], v[156:157], v[4:5] op_sel:[1,0,0] op_sel_hi:[1,1,1]
	v_pk_fma_f32 v[6:7], v[234:235], v[158:159], v[6:7] op_sel:[1,0,0] op_sel_hi:[1,1,1]
	v_pk_fma_f32 v[0:1], v[236:237], v[160:161], v[0:1] op_sel_hi:[0,1,1]
	v_pk_fma_f32 v[2:3], v[236:237], v[162:163], v[2:3] op_sel_hi:[0,1,1]
	v_pk_fma_f32 v[4:5], v[236:237], v[164:165], v[4:5] op_sel_hi:[0,1,1]
	v_pk_fma_f32 v[6:7], v[236:237], v[166:167], v[6:7] op_sel_hi:[0,1,1]
	v_pk_fma_f32 v[0:1], v[236:237], v[168:169], v[0:1] op_sel:[1,0,0] op_sel_hi:[1,1,1]
	v_pk_fma_f32 v[2:3], v[236:237], v[170:171], v[2:3] op_sel:[1,0,0] op_sel_hi:[1,1,1]
	v_pk_fma_f32 v[4:5], v[236:237], v[172:173], v[4:5] op_sel:[1,0,0] op_sel_hi:[1,1,1]
	v_pk_fma_f32 v[6:7], v[236:237], v[174:175], v[6:7] op_sel:[1,0,0] op_sel_hi:[1,1,1]
	v_pk_fma_f32 v[0:1], v[238:239], v[176:177], v[0:1] op_sel_hi:[0,1,1]
	v_pk_fma_f32 v[2:3], v[238:239], v[178:179], v[2:3] op_sel_hi:[0,1,1]
	v_pk_fma_f32 v[4:5], v[238:239], v[180:181], v[4:5] op_sel_hi:[0,1,1]
	v_pk_fma_f32 v[6:7], v[238:239], v[182:183], v[6:7] op_sel_hi:[0,1,1]
	v_pk_fma_f32 v[0:1], v[238:239], v[184:185], v[0:1] op_sel:[1,0,0] op_sel_hi:[1,1,1]
	v_pk_fma_f32 v[2:3], v[238:239], v[186:187], v[2:3] op_sel:[1,0,0] op_sel_hi:[1,1,1]
	v_pk_fma_f32 v[4:5], v[238:239], v[188:189], v[4:5] op_sel:[1,0,0] op_sel_hi:[1,1,1]
	v_pk_fma_f32 v[6:7], v[238:239], v[190:191], v[6:7] op_sel:[1,0,0] op_sel_hi:[1,1,1]
	v_lshlrev_b32_e32 v232, 16, v68
	v_and_b32_e32 v233, s15, v68
	v_lshlrev_b32_e32 v234, 16, v69
	v_and_b32_e32 v235, s15, v69
	v_lshlrev_b32_e32 v236, 16, v70
	v_and_b32_e32 v237, s15, v70
	v_lshlrev_b32_e32 v238, 16, v71
	v_and_b32_e32 v239, s15, v71
	v_pk_fma_f32 v[194:195], v[232:233], v[232:233], v[194:195]
	v_pk_fma_f32 v[194:195], v[234:235], v[234:235], v[194:195]
	v_pk_fma_f32 v[194:195], v[236:237], v[236:237], v[194:195]
	v_pk_fma_f32 v[194:195], v[238:239], v[238:239], v[194:195]
	v_pk_fma_f32 v[8:9], v[232:233], v[128:129], v[8:9] op_sel_hi:[0,1,1]
	v_pk_fma_f32 v[10:11], v[232:233], v[130:131], v[10:11] op_sel_hi:[0,1,1]
	v_pk_fma_f32 v[12:13], v[232:233], v[132:133], v[12:13] op_sel_hi:[0,1,1]
	v_pk_fma_f32 v[14:15], v[232:233], v[134:135], v[14:15] op_sel_hi:[0,1,1]
	v_pk_fma_f32 v[8:9], v[232:233], v[136:137], v[8:9] op_sel:[1,0,0] op_sel_hi:[1,1,1]
	v_pk_fma_f32 v[10:11], v[232:233], v[138:139], v[10:11] op_sel:[1,0,0] op_sel_hi:[1,1,1]
	v_pk_fma_f32 v[12:13], v[232:233], v[140:141], v[12:13] op_sel:[1,0,0] op_sel_hi:[1,1,1]
	v_pk_fma_f32 v[14:15], v[232:233], v[142:143], v[14:15] op_sel:[1,0,0] op_sel_hi:[1,1,1]
	v_pk_fma_f32 v[8:9], v[234:235], v[144:145], v[8:9] op_sel_hi:[0,1,1]
	v_pk_fma_f32 v[10:11], v[234:235], v[146:147], v[10:11] op_sel_hi:[0,1,1]
	v_pk_fma_f32 v[12:13], v[234:235], v[148:149], v[12:13] op_sel_hi:[0,1,1]
	v_pk_fma_f32 v[14:15], v[234:235], v[150:151], v[14:15] op_sel_hi:[0,1,1]
	v_pk_fma_f32 v[8:9], v[234:235], v[152:153], v[8:9] op_sel:[1,0,0] op_sel_hi:[1,1,1]
	v_pk_fma_f32 v[10:11], v[234:235], v[154:155], v[10:11] op_sel:[1,0,0] op_sel_hi:[1,1,1]
	v_pk_fma_f32 v[12:13], v[234:235], v[156:157], v[12:13] op_sel:[1,0,0] op_sel_hi:[1,1,1]
	v_pk_fma_f32 v[14:15], v[234:235], v[158:159], v[14:15] op_sel:[1,0,0] op_sel_hi:[1,1,1]
	v_pk_fma_f32 v[8:9], v[236:237], v[160:161], v[8:9] op_sel_hi:[0,1,1]
; #define LAS __attribute__((address_space(3)))
; __global__ void __launch_bounds__(NTHR, 2) fwd_kernel(Args args) {
;     ...
;             for (int i = 0; i < 16; ++i) { const int k = 2 * lane + 128 * i; f32x2 rv[8]; unsigned xw[8];
; #pragma unroll
;                 for (int e = 0; e < 8; ++e) rv[e] = *(const LAS f32x2*)(Rg + e * DM + k);
; #pragma unroll
;                 for (int q = 0; q < 8; ++q) xw[q] = *(const unsigned*)(XB + (size_t)(t0 + q) * DM + k);
; #pragma unroll
;                 for (int q = 0; q < 8; ++q) { const float x0 = bflo(xw[q]), x1 = bfhi(xw[q]); ssq[q] += x0 * x0 + x1 * x1;
; #pragma unroll
;                     for (int e = 0; e < 8; ++e) acc[q][e] += x0 * rv[e].x + x1 * rv[e].y; } }
	v_pk_fma_f32 v[10:11], v[236:237], v[162:163], v[10:11] op_sel_hi:[0,1,1]
	v_pk_fma_f32 v[12:13], v[236:237], v[164:165], v[12:13] op_sel_hi:[0,1,1]
	v_pk_fma_f32 v[14:15], v[236:237], v[166:167], v[14:15] op_sel_hi:[0,1,1]
	v_pk_fma_f32 v[8:9], v[236:237], v[168:169], v[8:9] op_sel:[1,0,0] op_sel_hi:[1,1,1]
	v_pk_fma_f32 v[10:11], v[236:237], v[170:171], v[10:11] op_sel:[1,0,0] op_sel_hi:[1,1,1]
	v_pk_fma_f32 v[12:13], v[236:237], v[172:173], v[12:13] op_sel:[1,0,0] op_sel_hi:[1,1,1]
	v_pk_fma_f32 v[14:15], v[236:237], v[174:175], v[14:15] op_sel:[1,0,0] op_sel_hi:[1,1,1]
	v_pk_fma_f32 v[8:9], v[238:239], v[176:177], v[8:9] op_sel_hi:[0,1,1]
	v_pk_fma_f32 v[10:11], v[238:239], v[178:179], v[10:11] op_sel_hi:[0,1,1]
	v_pk_fma_f32 v[12:13], v[238:239], v[180:181], v[12:13] op_sel_hi:[0,1,1]
	v_pk_fma_f32 v[14:15], v[238:239], v[182:183], v[14:15] op_sel_hi:[0,1,1]
	v_pk_fma_f32 v[8:9], v[238:239], v[184:185], v[8:9] op_sel:[1,0,0] op_sel_hi:[1,1,1]
	v_pk_fma_f32 v[10:11], v[238:239], v[186:187], v[10:11] op_sel:[1,0,0] op_sel_hi:[1,1,1]
	v_pk_fma_f32 v[12:13], v[238:239], v[188:189], v[12:13] op_sel:[1,0,0] op_sel_hi:[1,1,1]
	v_pk_fma_f32 v[14:15], v[238:239], v[190:191], v[14:15] op_sel:[1,0,0] op_sel_hi:[1,1,1]
	v_lshlrev_b32_e32 v232, 16, v72
	v_and_b32_e32 v233, s15, v72
	v_lshlrev_b32_e32 v234, 16, v73
	v_and_b32_e32 v235, s15, v73
	v_lshlrev_b32_e32 v236, 16, v74
	v_and_b32_e32 v237, s15, v74
	v_lshlrev_b32_e32 v238, 16, v75
	v_and_b32_e32 v239, s15, v75
	v_pk_fma_f32 v[196:197], v[232:233], v[232:233], v[196:197]
	v_pk_fma_f32 v[196:197], v[234:235], v[234:235], v[196:197]
	v_pk_fma_f32 v[196:197], v[236:237], v[236:237], v[196:197]
	v_pk_fma_f32 v[196:197], v[238:239], v[238:239], v[196:197]
	v_pk_fma_f32 v[16:17], v[232:233], v[128:129], v[16:17] op_sel_hi:[0,1,1]
	v_pk_fma_f32 v[18:19], v[232:233], v[130:131], v[18:19] op_sel_hi:[0,1,1]
	v_pk_fma_f32 v[20:21], v[232:233], v[132:133], v[20:21] op_sel_hi:[0,1,1]
	v_pk_fma_f32 v[22:23], v[232:233], v[134:135], v[22:23] op_sel_hi:[0,1,1]
	v_pk_fma_f32 v[16:17], v[232:233], v[136:137], v[16:17] op_sel:[1,0,0] op_sel_hi:[1,1,1]
	v_pk_fma_f32 v[18:19], v[232:233], v[138:139], v[18:19] op_sel:[1,0,0] op_sel_hi:[1,1,1]
	v_pk_fma_f32 v[20:21], v[232:233], v[140:141], v[20:21] op_sel:[1,0,0] op_sel_hi:[1,1,1]
	v_pk_fma_f32 v[22:23], v[232:233], v[142:143], v[22:23] op_sel:[1,0,0] op_sel_hi:[1,1,1]
	v_pk_fma_f32 v[16:17], v[234:235], v[144:145], v[16:17] op_sel_hi:[0,1,1]
	v_pk_fma_f32 v[18:19], v[234:235], v[146:147], v[18:19] op_sel_hi:[0,1,1]
	v_pk_fma_f32 v[20:21], v[234:235], v[148:149], v[20:21] op_sel_hi:[0,1,1]
	v_pk_fma_f32 v[22:23], v[234:235], v[150:151], v[22:23] op_sel_hi:[0,1,1]
	v_pk_fma_f32 v[16:17], v[234:235], v[152:153], v[16:17] op_sel:[1,0,0] op_sel_hi:[1,1,1]
	v_pk_fma_f32 v[18:19], v[234:235], v[154:155], v[18:19] op_sel:[1,0,0] op_sel_hi:[1,1,1]
	v_pk_fma_f32 v[20:21], v[234:235], v[156:157], v[20:21] op_sel:[1,0,0] op_sel_hi:[1,1,1]
	v_pk_fma_f32 v[22:23], v[234:235], v[158:159], v[22:23] op_sel:[1,0,0] op_sel_hi:[1,1,1]
	v_pk_fma_f32 v[16:17], v[236:237], v[160:161], v[16:17] op_sel_hi:[0,1,1]
	v_pk_fma_f32 v[18:19], v[236:237], v[162:163], v[18:19] op_sel_hi:[0,1,1]
	v_pk_fma_f32 v[20:21], v[236:237], v[164:165], v[20:21] op_sel_hi:[0,1,1]
	v_pk_fma_f32 v[22:23], v[236:237], v[166:167], v[22:23] op_sel_hi:[0,1,1]
	v_pk_fma_f32 v[16:17], v[236:237], v[168:169], v[16:17] op_sel:[1,0,0] op_sel_hi:[1,1,1]
	v_pk_fma_f32 v[18:19], v[236:237], v[170:171], v[18:19] op_sel:[1,0,0] op_sel_hi:[1,1,1]
	v_pk_fma_f32 v[20:21], v[236:237], v[172:173], v[20:21] op_sel:[1,0,0] op_sel_hi:[1,1,1]
	v_pk_fma_f32 v[22:23], v[236:237], v[174:175], v[22:23] op_sel:[1,0,0] op_sel_hi:[1,1,1]
	v_pk_fma_f32 v[16:17], v[238:239], v[176:177], v[16:17] op_sel_hi:[0,1,1]
	v_pk_fma_f32 v[18:19], v[238:239], v[178:179], v[18:19] op_sel_hi:[0,1,1]
	v_pk_fma_f32 v[20:21], v[238:239], v[180:181], v[20:21] op_sel_hi:[0,1,1]
	v_pk_fma_f32 v[22:23], v[238:239], v[182:183], v[22:23] op_sel_hi:[0,1,1]
	v_pk_fma_f32 v[16:17], v[238:239], v[184:185], v[16:17] op_sel:[1,0,0] op_sel_hi:[1,1,1]
	v_pk_fma_f32 v[18:19], v[238:239], v[186:187], v[18:19] op_sel:[1,0,0] op_sel_hi:[1,1,1]
	v_pk_fma_f32 v[20:21], v[238:239], v[188:189], v[20:21] op_sel:[1,0,0] op_sel_hi:[1,1,1]
	v_pk_fma_f32 v[22:23], v[238:239], v[190:191], v[22:23] op_sel:[1,0,0] op_sel_hi:[1,1,1]
	v_lshlrev_b32_e32 v232, 16, v76
	v_and_b32_e32 v233, s15, v76
	v_lshlrev_b32_e32 v234, 16, v77
	v_and_b32_e32 v235, s15, v77
	v_lshlrev_b32_e32 v236, 16, v78
	v_and_b32_e32 v237, s15, v78
	v_lshlrev_b32_e32 v238, 16, v79
	v_and_b32_e32 v239, s15, v79
	v_pk_fma_f32 v[198:199], v[232:233], v[232:233], v[198:199]
	v_pk_fma_f32 v[198:199], v[234:235], v[234:235], v[198:199]
	v_pk_fma_f32 v[198:199], v[236:237], v[236:237], v[198:199]
	v_pk_fma_f32 v[198:199], v[238:239], v[238:239], v[198:199]
	v_pk_fma_f32 v[24:25], v[232:233], v[128:129], v[24:25] op_sel_hi:[0,1,1]
	v_pk_fma_f32 v[26:27], v[232:233], v[130:131], v[26:27] op_sel_hi:[0,1,1]
	v_pk_fma_f32 v[28:29], v[232:233], v[132:133], v[28:29] op_sel_hi:[0,1,1]
	v_pk_fma_f32 v[30:31], v[232:233], v[134:135], v[30:31] op_sel_hi:[0,1,1]
	v_pk_fma_f32 v[24:25], v[232:233], v[136:137], v[24:25] op_sel:[1,0,0] op_sel_hi:[1,1,1]
	v_pk_fma_f32 v[26:27], v[232:233], v[138:139], v[26:27] op_sel:[1,0,0] op_sel_hi:[1,1,1]
	v_pk_fma_f32 v[28:29], v[232:233], v[140:141], v[28:29] op_sel:[1,0,0] op_sel_hi:[1,1,1]
	v_pk_fma_f32 v[30:31], v[232:233], v[142:143], v[30:31] op_sel:[1,0,0] op_sel_hi:[1,1,1]
	v_pk_fma_f32 v[24:25], v[234:235], v[144:145], v[24:25] op_sel_hi:[0,1,1]
	v_pk_fma_f32 v[26:27], v[234:235], v[146:147], v[26:27] op_sel_hi:[0,1,1]
; #define LAS __attribute__((address_space(3)))
; __global__ void __launch_bounds__(NTHR, 2) fwd_kernel(Args args) {
;     ...
;             for (int i = 0; i < 16; ++i) { const int k = 2 * lane + 128 * i; f32x2 rv[8]; unsigned xw[8];
; #pragma unroll
;                 for (int e = 0; e < 8; ++e) rv[e] = *(const LAS f32x2*)(Rg + e * DM + k);
; #pragma unroll
;                 for (int q = 0; q < 8; ++q) xw[q] = *(const unsigned*)(XB + (size_t)(t0 + q) * DM + k);
; #pragma unroll
;                 for (int q = 0; q < 8; ++q) { const float x0 = bflo(xw[q]), x1 = bfhi(xw[q]); ssq[q] += x0 * x0 + x1 * x1;
; #pragma unroll
;                     for (int e = 0; e < 8; ++e) acc[q][e] += x0 * rv[e].x + x1 * rv[e].y; } }
	v_pk_fma_f32 v[28:29], v[234:235], v[148:149], v[28:29] op_sel_hi:[0,1,1]
	v_pk_fma_f32 v[30:31], v[234:235], v[150:151], v[30:31] op_sel_hi:[0,1,1]
	v_pk_fma_f32 v[24:25], v[234:235], v[152:153], v[24:25] op_sel:[1,0,0] op_sel_hi:[1,1,1]
	v_pk_fma_f32 v[26:27], v[234:235], v[154:155], v[26:27] op_sel:[1,0,0] op_sel_hi:[1,1,1]
	v_pk_fma_f32 v[28:29], v[234:235], v[156:157], v[28:29] op_sel:[1,0,0] op_sel_hi:[1,1,1]
	v_pk_fma_f32 v[30:31], v[234:235], v[158:159], v[30:31] op_sel:[1,0,0] op_sel_hi:[1,1,1]
	v_pk_fma_f32 v[24:25], v[236:237], v[160:161], v[24:25] op_sel_hi:[0,1,1]
	v_pk_fma_f32 v[26:27], v[236:237], v[162:163], v[26:27] op_sel_hi:[0,1,1]
	v_pk_fma_f32 v[28:29], v[236:237], v[164:165], v[28:29] op_sel_hi:[0,1,1]
	v_pk_fma_f32 v[30:31], v[236:237], v[166:167], v[30:31] op_sel_hi:[0,1,1]
	v_pk_fma_f32 v[24:25], v[236:237], v[168:169], v[24:25] op_sel:[1,0,0] op_sel_hi:[1,1,1]
	v_pk_fma_f32 v[26:27], v[236:237], v[170:171], v[26:27] op_sel:[1,0,0] op_sel_hi:[1,1,1]
	v_pk_fma_f32 v[28:29], v[236:237], v[172:173], v[28:29] op_sel:[1,0,0] op_sel_hi:[1,1,1]
	v_pk_fma_f32 v[30:31], v[236:237], v[174:175], v[30:31] op_sel:[1,0,0] op_sel_hi:[1,1,1]
	v_pk_fma_f32 v[24:25], v[238:239], v[176:177], v[24:25] op_sel_hi:[0,1,1]
	v_pk_fma_f32 v[26:27], v[238:239], v[178:179], v[26:27] op_sel_hi:[0,1,1]
	v_pk_fma_f32 v[28:29], v[238:239], v[180:181], v[28:29] op_sel_hi:[0,1,1]
	v_pk_fma_f32 v[30:31], v[238:239], v[182:183], v[30:31] op_sel_hi:[0,1,1]
	v_pk_fma_f32 v[24:25], v[238:239], v[184:185], v[24:25] op_sel:[1,0,0] op_sel_hi:[1,1,1]
	v_pk_fma_f32 v[26:27], v[238:239], v[186:187], v[26:27] op_sel:[1,0,0] op_sel_hi:[1,1,1]
	v_pk_fma_f32 v[28:29], v[238:239], v[188:189], v[28:29] op_sel:[1,0,0] op_sel_hi:[1,1,1]
	v_pk_fma_f32 v[30:31], v[238:239], v[190:191], v[30:31] op_sel:[1,0,0] op_sel_hi:[1,1,1]
	v_lshlrev_b32_e32 v232, 16, v80
	v_and_b32_e32 v233, s15, v80
	v_lshlrev_b32_e32 v234, 16, v81
	v_and_b32_e32 v235, s15, v81
	v_lshlrev_b32_e32 v236, 16, v82
	v_and_b32_e32 v237, s15, v82
	v_lshlrev_b32_e32 v238, 16, v83
	v_and_b32_e32 v239, s15, v83
	v_pk_fma_f32 v[200:201], v[232:233], v[232:233], v[200:201]
	v_pk_fma_f32 v[200:201], v[234:235], v[234:235], v[200:201]
	v_pk_fma_f32 v[200:201], v[236:237], v[236:237], v[200:201]
	v_pk_fma_f32 v[200:201], v[238:239], v[238:239], v[200:201]
	v_pk_fma_f32 v[32:33], v[232:233], v[128:129], v[32:33] op_sel_hi:[0,1,1]
	v_pk_fma_f32 v[34:35], v[232:233], v[130:131], v[34:35] op_sel_hi:[0,1,1]
	v_pk_fma_f32 v[36:37], v[232:233], v[132:133], v[36:37] op_sel_hi:[0,1,1]
	v_pk_fma_f32 v[38:39], v[232:233], v[134:135], v[38:39] op_sel_hi:[0,1,1]
	v_pk_fma_f32 v[32:33], v[232:233], v[136:137], v[32:33] op_sel:[1,0,0] op_sel_hi:[1,1,1]
	v_pk_fma_f32 v[34:35], v[232:233], v[138:139], v[34:35] op_sel:[1,0,0] op_sel_hi:[1,1,1]
	v_pk_fma_f32 v[36:37], v[232:233], v[140:141], v[36:37] op_sel:[1,0,0] op_sel_hi:[1,1,1]
	v_pk_fma_f32 v[38:39], v[232:233], v[142:143], v[38:39] op_sel:[1,0,0] op_sel_hi:[1,1,1]
	v_pk_fma_f32 v[32:33], v[234:235], v[144:145], v[32:33] op_sel_hi:[0,1,1]
	v_pk_fma_f32 v[34:35], v[234:235], v[146:147], v[34:35] op_sel_hi:[0,1,1]
	v_pk_fma_f32 v[36:37], v[234:235], v[148:149], v[36:37] op_sel_hi:[0,1,1]
	v_pk_fma_f32 v[38:39], v[234:235], v[150:151], v[38:39] op_sel_hi:[0,1,1]
	v_pk_fma_f32 v[32:33], v[234:235], v[152:153], v[32:33] op_sel:[1,0,0] op_sel_hi:[1,1,1]
	v_pk_fma_f32 v[34:35], v[234:235], v[154:155], v[34:35] op_sel:[1,0,0] op_sel_hi:[1,1,1]
	v_pk_fma_f32 v[36:37], v[234:235], v[156:157], v[36:37] op_sel:[1,0,0] op_sel_hi:[1,1,1]
	v_pk_fma_f32 v[38:39], v[234:235], v[158:159], v[38:39] op_sel:[1,0,0] op_sel_hi:[1,1,1]
	v_pk_fma_f32 v[32:33], v[236:237], v[160:161], v[32:33] op_sel_hi:[0,1,1]
	v_pk_fma_f32 v[34:35], v[236:237], v[162:163], v[34:35] op_sel_hi:[0,1,1]
	v_pk_fma_f32 v[36:37], v[236:237], v[164:165], v[36:37] op_sel_hi:[0,1,1]
	v_pk_fma_f32 v[38:39], v[236:237], v[166:167], v[38:39] op_sel_hi:[0,1,1]
	v_pk_fma_f32 v[32:33], v[236:237], v[168:169], v[32:33] op_sel:[1,0,0] op_sel_hi:[1,1,1]
	v_pk_fma_f32 v[34:35], v[236:237], v[170:171], v[34:35] op_sel:[1,0,0] op_sel_hi:[1,1,1]
	v_pk_fma_f32 v[36:37], v[236:237], v[172:173], v[36:37] op_sel:[1,0,0] op_sel_hi:[1,1,1]
	v_pk_fma_f32 v[38:39], v[236:237], v[174:175], v[38:39] op_sel:[1,0,0] op_sel_hi:[1,1,1]
	v_pk_fma_f32 v[32:33], v[238:239], v[176:177], v[32:33] op_sel_hi:[0,1,1]
	v_pk_fma_f32 v[34:35], v[238:239], v[178:179], v[34:35] op_sel_hi:[0,1,1]
	v_pk_fma_f32 v[36:37], v[238:239], v[180:181], v[36:37] op_sel_hi:[0,1,1]
	v_pk_fma_f32 v[38:39], v[238:239], v[182:183], v[38:39] op_sel_hi:[0,1,1]
	v_pk_fma_f32 v[32:33], v[238:239], v[184:185], v[32:33] op_sel:[1,0,0] op_sel_hi:[1,1,1]
	v_pk_fma_f32 v[34:35], v[238:239], v[186:187], v[34:35] op_sel:[1,0,0] op_sel_hi:[1,1,1]
	v_pk_fma_f32 v[36:37], v[238:239], v[188:189], v[36:37] op_sel:[1,0,0] op_sel_hi:[1,1,1]
	v_pk_fma_f32 v[38:39], v[238:239], v[190:191], v[38:39] op_sel:[1,0,0] op_sel_hi:[1,1,1]
	v_lshlrev_b32_e32 v232, 16, v84
	v_and_b32_e32 v233, s15, v84
	v_lshlrev_b32_e32 v234, 16, v85
	v_and_b32_e32 v235, s15, v85
	v_lshlrev_b32_e32 v236, 16, v86
	v_and_b32_e32 v237, s15, v86
	v_lshlrev_b32_e32 v238, 16, v87
	v_and_b32_e32 v239, s15, v87
	v_pk_fma_f32 v[202:203], v[232:233], v[232:233], v[202:203]
	v_pk_fma_f32 v[202:203], v[234:235], v[234:235], v[202:203]
	v_pk_fma_f32 v[202:203], v[236:237], v[236:237], v[202:203]
	v_pk_fma_f32 v[202:203], v[238:239], v[238:239], v[202:203]
	v_pk_fma_f32 v[40:41], v[232:233], v[128:129], v[40:41] op_sel_hi:[0,1,1]
	v_pk_fma_f32 v[42:43], v[232:233], v[130:131], v[42:43] op_sel_hi:[0,1,1]
; #define LAS __attribute__((address_space(3)))
; __global__ void __launch_bounds__(NTHR, 2) fwd_kernel(Args args) {
;     ...
;             for (int i = 0; i < 16; ++i) { const int k = 2 * lane + 128 * i; f32x2 rv[8]; unsigned xw[8];
; #pragma unroll
;                 for (int e = 0; e < 8; ++e) rv[e] = *(const LAS f32x2*)(Rg + e * DM + k);
; #pragma unroll
;                 for (int q = 0; q < 8; ++q) xw[q] = *(const unsigned*)(XB + (size_t)(t0 + q) * DM + k);
; #pragma unroll
;                 for (int q = 0; q < 8; ++q) { const float x0 = bflo(xw[q]), x1 = bfhi(xw[q]); ssq[q] += x0 * x0 + x1 * x1;
; #pragma unroll
;                     for (int e = 0; e < 8; ++e) acc[q][e] += x0 * rv[e].x + x1 * rv[e].y; } }
	v_pk_fma_f32 v[44:45], v[232:233], v[132:133], v[44:45] op_sel_hi:[0,1,1]
	v_pk_fma_f32 v[46:47], v[232:233], v[134:135], v[46:47] op_sel_hi:[0,1,1]
	v_pk_fma_f32 v[40:41], v[232:233], v[136:137], v[40:41] op_sel:[1,0,0] op_sel_hi:[1,1,1]
	v_pk_fma_f32 v[42:43], v[232:233], v[138:139], v[42:43] op_sel:[1,0,0] op_sel_hi:[1,1,1]
	v_pk_fma_f32 v[44:45], v[232:233], v[140:141], v[44:45] op_sel:[1,0,0] op_sel_hi:[1,1,1]
	v_pk_fma_f32 v[46:47], v[232:233], v[142:143], v[46:47] op_sel:[1,0,0] op_sel_hi:[1,1,1]
	v_pk_fma_f32 v[40:41], v[234:235], v[144:145], v[40:41] op_sel_hi:[0,1,1]
	v_pk_fma_f32 v[42:43], v[234:235], v[146:147], v[42:43] op_sel_hi:[0,1,1]
	v_pk_fma_f32 v[44:45], v[234:235], v[148:149], v[44:45] op_sel_hi:[0,1,1]
	v_pk_fma_f32 v[46:47], v[234:235], v[150:151], v[46:47] op_sel_hi:[0,1,1]
	v_pk_fma_f32 v[40:41], v[234:235], v[152:153], v[40:41] op_sel:[1,0,0] op_sel_hi:[1,1,1]
	v_pk_fma_f32 v[42:43], v[234:235], v[154:155], v[42:43] op_sel:[1,0,0] op_sel_hi:[1,1,1]
	v_pk_fma_f32 v[44:45], v[234:235], v[156:157], v[44:45] op_sel:[1,0,0] op_sel_hi:[1,1,1]
	v_pk_fma_f32 v[46:47], v[234:235], v[158:159], v[46:47] op_sel:[1,0,0] op_sel_hi:[1,1,1]
	v_pk_fma_f32 v[40:41], v[236:237], v[160:161], v[40:41] op_sel_hi:[0,1,1]
	v_pk_fma_f32 v[42:43], v[236:237], v[162:163], v[42:43] op_sel_hi:[0,1,1]
	v_pk_fma_f32 v[44:45], v[236:237], v[164:165], v[44:45] op_sel_hi:[0,1,1]
	v_pk_fma_f32 v[46:47], v[236:237], v[166:167], v[46:47] op_sel_hi:[0,1,1]
	v_pk_fma_f32 v[40:41], v[236:237], v[168:169], v[40:41] op_sel:[1,0,0] op_sel_hi:[1,1,1]
	v_pk_fma_f32 v[42:43], v[236:237], v[170:171], v[42:43] op_sel:[1,0,0] op_sel_hi:[1,1,1]
	v_pk_fma_f32 v[44:45], v[236:237], v[172:173], v[44:45] op_sel:[1,0,0] op_sel_hi:[1,1,1]
	v_pk_fma_f32 v[46:47], v[236:237], v[174:175], v[46:47] op_sel:[1,0,0] op_sel_hi:[1,1,1]
	v_pk_fma_f32 v[40:41], v[238:239], v[176:177], v[40:41] op_sel_hi:[0,1,1]
	v_pk_fma_f32 v[42:43], v[238:239], v[178:179], v[42:43] op_sel_hi:[0,1,1]
	v_pk_fma_f32 v[44:45], v[238:239], v[180:181], v[44:45] op_sel_hi:[0,1,1]
	v_pk_fma_f32 v[46:47], v[238:239], v[182:183], v[46:47] op_sel_hi:[0,1,1]
	v_pk_fma_f32 v[40:41], v[238:239], v[184:185], v[40:41] op_sel:[1,0,0] op_sel_hi:[1,1,1]
	v_pk_fma_f32 v[42:43], v[238:239], v[186:187], v[42:43] op_sel:[1,0,0] op_sel_hi:[1,1,1]
	v_pk_fma_f32 v[44:45], v[238:239], v[188:189], v[44:45] op_sel:[1,0,0] op_sel_hi:[1,1,1]
	v_pk_fma_f32 v[46:47], v[238:239], v[190:191], v[46:47] op_sel:[1,0,0] op_sel_hi:[1,1,1]
	v_lshlrev_b32_e32 v232, 16, v88
	v_and_b32_e32 v233, s15, v88
	v_lshlrev_b32_e32 v234, 16, v89
	v_and_b32_e32 v235, s15, v89
	v_lshlrev_b32_e32 v236, 16, v90
	v_and_b32_e32 v237, s15, v90
	v_lshlrev_b32_e32 v238, 16, v91
	v_and_b32_e32 v239, s15, v91
	v_pk_fma_f32 v[204:205], v[232:233], v[232:233], v[204:205]
	v_pk_fma_f32 v[204:205], v[234:235], v[234:235], v[204:205]
	v_pk_fma_f32 v[204:205], v[236:237], v[236:237], v[204:205]
	v_pk_fma_f32 v[204:205], v[238:239], v[238:239], v[204:205]
	v_pk_fma_f32 v[48:49], v[232:233], v[128:129], v[48:49] op_sel_hi:[0,1,1]
	v_pk_fma_f32 v[50:51], v[232:233], v[130:131], v[50:51] op_sel_hi:[0,1,1]
	v_pk_fma_f32 v[52:53], v[232:233], v[132:133], v[52:53] op_sel_hi:[0,1,1]
	v_pk_fma_f32 v[54:55], v[232:233], v[134:135], v[54:55] op_sel_hi:[0,1,1]
	v_pk_fma_f32 v[48:49], v[232:233], v[136:137], v[48:49] op_sel:[1,0,0] op_sel_hi:[1,1,1]
	v_pk_fma_f32 v[50:51], v[232:233], v[138:139], v[50:51] op_sel:[1,0,0] op_sel_hi:[1,1,1]
	v_pk_fma_f32 v[52:53], v[232:233], v[140:141], v[52:53] op_sel:[1,0,0] op_sel_hi:[1,1,1]
	v_pk_fma_f32 v[54:55], v[232:233], v[142:143], v[54:55] op_sel:[1,0,0] op_sel_hi:[1,1,1]
	v_pk_fma_f32 v[48:49], v[234:235], v[144:145], v[48:49] op_sel_hi:[0,1,1]
	v_pk_fma_f32 v[50:51], v[234:235], v[146:147], v[50:51] op_sel_hi:[0,1,1]
	v_pk_fma_f32 v[52:53], v[234:235], v[148:149], v[52:53] op_sel_hi:[0,1,1]
	v_pk_fma_f32 v[54:55], v[234:235], v[150:151], v[54:55] op_sel_hi:[0,1,1]
	v_pk_fma_f32 v[48:49], v[234:235], v[152:153], v[48:49] op_sel:[1,0,0] op_sel_hi:[1,1,1]
	v_pk_fma_f32 v[50:51], v[234:235], v[154:155], v[50:51] op_sel:[1,0,0] op_sel_hi:[1,1,1]
	v_pk_fma_f32 v[52:53], v[234:235], v[156:157], v[52:53] op_sel:[1,0,0] op_sel_hi:[1,1,1]
	v_pk_fma_f32 v[54:55], v[234:235], v[158:159], v[54:55] op_sel:[1,0,0] op_sel_hi:[1,1,1]
	v_pk_fma_f32 v[48:49], v[236:237], v[160:161], v[48:49] op_sel_hi:[0,1,1]
	v_pk_fma_f32 v[50:51], v[236:237], v[162:163], v[50:51] op_sel_hi:[0,1,1]
	v_pk_fma_f32 v[52:53], v[236:237], v[164:165], v[52:53] op_sel_hi:[0,1,1]
	v_pk_fma_f32 v[54:55], v[236:237], v[166:167], v[54:55] op_sel_hi:[0,1,1]
	v_pk_fma_f32 v[48:49], v[236:237], v[168:169], v[48:49] op_sel:[1,0,0] op_sel_hi:[1,1,1]
	v_pk_fma_f32 v[50:51], v[236:237], v[170:171], v[50:51] op_sel:[1,0,0] op_sel_hi:[1,1,1]
	v_pk_fma_f32 v[52:53], v[236:237], v[172:173], v[52:53] op_sel:[1,0,0] op_sel_hi:[1,1,1]
	v_pk_fma_f32 v[54:55], v[236:237], v[174:175], v[54:55] op_sel:[1,0,0] op_sel_hi:[1,1,1]
	v_pk_fma_f32 v[48:49], v[238:239], v[176:177], v[48:49] op_sel_hi:[0,1,1]
	v_pk_fma_f32 v[50:51], v[238:239], v[178:179], v[50:51] op_sel_hi:[0,1,1]
	v_pk_fma_f32 v[52:53], v[238:239], v[180:181], v[52:53] op_sel_hi:[0,1,1]
	v_pk_fma_f32 v[54:55], v[238:239], v[182:183], v[54:55] op_sel_hi:[0,1,1]
	v_pk_fma_f32 v[48:49], v[238:239], v[184:185], v[48:49] op_sel:[1,0,0] op_sel_hi:[1,1,1]
	v_pk_fma_f32 v[50:51], v[238:239], v[186:187], v[50:51] op_sel:[1,0,0] op_sel_hi:[1,1,1]
	v_pk_fma_f32 v[52:53], v[238:239], v[188:189], v[52:53] op_sel:[1,0,0] op_sel_hi:[1,1,1]
	v_pk_fma_f32 v[54:55], v[238:239], v[190:191], v[54:55] op_sel:[1,0,0] op_sel_hi:[1,1,1]
; #define LAS __attribute__((address_space(3)))
; __global__ void __launch_bounds__(NTHR, 2) fwd_kernel(Args args) {
;     ...
;             for (int i = 0; i < 16; ++i) { const int k = 2 * lane + 128 * i; f32x2 rv[8]; unsigned xw[8];
; #pragma unroll
;                 for (int e = 0; e < 8; ++e) rv[e] = *(const LAS f32x2*)(Rg + e * DM + k);
; #pragma unroll
;                 for (int q = 0; q < 8; ++q) xw[q] = *(const unsigned*)(XB + (size_t)(t0 + q) * DM + k);
; #pragma unroll
;                 for (int q = 0; q < 8; ++q) { const float x0 = bflo(xw[q]), x1 = bfhi(xw[q]); ssq[q] += x0 * x0 + x1 * x1;
; #pragma unroll
;                     for (int e = 0; e < 8; ++e) acc[q][e] += x0 * rv[e].x + x1 * rv[e].y; } }
	v_lshlrev_b32_e32 v232, 16, v92
	v_and_b32_e32 v233, s15, v92
	v_lshlrev_b32_e32 v234, 16, v93
	v_and_b32_e32 v235, s15, v93
	v_lshlrev_b32_e32 v236, 16, v94
	v_and_b32_e32 v237, s15, v94
	v_lshlrev_b32_e32 v238, 16, v95
	v_and_b32_e32 v239, s15, v95
	v_pk_fma_f32 v[206:207], v[232:233], v[232:233], v[206:207]
	v_pk_fma_f32 v[206:207], v[234:235], v[234:235], v[206:207]
	v_pk_fma_f32 v[206:207], v[236:237], v[236:237], v[206:207]
	v_pk_fma_f32 v[206:207], v[238:239], v[238:239], v[206:207]
	v_pk_fma_f32 v[56:57], v[232:233], v[128:129], v[56:57] op_sel_hi:[0,1,1]
	v_pk_fma_f32 v[58:59], v[232:233], v[130:131], v[58:59] op_sel_hi:[0,1,1]
	v_pk_fma_f32 v[60:61], v[232:233], v[132:133], v[60:61] op_sel_hi:[0,1,1]
	v_pk_fma_f32 v[62:63], v[232:233], v[134:135], v[62:63] op_sel_hi:[0,1,1]
	v_pk_fma_f32 v[56:57], v[232:233], v[136:137], v[56:57] op_sel:[1,0,0] op_sel_hi:[1,1,1]
	v_pk_fma_f32 v[58:59], v[232:233], v[138:139], v[58:59] op_sel:[1,0,0] op_sel_hi:[1,1,1]
	v_pk_fma_f32 v[60:61], v[232:233], v[140:141], v[60:61] op_sel:[1,0,0] op_sel_hi:[1,1,1]
	v_pk_fma_f32 v[62:63], v[232:233], v[142:143], v[62:63] op_sel:[1,0,0] op_sel_hi:[1,1,1]
	v_pk_fma_f32 v[56:57], v[234:235], v[144:145], v[56:57] op_sel_hi:[0,1,1]
	v_pk_fma_f32 v[58:59], v[234:235], v[146:147], v[58:59] op_sel_hi:[0,1,1]
	v_pk_fma_f32 v[60:61], v[234:235], v[148:149], v[60:61] op_sel_hi:[0,1,1]
	v_pk_fma_f32 v[62:63], v[234:235], v[150:151], v[62:63] op_sel_hi:[0,1,1]
	v_pk_fma_f32 v[56:57], v[234:235], v[152:153], v[56:57] op_sel:[1,0,0] op_sel_hi:[1,1,1]
	v_pk_fma_f32 v[58:59], v[234:235], v[154:155], v[58:59] op_sel:[1,0,0] op_sel_hi:[1,1,1]
	v_pk_fma_f32 v[60:61], v[234:235], v[156:157], v[60:61] op_sel:[1,0,0] op_sel_hi:[1,1,1]
	v_pk_fma_f32 v[62:63], v[234:235], v[158:159], v[62:63] op_sel:[1,0,0] op_sel_hi:[1,1,1]
	v_pk_fma_f32 v[56:57], v[236:237], v[160:161], v[56:57] op_sel_hi:[0,1,1]
	v_pk_fma_f32 v[58:59], v[236:237], v[162:163], v[58:59] op_sel_hi:[0,1,1]
	v_pk_fma_f32 v[60:61], v[236:237], v[164:165], v[60:61] op_sel_hi:[0,1,1]
	v_pk_fma_f32 v[62:63], v[236:237], v[166:167], v[62:63] op_sel_hi:[0,1,1]
	v_pk_fma_f32 v[56:57], v[236:237], v[168:169], v[56:57] op_sel:[1,0,0] op_sel_hi:[1,1,1]
	v_pk_fma_f32 v[58:59], v[236:237], v[170:171], v[58:59] op_sel:[1,0,0] op_sel_hi:[1,1,1]
	v_pk_fma_f32 v[60:61], v[236:237], v[172:173], v[60:61] op_sel:[1,0,0] op_sel_hi:[1,1,1]
	v_pk_fma_f32 v[62:63], v[236:237], v[174:175], v[62:63] op_sel:[1,0,0] op_sel_hi:[1,1,1]
	v_pk_fma_f32 v[56:57], v[238:239], v[176:177], v[56:57] op_sel_hi:[0,1,1]
	v_pk_fma_f32 v[58:59], v[238:239], v[178:179], v[58:59] op_sel_hi:[0,1,1]
	v_pk_fma_f32 v[60:61], v[238:239], v[180:181], v[60:61] op_sel_hi:[0,1,1]
	v_pk_fma_f32 v[62:63], v[238:239], v[182:183], v[62:63] op_sel_hi:[0,1,1]
	v_pk_fma_f32 v[56:57], v[238:239], v[184:185], v[56:57] op_sel:[1,0,0] op_sel_hi:[1,1,1]
	v_pk_fma_f32 v[58:59], v[238:239], v[186:187], v[58:59] op_sel:[1,0,0] op_sel_hi:[1,1,1]
	v_pk_fma_f32 v[60:61], v[238:239], v[188:189], v[60:61] op_sel:[1,0,0] op_sel_hi:[1,1,1]
	v_pk_fma_f32 v[62:63], v[238:239], v[190:191], v[62:63] op_sel:[1,0,0] op_sel_hi:[1,1,1]
	global_load_dwordx4 v[64:67], v208, s[40:41] offset:2048
	global_load_dwordx4 v[68:71], v208, s[42:43] offset:2048
	global_load_dwordx4 v[72:75], v208, s[44:45] offset:2048
	global_load_dwordx4 v[76:79], v208, s[46:47] offset:2048
	global_load_dwordx4 v[80:83], v208, s[48:49] offset:2048
	global_load_dwordx4 v[84:87], v208, s[50:51] offset:2048
	global_load_dwordx4 v[88:91], v208, s[52:53] offset:2048
	global_load_dwordx4 v[92:95], v208, s[54:55] offset:2048
	ds_read_b128 v[128:131], v208 offset:16384
	ds_read_b128 v[132:135], v208 offset:17408
	ds_read_b128 v[136:139], v208 offset:18432
	ds_read_b128 v[140:143], v208 offset:19456
	ds_read_b128 v[144:147], v208 offset:20480
	ds_read_b128 v[148:151], v208 offset:21504
	ds_read_b128 v[152:155], v208 offset:22528
	ds_read_b128 v[156:159], v208 offset:23552
	ds_read_b128 v[160:163], v208 offset:24576
	ds_read_b128 v[164:167], v208 offset:25600
	ds_read_b128 v[168:171], v208 offset:26624
	ds_read_b128 v[172:175], v208 offset:27648
	ds_read_b128 v[176:179], v208 offset:28672
	ds_read_b128 v[180:183], v208 offset:29696
	ds_read_b128 v[184:187], v208 offset:30720
	ds_read_b128 v[188:191], v208 offset:31744
	s_waitcnt vmcnt(8)
	s_waitcnt lgkmcnt(0)
; #define LAS __attribute__((address_space(3)))
; __global__ void __launch_bounds__(NTHR, 2) fwd_kernel(Args args) {
;     ...
;             for (int i = 0; i < 16; ++i) { const int k = 2 * lane + 128 * i; f32x2 rv[8]; unsigned xw[8];
; #pragma unroll
;                 for (int e = 0; e < 8; ++e) rv[e] = *(const LAS f32x2*)(Rg + e * DM + k);
; #pragma unroll
;                 for (int q = 0; q < 8; ++q) xw[q] = *(const unsigned*)(XB + (size_t)(t0 + q) * DM + k);
; #pragma unroll
;                 for (int q = 0; q < 8; ++q) { const float x0 = bflo(xw[q]), x1 = bfhi(xw[q]); ssq[q] += x0 * x0 + x1 * x1;
; #pragma unroll
;                     for (int e = 0; e < 8; ++e) acc[q][e] += x0 * rv[e].x + x1 * rv[e].y; } }
	v_lshlrev_b32_e32 v232, 16, v96
	v_and_b32_e32 v233, s15, v96
	v_lshlrev_b32_e32 v234, 16, v97
	v_and_b32_e32 v235, s15, v97
	v_lshlrev_b32_e32 v236, 16, v98
	v_and_b32_e32 v237, s15, v98
	v_lshlrev_b32_e32 v238, 16, v99
	v_and_b32_e32 v239, s15, v99
	v_pk_fma_f32 v[192:193], v[232:233], v[232:233], v[192:193]
	v_pk_fma_f32 v[192:193], v[234:235], v[234:235], v[192:193]
	v_pk_fma_f32 v[192:193], v[236:237], v[236:237], v[192:193]
	v_pk_fma_f32 v[192:193], v[238:239], v[238:239], v[192:193]
	v_pk_fma_f32 v[0:1], v[232:233], v[128:129], v[0:1] op_sel_hi:[0,1,1]
	v_pk_fma_f32 v[2:3], v[232:233], v[130:131], v[2:3] op_sel_hi:[0,1,1]
	v_pk_fma_f32 v[4:5], v[232:233], v[132:133], v[4:5] op_sel_hi:[0,1,1]
	v_pk_fma_f32 v[6:7], v[232:233], v[134:135], v[6:7] op_sel_hi:[0,1,1]
	v_pk_fma_f32 v[0:1], v[232:233], v[136:137], v[0:1] op_sel:[1,0,0] op_sel_hi:[1,1,1]
	v_pk_fma_f32 v[2:3], v[232:233], v[138:139], v[2:3] op_sel:[1,0,0] op_sel_hi:[1,1,1]
	v_pk_fma_f32 v[4:5], v[232:233], v[140:141], v[4:5] op_sel:[1,0,0] op_sel_hi:[1,1,1]
	v_pk_fma_f32 v[6:7], v[232:233], v[142:143], v[6:7] op_sel:[1,0,0] op_sel_hi:[1,1,1]
	v_pk_fma_f32 v[0:1], v[234:235], v[144:145], v[0:1] op_sel_hi:[0,1,1]
	v_pk_fma_f32 v[2:3], v[234:235], v[146:147], v[2:3] op_sel_hi:[0,1,1]
	v_pk_fma_f32 v[4:5], v[234:235], v[148:149], v[4:5] op_sel_hi:[0,1,1]
	v_pk_fma_f32 v[6:7], v[234:235], v[150:151], v[6:7] op_sel_hi:[0,1,1]
	v_pk_fma_f32 v[0:1], v[234:235], v[152:153], v[0:1] op_sel:[1,0,0] op_sel_hi:[1,1,1]
	v_pk_fma_f32 v[2:3], v[234:235], v[154:155], v[2:3] op_sel:[1,0,0] op_sel_hi:[1,1,1]
	v_pk_fma_f32 v[4:5], v[234:235], v[156:157], v[4:5] op_sel:[1,0,0] op_sel_hi:[1,1,1]
	v_pk_fma_f32 v[6:7], v[234:235], v[158:159], v[6:7] op_sel:[1,0,0] op_sel_hi:[1,1,1]
	v_pk_fma_f32 v[0:1], v[236:237], v[160:161], v[0:1] op_sel_hi:[0,1,1]
	v_pk_fma_f32 v[2:3], v[236:237], v[162:163], v[2:3] op_sel_hi:[0,1,1]
	v_pk_fma_f32 v[4:5], v[236:237], v[164:165], v[4:5] op_sel_hi:[0,1,1]
	v_pk_fma_f32 v[6:7], v[236:237], v[166:167], v[6:7] op_sel_hi:[0,1,1]
	v_pk_fma_f32 v[0:1], v[236:237], v[168:169], v[0:1] op_sel:[1,0,0] op_sel_hi:[1,1,1]
	v_pk_fma_f32 v[2:3], v[236:237], v[170:171], v[2:3] op_sel:[1,0,0] op_sel_hi:[1,1,1]
	v_pk_fma_f32 v[4:5], v[236:237], v[172:173], v[4:5] op_sel:[1,0,0] op_sel_hi:[1,1,1]
	v_pk_fma_f32 v[6:7], v[236:237], v[174:175], v[6:7] op_sel:[1,0,0] op_sel_hi:[1,1,1]
	v_pk_fma_f32 v[0:1], v[238:239], v[176:177], v[0:1] op_sel_hi:[0,1,1]
	v_pk_fma_f32 v[2:3], v[238:239], v[178:179], v[2:3] op_sel_hi:[0,1,1]
	v_pk_fma_f32 v[4:5], v[238:239], v[180:181], v[4:5] op_sel_hi:[0,1,1]
	v_pk_fma_f32 v[6:7], v[238:239], v[182:183], v[6:7] op_sel_hi:[0,1,1]
	v_pk_fma_f32 v[0:1], v[238:239], v[184:185], v[0:1] op_sel:[1,0,0] op_sel_hi:[1,1,1]
	v_pk_fma_f32 v[2:3], v[238:239], v[186:187], v[2:3] op_sel:[1,0,0] op_sel_hi:[1,1,1]
	v_pk_fma_f32 v[4:5], v[238:239], v[188:189], v[4:5] op_sel:[1,0,0] op_sel_hi:[1,1,1]
	v_pk_fma_f32 v[6:7], v[238:239], v[190:191], v[6:7] op_sel:[1,0,0] op_sel_hi:[1,1,1]
	v_lshlrev_b32_e32 v232, 16, v100
	v_and_b32_e32 v233, s15, v100
	v_lshlrev_b32_e32 v234, 16, v101
	v_and_b32_e32 v235, s15, v101
	v_lshlrev_b32_e32 v236, 16, v102
	v_and_b32_e32 v237, s15, v102
	v_lshlrev_b32_e32 v238, 16, v103
	v_and_b32_e32 v239, s15, v103
	v_pk_fma_f32 v[194:195], v[232:233], v[232:233], v[194:195]
	v_pk_fma_f32 v[194:195], v[234:235], v[234:235], v[194:195]
	v_pk_fma_f32 v[194:195], v[236:237], v[236:237], v[194:195]
	v_pk_fma_f32 v[194:195], v[238:239], v[238:239], v[194:195]
	v_pk_fma_f32 v[8:9], v[232:233], v[128:129], v[8:9] op_sel_hi:[0,1,1]
	v_pk_fma_f32 v[10:11], v[232:233], v[130:131], v[10:11] op_sel_hi:[0,1,1]
	v_pk_fma_f32 v[12:13], v[232:233], v[132:133], v[12:13] op_sel_hi:[0,1,1]
	v_pk_fma_f32 v[14:15], v[232:233], v[134:135], v[14:15] op_sel_hi:[0,1,1]
	v_pk_fma_f32 v[8:9], v[232:233], v[136:137], v[8:9] op_sel:[1,0,0] op_sel_hi:[1,1,1]
	v_pk_fma_f32 v[10:11], v[232:233], v[138:139], v[10:11] op_sel:[1,0,0] op_sel_hi:[1,1,1]
	v_pk_fma_f32 v[12:13], v[232:233], v[140:141], v[12:13] op_sel:[1,0,0] op_sel_hi:[1,1,1]
	v_pk_fma_f32 v[14:15], v[232:233], v[142:143], v[14:15] op_sel:[1,0,0] op_sel_hi:[1,1,1]
	v_pk_fma_f32 v[8:9], v[234:235], v[144:145], v[8:9] op_sel_hi:[0,1,1]
	v_pk_fma_f32 v[10:11], v[234:235], v[146:147], v[10:11] op_sel_hi:[0,1,1]
	v_pk_fma_f32 v[12:13], v[234:235], v[148:149], v[12:13] op_sel_hi:[0,1,1]
	v_pk_fma_f32 v[14:15], v[234:235], v[150:151], v[14:15] op_sel_hi:[0,1,1]
	v_pk_fma_f32 v[8:9], v[234:235], v[152:153], v[8:9] op_sel:[1,0,0] op_sel_hi:[1,1,1]
	v_pk_fma_f32 v[10:11], v[234:235], v[154:155], v[10:11] op_sel:[1,0,0] op_sel_hi:[1,1,1]
	v_pk_fma_f32 v[12:13], v[234:235], v[156:157], v[12:13] op_sel:[1,0,0] op_sel_hi:[1,1,1]
	v_pk_fma_f32 v[14:15], v[234:235], v[158:159], v[14:15] op_sel:[1,0,0] op_sel_hi:[1,1,1]
	v_pk_fma_f32 v[8:9], v[236:237], v[160:161], v[8:9] op_sel_hi:[0,1,1]
	v_pk_fma_f32 v[10:11], v[236:237], v[162:163], v[10:11] op_sel_hi:[0,1,1]
	v_pk_fma_f32 v[12:13], v[236:237], v[164:165], v[12:13] op_sel_hi:[0,1,1]
	v_pk_fma_f32 v[14:15], v[236:237], v[166:167], v[14:15] op_sel_hi:[0,1,1]
	v_pk_fma_f32 v[8:9], v[236:237], v[168:169], v[8:9] op_sel:[1,0,0] op_sel_hi:[1,1,1]
	v_pk_fma_f32 v[10:11], v[236:237], v[170:171], v[10:11] op_sel:[1,0,0] op_sel_hi:[1,1,1]
	v_pk_fma_f32 v[12:13], v[236:237], v[172:173], v[12:13] op_sel:[1,0,0] op_sel_hi:[1,1,1]
	v_pk_fma_f32 v[14:15], v[236:237], v[174:175], v[14:15] op_sel:[1,0,0] op_sel_hi:[1,1,1]
	v_pk_fma_f32 v[8:9], v[238:239], v[176:177], v[8:9] op_sel_hi:[0,1,1]
	v_pk_fma_f32 v[10:11], v[238:239], v[178:179], v[10:11] op_sel_hi:[0,1,1]
; #define LAS __attribute__((address_space(3)))
; __global__ void __launch_bounds__(NTHR, 2) fwd_kernel(Args args) {
;     ...
;             for (int i = 0; i < 16; ++i) { const int k = 2 * lane + 128 * i; f32x2 rv[8]; unsigned xw[8];
; #pragma unroll
;                 for (int e = 0; e < 8; ++e) rv[e] = *(const LAS f32x2*)(Rg + e * DM + k);
; #pragma unroll
;                 for (int q = 0; q < 8; ++q) xw[q] = *(const unsigned*)(XB + (size_t)(t0 + q) * DM + k);
; #pragma unroll
;                 for (int q = 0; q < 8; ++q) { const float x0 = bflo(xw[q]), x1 = bfhi(xw[q]); ssq[q] += x0 * x0 + x1 * x1;
; #pragma unroll
;                     for (int e = 0; e < 8; ++e) acc[q][e] += x0 * rv[e].x + x1 * rv[e].y; } }
	v_pk_fma_f32 v[12:13], v[238:239], v[180:181], v[12:13] op_sel_hi:[0,1,1]
	v_pk_fma_f32 v[14:15], v[238:239], v[182:183], v[14:15] op_sel_hi:[0,1,1]
	v_pk_fma_f32 v[8:9], v[238:239], v[184:185], v[8:9] op_sel:[1,0,0] op_sel_hi:[1,1,1]
	v_pk_fma_f32 v[10:11], v[238:239], v[186:187], v[10:11] op_sel:[1,0,0] op_sel_hi:[1,1,1]
	v_pk_fma_f32 v[12:13], v[238:239], v[188:189], v[12:13] op_sel:[1,0,0] op_sel_hi:[1,1,1]
	v_pk_fma_f32 v[14:15], v[238:239], v[190:191], v[14:15] op_sel:[1,0,0] op_sel_hi:[1,1,1]
	v_lshlrev_b32_e32 v232, 16, v104
	v_and_b32_e32 v233, s15, v104
	v_lshlrev_b32_e32 v234, 16, v105
	v_and_b32_e32 v235, s15, v105
	v_lshlrev_b32_e32 v236, 16, v106
	v_and_b32_e32 v237, s15, v106
	v_lshlrev_b32_e32 v238, 16, v107
	v_and_b32_e32 v239, s15, v107
	v_pk_fma_f32 v[196:197], v[232:233], v[232:233], v[196:197]
	v_pk_fma_f32 v[196:197], v[234:235], v[234:235], v[196:197]
	v_pk_fma_f32 v[196:197], v[236:237], v[236:237], v[196:197]
	v_pk_fma_f32 v[196:197], v[238:239], v[238:239], v[196:197]
	v_pk_fma_f32 v[16:17], v[232:233], v[128:129], v[16:17] op_sel_hi:[0,1,1]
	v_pk_fma_f32 v[18:19], v[232:233], v[130:131], v[18:19] op_sel_hi:[0,1,1]
	v_pk_fma_f32 v[20:21], v[232:233], v[132:133], v[20:21] op_sel_hi:[0,1,1]
	v_pk_fma_f32 v[22:23], v[232:233], v[134:135], v[22:23] op_sel_hi:[0,1,1]
	v_pk_fma_f32 v[16:17], v[232:233], v[136:137], v[16:17] op_sel:[1,0,0] op_sel_hi:[1,1,1]
	v_pk_fma_f32 v[18:19], v[232:233], v[138:139], v[18:19] op_sel:[1,0,0] op_sel_hi:[1,1,1]
	v_pk_fma_f32 v[20:21], v[232:233], v[140:141], v[20:21] op_sel:[1,0,0] op_sel_hi:[1,1,1]
	v_pk_fma_f32 v[22:23], v[232:233], v[142:143], v[22:23] op_sel:[1,0,0] op_sel_hi:[1,1,1]
	v_pk_fma_f32 v[16:17], v[234:235], v[144:145], v[16:17] op_sel_hi:[0,1,1]
	v_pk_fma_f32 v[18:19], v[234:235], v[146:147], v[18:19] op_sel_hi:[0,1,1]
	v_pk_fma_f32 v[20:21], v[234:235], v[148:149], v[20:21] op_sel_hi:[0,1,1]
	v_pk_fma_f32 v[22:23], v[234:235], v[150:151], v[22:23] op_sel_hi:[0,1,1]
	v_pk_fma_f32 v[16:17], v[234:235], v[152:153], v[16:17] op_sel:[1,0,0] op_sel_hi:[1,1,1]
	v_pk_fma_f32 v[18:19], v[234:235], v[154:155], v[18:19] op_sel:[1,0,0] op_sel_hi:[1,1,1]
	v_pk_fma_f32 v[20:21], v[234:235], v[156:157], v[20:21] op_sel:[1,0,0] op_sel_hi:[1,1,1]
	v_pk_fma_f32 v[22:23], v[234:235], v[158:159], v[22:23] op_sel:[1,0,0] op_sel_hi:[1,1,1]
	v_pk_fma_f32 v[16:17], v[236:237], v[160:161], v[16:17] op_sel_hi:[0,1,1]
	v_pk_fma_f32 v[18:19], v[236:237], v[162:163], v[18:19] op_sel_hi:[0,1,1]
	v_pk_fma_f32 v[20:21], v[236:237], v[164:165], v[20:21] op_sel_hi:[0,1,1]
	v_pk_fma_f32 v[22:23], v[236:237], v[166:167], v[22:23] op_sel_hi:[0,1,1]
	v_pk_fma_f32 v[16:17], v[236:237], v[168:169], v[16:17] op_sel:[1,0,0] op_sel_hi:[1,1,1]
	v_pk_fma_f32 v[18:19], v[236:237], v[170:171], v[18:19] op_sel:[1,0,0] op_sel_hi:[1,1,1]
	v_pk_fma_f32 v[20:21], v[236:237], v[172:173], v[20:21] op_sel:[1,0,0] op_sel_hi:[1,1,1]
	v_pk_fma_f32 v[22:23], v[236:237], v[174:175], v[22:23] op_sel:[1,0,0] op_sel_hi:[1,1,1]
	v_pk_fma_f32 v[16:17], v[238:239], v[176:177], v[16:17] op_sel_hi:[0,1,1]
	v_pk_fma_f32 v[18:19], v[238:239], v[178:179], v[18:19] op_sel_hi:[0,1,1]
	v_pk_fma_f32 v[20:21], v[238:239], v[180:181], v[20:21] op_sel_hi:[0,1,1]
	v_pk_fma_f32 v[22:23], v[238:239], v[182:183], v[22:23] op_sel_hi:[0,1,1]
	v_pk_fma_f32 v[16:17], v[238:239], v[184:185], v[16:17] op_sel:[1,0,0] op_sel_hi:[1,1,1]
	v_pk_fma_f32 v[18:19], v[238:239], v[186:187], v[18:19] op_sel:[1,0,0] op_sel_hi:[1,1,1]
	v_pk_fma_f32 v[20:21], v[238:239], v[188:189], v[20:21] op_sel:[1,0,0] op_sel_hi:[1,1,1]
	v_pk_fma_f32 v[22:23], v[238:239], v[190:191], v[22:23] op_sel:[1,0,0] op_sel_hi:[1,1,1]
	v_lshlrev_b32_e32 v232, 16, v108
	v_and_b32_e32 v233, s15, v108
	v_lshlrev_b32_e32 v234, 16, v109
	v_and_b32_e32 v235, s15, v109
	v_lshlrev_b32_e32 v236, 16, v110
	v_and_b32_e32 v237, s15, v110
	v_lshlrev_b32_e32 v238, 16, v111
	v_and_b32_e32 v239, s15, v111
	v_pk_fma_f32 v[198:199], v[232:233], v[232:233], v[198:199]
	v_pk_fma_f32 v[198:199], v[234:235], v[234:235], v[198:199]
	v_pk_fma_f32 v[198:199], v[236:237], v[236:237], v[198:199]
	v_pk_fma_f32 v[198:199], v[238:239], v[238:239], v[198:199]
	v_pk_fma_f32 v[24:25], v[232:233], v[128:129], v[24:25] op_sel_hi:[0,1,1]
	v_pk_fma_f32 v[26:27], v[232:233], v[130:131], v[26:27] op_sel_hi:[0,1,1]
	v_pk_fma_f32 v[28:29], v[232:233], v[132:133], v[28:29] op_sel_hi:[0,1,1]
	v_pk_fma_f32 v[30:31], v[232:233], v[134:135], v[30:31] op_sel_hi:[0,1,1]
	v_pk_fma_f32 v[24:25], v[232:233], v[136:137], v[24:25] op_sel:[1,0,0] op_sel_hi:[1,1,1]
	v_pk_fma_f32 v[26:27], v[232:233], v[138:139], v[26:27] op_sel:[1,0,0] op_sel_hi:[1,1,1]
	v_pk_fma_f32 v[28:29], v[232:233], v[140:141], v[28:29] op_sel:[1,0,0] op_sel_hi:[1,1,1]
	v_pk_fma_f32 v[30:31], v[232:233], v[142:143], v[30:31] op_sel:[1,0,0] op_sel_hi:[1,1,1]
	v_pk_fma_f32 v[24:25], v[234:235], v[144:145], v[24:25] op_sel_hi:[0,1,1]
	v_pk_fma_f32 v[26:27], v[234:235], v[146:147], v[26:27] op_sel_hi:[0,1,1]
	v_pk_fma_f32 v[28:29], v[234:235], v[148:149], v[28:29] op_sel_hi:[0,1,1]
	v_pk_fma_f32 v[30:31], v[234:235], v[150:151], v[30:31] op_sel_hi:[0,1,1]
	v_pk_fma_f32 v[24:25], v[234:235], v[152:153], v[24:25] op_sel:[1,0,0] op_sel_hi:[1,1,1]
	v_pk_fma_f32 v[26:27], v[234:235], v[154:155], v[26:27] op_sel:[1,0,0] op_sel_hi:[1,1,1]
	v_pk_fma_f32 v[28:29], v[234:235], v[156:157], v[28:29] op_sel:[1,0,0] op_sel_hi:[1,1,1]
	v_pk_fma_f32 v[30:31], v[234:235], v[158:159], v[30:31] op_sel:[1,0,0] op_sel_hi:[1,1,1]
	v_pk_fma_f32 v[24:25], v[236:237], v[160:161], v[24:25] op_sel_hi:[0,1,1]
	v_pk_fma_f32 v[26:27], v[236:237], v[162:163], v[26:27] op_sel_hi:[0,1,1]
; #define LAS __attribute__((address_space(3)))
; __global__ void __launch_bounds__(NTHR, 2) fwd_kernel(Args args) {
;     ...
;             for (int i = 0; i < 16; ++i) { const int k = 2 * lane + 128 * i; f32x2 rv[8]; unsigned xw[8];
; #pragma unroll
;                 for (int e = 0; e < 8; ++e) rv[e] = *(const LAS f32x2*)(Rg + e * DM + k);
; #pragma unroll
;                 for (int q = 0; q < 8; ++q) xw[q] = *(const unsigned*)(XB + (size_t)(t0 + q) * DM + k);
; #pragma unroll
;                 for (int q = 0; q < 8; ++q) { const float x0 = bflo(xw[q]), x1 = bfhi(xw[q]); ssq[q] += x0 * x0 + x1 * x1;
; #pragma unroll
;                     for (int e = 0; e < 8; ++e) acc[q][e] += x0 * rv[e].x + x1 * rv[e].y; } }
	v_pk_fma_f32 v[28:29], v[236:237], v[164:165], v[28:29] op_sel_hi:[0,1,1]
	v_pk_fma_f32 v[30:31], v[236:237], v[166:167], v[30:31] op_sel_hi:[0,1,1]
	v_pk_fma_f32 v[24:25], v[236:237], v[168:169], v[24:25] op_sel:[1,0,0] op_sel_hi:[1,1,1]
	v_pk_fma_f32 v[26:27], v[236:237], v[170:171], v[26:27] op_sel:[1,0,0] op_sel_hi:[1,1,1]
	v_pk_fma_f32 v[28:29], v[236:237], v[172:173], v[28:29] op_sel:[1,0,0] op_sel_hi:[1,1,1]
	v_pk_fma_f32 v[30:31], v[236:237], v[174:175], v[30:31] op_sel:[1,0,0] op_sel_hi:[1,1,1]
	v_pk_fma_f32 v[24:25], v[238:239], v[176:177], v[24:25] op_sel_hi:[0,1,1]
	v_pk_fma_f32 v[26:27], v[238:239], v[178:179], v[26:27] op_sel_hi:[0,1,1]
	v_pk_fma_f32 v[28:29], v[238:239], v[180:181], v[28:29] op_sel_hi:[0,1,1]
	v_pk_fma_f32 v[30:31], v[238:239], v[182:183], v[30:31] op_sel_hi:[0,1,1]
	v_pk_fma_f32 v[24:25], v[238:239], v[184:185], v[24:25] op_sel:[1,0,0] op_sel_hi:[1,1,1]
	v_pk_fma_f32 v[26:27], v[238:239], v[186:187], v[26:27] op_sel:[1,0,0] op_sel_hi:[1,1,1]
	v_pk_fma_f32 v[28:29], v[238:239], v[188:189], v[28:29] op_sel:[1,0,0] op_sel_hi:[1,1,1]
	v_pk_fma_f32 v[30:31], v[238:239], v[190:191], v[30:31] op_sel:[1,0,0] op_sel_hi:[1,1,1]
	v_lshlrev_b32_e32 v232, 16, v112
	v_and_b32_e32 v233, s15, v112
	v_lshlrev_b32_e32 v234, 16, v113
	v_and_b32_e32 v235, s15, v113
	v_lshlrev_b32_e32 v236, 16, v114
	v_and_b32_e32 v237, s15, v114
	v_lshlrev_b32_e32 v238, 16, v115
	v_and_b32_e32 v239, s15, v115
	v_pk_fma_f32 v[200:201], v[232:233], v[232:233], v[200:201]
	v_pk_fma_f32 v[200:201], v[234:235], v[234:235], v[200:201]
	v_pk_fma_f32 v[200:201], v[236:237], v[236:237], v[200:201]
	v_pk_fma_f32 v[200:201], v[238:239], v[238:239], v[200:201]
	v_pk_fma_f32 v[32:33], v[232:233], v[128:129], v[32:33] op_sel_hi:[0,1,1]
	v_pk_fma_f32 v[34:35], v[232:233], v[130:131], v[34:35] op_sel_hi:[0,1,1]
	v_pk_fma_f32 v[36:37], v[232:233], v[132:133], v[36:37] op_sel_hi:[0,1,1]
	v_pk_fma_f32 v[38:39], v[232:233], v[134:135], v[38:39] op_sel_hi:[0,1,1]
	v_pk_fma_f32 v[32:33], v[232:233], v[136:137], v[32:33] op_sel:[1,0,0] op_sel_hi:[1,1,1]
	v_pk_fma_f32 v[34:35], v[232:233], v[138:139], v[34:35] op_sel:[1,0,0] op_sel_hi:[1,1,1]
	v_pk_fma_f32 v[36:37], v[232:233], v[140:141], v[36:37] op_sel:[1,0,0] op_sel_hi:[1,1,1]
	v_pk_fma_f32 v[38:39], v[232:233], v[142:143], v[38:39] op_sel:[1,0,0] op_sel_hi:[1,1,1]
	v_pk_fma_f32 v[32:33], v[234:235], v[144:145], v[32:33] op_sel_hi:[0,1,1]
	v_pk_fma_f32 v[34:35], v[234:235], v[146:147], v[34:35] op_sel_hi:[0,1,1]
	v_pk_fma_f32 v[36:37], v[234:235], v[148:149], v[36:37] op_sel_hi:[0,1,1]
	v_pk_fma_f32 v[38:39], v[234:235], v[150:151], v[38:39] op_sel_hi:[0,1,1]
	v_pk_fma_f32 v[32:33], v[234:235], v[152:153], v[32:33] op_sel:[1,0,0] op_sel_hi:[1,1,1]
	v_pk_fma_f32 v[34:35], v[234:235], v[154:155], v[34:35] op_sel:[1,0,0] op_sel_hi:[1,1,1]
	v_pk_fma_f32 v[36:37], v[234:235], v[156:157], v[36:37] op_sel:[1,0,0] op_sel_hi:[1,1,1]
	v_pk_fma_f32 v[38:39], v[234:235], v[158:159], v[38:39] op_sel:[1,0,0] op_sel_hi:[1,1,1]
	v_pk_fma_f32 v[32:33], v[236:237], v[160:161], v[32:33] op_sel_hi:[0,1,1]
	v_pk_fma_f32 v[34:35], v[236:237], v[162:163], v[34:35] op_sel_hi:[0,1,1]
	v_pk_fma_f32 v[36:37], v[236:237], v[164:165], v[36:37] op_sel_hi:[0,1,1]
	v_pk_fma_f32 v[38:39], v[236:237], v[166:167], v[38:39] op_sel_hi:[0,1,1]
	v_pk_fma_f32 v[32:33], v[236:237], v[168:169], v[32:33] op_sel:[1,0,0] op_sel_hi:[1,1,1]
	v_pk_fma_f32 v[34:35], v[236:237], v[170:171], v[34:35] op_sel:[1,0,0] op_sel_hi:[1,1,1]
	v_pk_fma_f32 v[36:37], v[236:237], v[172:173], v[36:37] op_sel:[1,0,0] op_sel_hi:[1,1,1]
	v_pk_fma_f32 v[38:39], v[236:237], v[174:175], v[38:39] op_sel:[1,0,0] op_sel_hi:[1,1,1]
	v_pk_fma_f32 v[32:33], v[238:239], v[176:177], v[32:33] op_sel_hi:[0,1,1]
	v_pk_fma_f32 v[34:35], v[238:239], v[178:179], v[34:35] op_sel_hi:[0,1,1]
	v_pk_fma_f32 v[36:37], v[238:239], v[180:181], v[36:37] op_sel_hi:[0,1,1]
	v_pk_fma_f32 v[38:39], v[238:239], v[182:183], v[38:39] op_sel_hi:[0,1,1]
	v_pk_fma_f32 v[32:33], v[238:239], v[184:185], v[32:33] op_sel:[1,0,0] op_sel_hi:[1,1,1]
	v_pk_fma_f32 v[34:35], v[238:239], v[186:187], v[34:35] op_sel:[1,0,0] op_sel_hi:[1,1,1]
	v_pk_fma_f32 v[36:37], v[238:239], v[188:189], v[36:37] op_sel:[1,0,0] op_sel_hi:[1,1,1]
	v_pk_fma_f32 v[38:39], v[238:239], v[190:191], v[38:39] op_sel:[1,0,0] op_sel_hi:[1,1,1]
	v_lshlrev_b32_e32 v232, 16, v116
	v_and_b32_e32 v233, s15, v116
	v_lshlrev_b32_e32 v234, 16, v117
	v_and_b32_e32 v235, s15, v117
	v_lshlrev_b32_e32 v236, 16, v118
	v_and_b32_e32 v237, s15, v118
	v_lshlrev_b32_e32 v238, 16, v119
	v_and_b32_e32 v239, s15, v119
	v_pk_fma_f32 v[202:203], v[232:233], v[232:233], v[202:203]
	v_pk_fma_f32 v[202:203], v[234:235], v[234:235], v[202:203]
	v_pk_fma_f32 v[202:203], v[236:237], v[236:237], v[202:203]
	v_pk_fma_f32 v[202:203], v[238:239], v[238:239], v[202:203]
	v_pk_fma_f32 v[40:41], v[232:233], v[128:129], v[40:41] op_sel_hi:[0,1,1]
	v_pk_fma_f32 v[42:43], v[232:233], v[130:131], v[42:43] op_sel_hi:[0,1,1]
	v_pk_fma_f32 v[44:45], v[232:233], v[132:133], v[44:45] op_sel_hi:[0,1,1]
	v_pk_fma_f32 v[46:47], v[232:233], v[134:135], v[46:47] op_sel_hi:[0,1,1]
	v_pk_fma_f32 v[40:41], v[232:233], v[136:137], v[40:41] op_sel:[1,0,0] op_sel_hi:[1,1,1]
	v_pk_fma_f32 v[42:43], v[232:233], v[138:139], v[42:43] op_sel:[1,0,0] op_sel_hi:[1,1,1]
	v_pk_fma_f32 v[44:45], v[232:233], v[140:141], v[44:45] op_sel:[1,0,0] op_sel_hi:[1,1,1]
	v_pk_fma_f32 v[46:47], v[232:233], v[142:143], v[46:47] op_sel:[1,0,0] op_sel_hi:[1,1,1]
	v_pk_fma_f32 v[40:41], v[234:235], v[144:145], v[40:41] op_sel_hi:[0,1,1]
	v_pk_fma_f32 v[42:43], v[234:235], v[146:147], v[42:43] op_sel_hi:[0,1,1]
; #define LAS __attribute__((address_space(3)))
; __global__ void __launch_bounds__(NTHR, 2) fwd_kernel(Args args) {
;     ...
;             for (int i = 0; i < 16; ++i) { const int k = 2 * lane + 128 * i; f32x2 rv[8]; unsigned xw[8];
; #pragma unroll
;                 for (int e = 0; e < 8; ++e) rv[e] = *(const LAS f32x2*)(Rg + e * DM + k);
; #pragma unroll
;                 for (int q = 0; q < 8; ++q) xw[q] = *(const unsigned*)(XB + (size_t)(t0 + q) * DM + k);
; #pragma unroll
;                 for (int q = 0; q < 8; ++q) { const float x0 = bflo(xw[q]), x1 = bfhi(xw[q]); ssq[q] += x0 * x0 + x1 * x1;
; #pragma unroll
;                     for (int e = 0; e < 8; ++e) acc[q][e] += x0 * rv[e].x + x1 * rv[e].y; } }
	v_pk_fma_f32 v[44:45], v[234:235], v[148:149], v[44:45] op_sel_hi:[0,1,1]
	v_pk_fma_f32 v[46:47], v[234:235], v[150:151], v[46:47] op_sel_hi:[0,1,1]
	v_pk_fma_f32 v[40:41], v[234:235], v[152:153], v[40:41] op_sel:[1,0,0] op_sel_hi:[1,1,1]
	v_pk_fma_f32 v[42:43], v[234:235], v[154:155], v[42:43] op_sel:[1,0,0] op_sel_hi:[1,1,1]
	v_pk_fma_f32 v[44:45], v[234:235], v[156:157], v[44:45] op_sel:[1,0,0] op_sel_hi:[1,1,1]
	v_pk_fma_f32 v[46:47], v[234:235], v[158:159], v[46:47] op_sel:[1,0,0] op_sel_hi:[1,1,1]
	v_pk_fma_f32 v[40:41], v[236:237], v[160:161], v[40:41] op_sel_hi:[0,1,1]
	v_pk_fma_f32 v[42:43], v[236:237], v[162:163], v[42:43] op_sel_hi:[0,1,1]
	v_pk_fma_f32 v[44:45], v[236:237], v[164:165], v[44:45] op_sel_hi:[0,1,1]
	v_pk_fma_f32 v[46:47], v[236:237], v[166:167], v[46:47] op_sel_hi:[0,1,1]
	v_pk_fma_f32 v[40:41], v[236:237], v[168:169], v[40:41] op_sel:[1,0,0] op_sel_hi:[1,1,1]
	v_pk_fma_f32 v[42:43], v[236:237], v[170:171], v[42:43] op_sel:[1,0,0] op_sel_hi:[1,1,1]
	v_pk_fma_f32 v[44:45], v[236:237], v[172:173], v[44:45] op_sel:[1,0,0] op_sel_hi:[1,1,1]
	v_pk_fma_f32 v[46:47], v[236:237], v[174:175], v[46:47] op_sel:[1,0,0] op_sel_hi:[1,1,1]
	v_pk_fma_f32 v[40:41], v[238:239], v[176:177], v[40:41] op_sel_hi:[0,1,1]
	v_pk_fma_f32 v[42:43], v[238:239], v[178:179], v[42:43] op_sel_hi:[0,1,1]
	v_pk_fma_f32 v[44:45], v[238:239], v[180:181], v[44:45] op_sel_hi:[0,1,1]
	v_pk_fma_f32 v[46:47], v[238:239], v[182:183], v[46:47] op_sel_hi:[0,1,1]
	v_pk_fma_f32 v[40:41], v[238:239], v[184:185], v[40:41] op_sel:[1,0,0] op_sel_hi:[1,1,1]
	v_pk_fma_f32 v[42:43], v[238:239], v[186:187], v[42:43] op_sel:[1,0,0] op_sel_hi:[1,1,1]
	v_pk_fma_f32 v[44:45], v[238:239], v[188:189], v[44:45] op_sel:[1,0,0] op_sel_hi:[1,1,1]
	v_pk_fma_f32 v[46:47], v[238:239], v[190:191], v[46:47] op_sel:[1,0,0] op_sel_hi:[1,1,1]
	v_lshlrev_b32_e32 v232, 16, v120
	v_and_b32_e32 v233, s15, v120
	v_lshlrev_b32_e32 v234, 16, v121
	v_and_b32_e32 v235, s15, v121
	v_lshlrev_b32_e32 v236, 16, v122
	v_and_b32_e32 v237, s15, v122
	v_lshlrev_b32_e32 v238, 16, v123
	v_and_b32_e32 v239, s15, v123
	v_pk_fma_f32 v[204:205], v[232:233], v[232:233], v[204:205]
	v_pk_fma_f32 v[204:205], v[234:235], v[234:235], v[204:205]
	v_pk_fma_f32 v[204:205], v[236:237], v[236:237], v[204:205]
	v_pk_fma_f32 v[204:205], v[238:239], v[238:239], v[204:205]
	v_pk_fma_f32 v[48:49], v[232:233], v[128:129], v[48:49] op_sel_hi:[0,1,1]
	v_pk_fma_f32 v[50:51], v[232:233], v[130:131], v[50:51] op_sel_hi:[0,1,1]
	v_pk_fma_f32 v[52:53], v[232:233], v[132:133], v[52:53] op_sel_hi:[0,1,1]
	v_pk_fma_f32 v[54:55], v[232:233], v[134:135], v[54:55] op_sel_hi:[0,1,1]
	v_pk_fma_f32 v[48:49], v[232:233], v[136:137], v[48:49] op_sel:[1,0,0] op_sel_hi:[1,1,1]
	v_pk_fma_f32 v[50:51], v[232:233], v[138:139], v[50:51] op_sel:[1,0,0] op_sel_hi:[1,1,1]
	v_pk_fma_f32 v[52:53], v[232:233], v[140:141], v[52:53] op_sel:[1,0,0] op_sel_hi:[1,1,1]
	v_pk_fma_f32 v[54:55], v[232:233], v[142:143], v[54:55] op_sel:[1,0,0] op_sel_hi:[1,1,1]
	v_pk_fma_f32 v[48:49], v[234:235], v[144:145], v[48:49] op_sel_hi:[0,1,1]
	v_pk_fma_f32 v[50:51], v[234:235], v[146:147], v[50:51] op_sel_hi:[0,1,1]
	v_pk_fma_f32 v[52:53], v[234:235], v[148:149], v[52:53] op_sel_hi:[0,1,1]
	v_pk_fma_f32 v[54:55], v[234:235], v[150:151], v[54:55] op_sel_hi:[0,1,1]
	v_pk_fma_f32 v[48:49], v[234:235], v[152:153], v[48:49] op_sel:[1,0,0] op_sel_hi:[1,1,1]
	v_pk_fma_f32 v[50:51], v[234:235], v[154:155], v[50:51] op_sel:[1,0,0] op_sel_hi:[1,1,1]
	v_pk_fma_f32 v[52:53], v[234:235], v[156:157], v[52:53] op_sel:[1,0,0] op_sel_hi:[1,1,1]
	v_pk_fma_f32 v[54:55], v[234:235], v[158:159], v[54:55] op_sel:[1,0,0] op_sel_hi:[1,1,1]
	v_pk_fma_f32 v[48:49], v[236:237], v[160:161], v[48:49] op_sel_hi:[0,1,1]
	v_pk_fma_f32 v[50:51], v[236:237], v[162:163], v[50:51] op_sel_hi:[0,1,1]
	v_pk_fma_f32 v[52:53], v[236:237], v[164:165], v[52:53] op_sel_hi:[0,1,1]
	v_pk_fma_f32 v[54:55], v[236:237], v[166:167], v[54:55] op_sel_hi:[0,1,1]
	v_pk_fma_f32 v[48:49], v[236:237], v[168:169], v[48:49] op_sel:[1,0,0] op_sel_hi:[1,1,1]
	v_pk_fma_f32 v[50:51], v[236:237], v[170:171], v[50:51] op_sel:[1,0,0] op_sel_hi:[1,1,1]
	v_pk_fma_f32 v[52:53], v[236:237], v[172:173], v[52:53] op_sel:[1,0,0] op_sel_hi:[1,1,1]
	v_pk_fma_f32 v[54:55], v[236:237], v[174:175], v[54:55] op_sel:[1,0,0] op_sel_hi:[1,1,1]
	v_pk_fma_f32 v[48:49], v[238:239], v[176:177], v[48:49] op_sel_hi:[0,1,1]
	v_pk_fma_f32 v[50:51], v[238:239], v[178:179], v[50:51] op_sel_hi:[0,1,1]
	v_pk_fma_f32 v[52:53], v[238:239], v[180:181], v[52:53] op_sel_hi:[0,1,1]
	v_pk_fma_f32 v[54:55], v[238:239], v[182:183], v[54:55] op_sel_hi:[0,1,1]
	v_pk_fma_f32 v[48:49], v[238:239], v[184:185], v[48:49] op_sel:[1,0,0] op_sel_hi:[1,1,1]
	v_pk_fma_f32 v[50:51], v[238:239], v[186:187], v[50:51] op_sel:[1,0,0] op_sel_hi:[1,1,1]
	v_pk_fma_f32 v[52:53], v[238:239], v[188:189], v[52:53] op_sel:[1,0,0] op_sel_hi:[1,1,1]
	v_pk_fma_f32 v[54:55], v[238:239], v[190:191], v[54:55] op_sel:[1,0,0] op_sel_hi:[1,1,1]
	v_lshlrev_b32_e32 v232, 16, v124
	v_and_b32_e32 v233, s15, v124
	v_lshlrev_b32_e32 v234, 16, v125
	v_and_b32_e32 v235, s15, v125
	v_lshlrev_b32_e32 v236, 16, v126
	v_and_b32_e32 v237, s15, v126
	v_lshlrev_b32_e32 v238, 16, v127
	v_and_b32_e32 v239, s15, v127
	v_pk_fma_f32 v[206:207], v[232:233], v[232:233], v[206:207]
	v_pk_fma_f32 v[206:207], v[234:235], v[234:235], v[206:207]
	v_pk_fma_f32 v[206:207], v[236:237], v[236:237], v[206:207]
	v_pk_fma_f32 v[206:207], v[238:239], v[238:239], v[206:207]
	v_pk_fma_f32 v[56:57], v[232:233], v[128:129], v[56:57] op_sel_hi:[0,1,1]
	v_pk_fma_f32 v[58:59], v[232:233], v[130:131], v[58:59] op_sel_hi:[0,1,1]
; #define LAS __attribute__((address_space(3)))
; __global__ void __launch_bounds__(NTHR, 2) fwd_kernel(Args args) {
;     ...
;             for (int i = 0; i < 16; ++i) { const int k = 2 * lane + 128 * i; f32x2 rv[8]; unsigned xw[8];
; #pragma unroll
;                 for (int e = 0; e < 8; ++e) rv[e] = *(const LAS f32x2*)(Rg + e * DM + k);
; #pragma unroll
;                 for (int q = 0; q < 8; ++q) xw[q] = *(const unsigned*)(XB + (size_t)(t0 + q) * DM + k);
; #pragma unroll
;                 for (int q = 0; q < 8; ++q) { const float x0 = bflo(xw[q]), x1 = bfhi(xw[q]); ssq[q] += x0 * x0 + x1 * x1;
; #pragma unroll
;                     for (int e = 0; e < 8; ++e) acc[q][e] += x0 * rv[e].x + x1 * rv[e].y; } }
	v_pk_fma_f32 v[60:61], v[232:233], v[132:133], v[60:61] op_sel_hi:[0,1,1]
	v_pk_fma_f32 v[62:63], v[232:233], v[134:135], v[62:63] op_sel_hi:[0,1,1]
	v_pk_fma_f32 v[56:57], v[232:233], v[136:137], v[56:57] op_sel:[1,0,0] op_sel_hi:[1,1,1]
	v_pk_fma_f32 v[58:59], v[232:233], v[138:139], v[58:59] op_sel:[1,0,0] op_sel_hi:[1,1,1]
	v_pk_fma_f32 v[60:61], v[232:233], v[140:141], v[60:61] op_sel:[1,0,0] op_sel_hi:[1,1,1]
	v_pk_fma_f32 v[62:63], v[232:233], v[142:143], v[62:63] op_sel:[1,0,0] op_sel_hi:[1,1,1]
	v_pk_fma_f32 v[56:57], v[234:235], v[144:145], v[56:57] op_sel_hi:[0,1,1]
	v_pk_fma_f32 v[58:59], v[234:235], v[146:147], v[58:59] op_sel_hi:[0,1,1]
	v_pk_fma_f32 v[60:61], v[234:235], v[148:149], v[60:61] op_sel_hi:[0,1,1]
	v_pk_fma_f32 v[62:63], v[234:235], v[150:151], v[62:63] op_sel_hi:[0,1,1]
	v_pk_fma_f32 v[56:57], v[234:235], v[152:153], v[56:57] op_sel:[1,0,0] op_sel_hi:[1,1,1]
	v_pk_fma_f32 v[58:59], v[234:235], v[154:155], v[58:59] op_sel:[1,0,0] op_sel_hi:[1,1,1]
	v_pk_fma_f32 v[60:61], v[234:235], v[156:157], v[60:61] op_sel:[1,0,0] op_sel_hi:[1,1,1]
	v_pk_fma_f32 v[62:63], v[234:235], v[158:159], v[62:63] op_sel:[1,0,0] op_sel_hi:[1,1,1]
	v_pk_fma_f32 v[56:57], v[236:237], v[160:161], v[56:57] op_sel_hi:[0,1,1]
	v_pk_fma_f32 v[58:59], v[236:237], v[162:163], v[58:59] op_sel_hi:[0,1,1]
	v_pk_fma_f32 v[60:61], v[236:237], v[164:165], v[60:61] op_sel_hi:[0,1,1]
	v_pk_fma_f32 v[62:63], v[236:237], v[166:167], v[62:63] op_sel_hi:[0,1,1]
	v_pk_fma_f32 v[56:57], v[236:237], v[168:169], v[56:57] op_sel:[1,0,0] op_sel_hi:[1,1,1]
	v_pk_fma_f32 v[58:59], v[236:237], v[170:171], v[58:59] op_sel:[1,0,0] op_sel_hi:[1,1,1]
	v_pk_fma_f32 v[60:61], v[236:237], v[172:173], v[60:61] op_sel:[1,0,0] op_sel_hi:[1,1,1]
	v_pk_fma_f32 v[62:63], v[236:237], v[174:175], v[62:63] op_sel:[1,0,0] op_sel_hi:[1,1,1]
	v_pk_fma_f32 v[56:57], v[238:239], v[176:177], v[56:57] op_sel_hi:[0,1,1]
	v_pk_fma_f32 v[58:59], v[238:239], v[178:179], v[58:59] op_sel_hi:[0,1,1]
	v_pk_fma_f32 v[60:61], v[238:239], v[180:181], v[60:61] op_sel_hi:[0,1,1]
	v_pk_fma_f32 v[62:63], v[238:239], v[182:183], v[62:63] op_sel_hi:[0,1,1]
	v_pk_fma_f32 v[56:57], v[238:239], v[184:185], v[56:57] op_sel:[1,0,0] op_sel_hi:[1,1,1]
	v_pk_fma_f32 v[58:59], v[238:239], v[186:187], v[58:59] op_sel:[1,0,0] op_sel_hi:[1,1,1]
	v_pk_fma_f32 v[60:61], v[238:239], v[188:189], v[60:61] op_sel:[1,0,0] op_sel_hi:[1,1,1]
	v_pk_fma_f32 v[62:63], v[238:239], v[190:191], v[62:63] op_sel:[1,0,0] op_sel_hi:[1,1,1]
	global_load_dwordx4 v[96:99], v208, s[40:41] offset:3072
	global_load_dwordx4 v[100:103], v208, s[42:43] offset:3072
	global_load_dwordx4 v[104:107], v208, s[44:45] offset:3072
	global_load_dwordx4 v[108:111], v208, s[46:47] offset:3072
	global_load_dwordx4 v[112:115], v208, s[48:49] offset:3072
	global_load_dwordx4 v[116:119], v208, s[50:51] offset:3072
	global_load_dwordx4 v[120:123], v208, s[52:53] offset:3072
	global_load_dwordx4 v[124:127], v208, s[54:55] offset:3072
	ds_read_b128 v[128:131], v208 offset:32768
	ds_read_b128 v[132:135], v208 offset:33792
	ds_read_b128 v[136:139], v208 offset:34816
	ds_read_b128 v[140:143], v208 offset:35840
	ds_read_b128 v[144:147], v208 offset:36864
	ds_read_b128 v[148:151], v208 offset:37888
	ds_read_b128 v[152:155], v208 offset:38912
	ds_read_b128 v[156:159], v208 offset:39936
	ds_read_b128 v[160:163], v208 offset:40960
	ds_read_b128 v[164:167], v208 offset:41984
	ds_read_b128 v[168:171], v208 offset:43008
	ds_read_b128 v[172:175], v208 offset:44032
	ds_read_b128 v[176:179], v208 offset:45056
	ds_read_b128 v[180:183], v208 offset:46080
	ds_read_b128 v[184:187], v208 offset:47104
	ds_read_b128 v[188:191], v208 offset:48128
	s_waitcnt vmcnt(8)
	s_waitcnt lgkmcnt(0)
	v_lshlrev_b32_e32 v232, 16, v64
	v_and_b32_e32 v233, s15, v64
	v_lshlrev_b32_e32 v234, 16, v65
	v_and_b32_e32 v235, s15, v65
	v_lshlrev_b32_e32 v236, 16, v66
	v_and_b32_e32 v237, s15, v66
	v_lshlrev_b32_e32 v238, 16, v67
	v_and_b32_e32 v239, s15, v67
	v_pk_fma_f32 v[192:193], v[232:233], v[232:233], v[192:193]
	v_pk_fma_f32 v[192:193], v[234:235], v[234:235], v[192:193]
	v_pk_fma_f32 v[192:193], v[236:237], v[236:237], v[192:193]
	v_pk_fma_f32 v[192:193], v[238:239], v[238:239], v[192:193]
	v_pk_fma_f32 v[0:1], v[232:233], v[128:129], v[0:1] op_sel_hi:[0,1,1]
	v_pk_fma_f32 v[2:3], v[232:233], v[130:131], v[2:3] op_sel_hi:[0,1,1]
	v_pk_fma_f32 v[4:5], v[232:233], v[132:133], v[4:5] op_sel_hi:[0,1,1]
	v_pk_fma_f32 v[6:7], v[232:233], v[134:135], v[6:7] op_sel_hi:[0,1,1]
	v_pk_fma_f32 v[0:1], v[232:233], v[136:137], v[0:1] op_sel:[1,0,0] op_sel_hi:[1,1,1]
	v_pk_fma_f32 v[2:3], v[232:233], v[138:139], v[2:3] op_sel:[1,0,0] op_sel_hi:[1,1,1]
	v_pk_fma_f32 v[4:5], v[232:233], v[140:141], v[4:5] op_sel:[1,0,0] op_sel_hi:[1,1,1]
	v_pk_fma_f32 v[6:7], v[232:233], v[142:143], v[6:7] op_sel:[1,0,0] op_sel_hi:[1,1,1]
	v_pk_fma_f32 v[0:1], v[234:235], v[144:145], v[0:1] op_sel_hi:[0,1,1]
	v_pk_fma_f32 v[2:3], v[234:235], v[146:147], v[2:3] op_sel_hi:[0,1,1]
	v_pk_fma_f32 v[4:5], v[234:235], v[148:149], v[4:5] op_sel_hi:[0,1,1]
	v_pk_fma_f32 v[6:7], v[234:235], v[150:151], v[6:7] op_sel_hi:[0,1,1]
	v_pk_fma_f32 v[0:1], v[234:235], v[152:153], v[0:1] op_sel:[1,0,0] op_sel_hi:[1,1,1]
	v_pk_fma_f32 v[2:3], v[234:235], v[154:155], v[2:3] op_sel:[1,0,0] op_sel_hi:[1,1,1]
	v_pk_fma_f32 v[4:5], v[234:235], v[156:157], v[4:5] op_sel:[1,0,0] op_sel_hi:[1,1,1]
	v_pk_fma_f32 v[6:7], v[234:235], v[158:159], v[6:7] op_sel:[1,0,0] op_sel_hi:[1,1,1]
	v_pk_fma_f32 v[0:1], v[236:237], v[160:161], v[0:1] op_sel_hi:[0,1,1]
	v_pk_fma_f32 v[2:3], v[236:237], v[162:163], v[2:3] op_sel_hi:[0,1,1]
; #define LAS __attribute__((address_space(3)))
; __global__ void __launch_bounds__(NTHR, 2) fwd_kernel(Args args) {
;     ...
;             for (int i = 0; i < 16; ++i) { const int k = 2 * lane + 128 * i; f32x2 rv[8]; unsigned xw[8];
; #pragma unroll
;                 for (int e = 0; e < 8; ++e) rv[e] = *(const LAS f32x2*)(Rg + e * DM + k);
; #pragma unroll
;                 for (int q = 0; q < 8; ++q) xw[q] = *(const unsigned*)(XB + (size_t)(t0 + q) * DM + k);
; #pragma unroll
;                 for (int q = 0; q < 8; ++q) { const float x0 = bflo(xw[q]), x1 = bfhi(xw[q]); ssq[q] += x0 * x0 + x1 * x1;
; #pragma unroll
;                     for (int e = 0; e < 8; ++e) acc[q][e] += x0 * rv[e].x + x1 * rv[e].y; } }
	v_pk_fma_f32 v[4:5], v[236:237], v[164:165], v[4:5] op_sel_hi:[0,1,1]
	v_pk_fma_f32 v[6:7], v[236:237], v[166:167], v[6:7] op_sel_hi:[0,1,1]
	v_pk_fma_f32 v[0:1], v[236:237], v[168:169], v[0:1] op_sel:[1,0,0] op_sel_hi:[1,1,1]
	v_pk_fma_f32 v[2:3], v[236:237], v[170:171], v[2:3] op_sel:[1,0,0] op_sel_hi:[1,1,1]
	v_pk_fma_f32 v[4:5], v[236:237], v[172:173], v[4:5] op_sel:[1,0,0] op_sel_hi:[1,1,1]
	v_pk_fma_f32 v[6:7], v[236:237], v[174:175], v[6:7] op_sel:[1,0,0] op_sel_hi:[1,1,1]
	v_pk_fma_f32 v[0:1], v[238:239], v[176:177], v[0:1] op_sel_hi:[0,1,1]
	v_pk_fma_f32 v[2:3], v[238:239], v[178:179], v[2:3] op_sel_hi:[0,1,1]
	v_pk_fma_f32 v[4:5], v[238:239], v[180:181], v[4:5] op_sel_hi:[0,1,1]
	v_pk_fma_f32 v[6:7], v[238:239], v[182:183], v[6:7] op_sel_hi:[0,1,1]
	v_pk_fma_f32 v[0:1], v[238:239], v[184:185], v[0:1] op_sel:[1,0,0] op_sel_hi:[1,1,1]
	v_pk_fma_f32 v[2:3], v[238:239], v[186:187], v[2:3] op_sel:[1,0,0] op_sel_hi:[1,1,1]
	v_pk_fma_f32 v[4:5], v[238:239], v[188:189], v[4:5] op_sel:[1,0,0] op_sel_hi:[1,1,1]
	v_pk_fma_f32 v[6:7], v[238:239], v[190:191], v[6:7] op_sel:[1,0,0] op_sel_hi:[1,1,1]
	v_lshlrev_b32_e32 v232, 16, v68
	v_and_b32_e32 v233, s15, v68
	v_lshlrev_b32_e32 v234, 16, v69
	v_and_b32_e32 v235, s15, v69
	v_lshlrev_b32_e32 v236, 16, v70
	v_and_b32_e32 v237, s15, v70
	v_lshlrev_b32_e32 v238, 16, v71
	v_and_b32_e32 v239, s15, v71
	v_pk_fma_f32 v[194:195], v[232:233], v[232:233], v[194:195]
	v_pk_fma_f32 v[194:195], v[234:235], v[234:235], v[194:195]
	v_pk_fma_f32 v[194:195], v[236:237], v[236:237], v[194:195]
	v_pk_fma_f32 v[194:195], v[238:239], v[238:239], v[194:195]
	v_pk_fma_f32 v[8:9], v[232:233], v[128:129], v[8:9] op_sel_hi:[0,1,1]
	v_pk_fma_f32 v[10:11], v[232:233], v[130:131], v[10:11] op_sel_hi:[0,1,1]
	v_pk_fma_f32 v[12:13], v[232:233], v[132:133], v[12:13] op_sel_hi:[0,1,1]
	v_pk_fma_f32 v[14:15], v[232:233], v[134:135], v[14:15] op_sel_hi:[0,1,1]
	v_pk_fma_f32 v[8:9], v[232:233], v[136:137], v[8:9] op_sel:[1,0,0] op_sel_hi:[1,1,1]
	v_pk_fma_f32 v[10:11], v[232:233], v[138:139], v[10:11] op_sel:[1,0,0] op_sel_hi:[1,1,1]
	v_pk_fma_f32 v[12:13], v[232:233], v[140:141], v[12:13] op_sel:[1,0,0] op_sel_hi:[1,1,1]
	v_pk_fma_f32 v[14:15], v[232:233], v[142:143], v[14:15] op_sel:[1,0,0] op_sel_hi:[1,1,1]
	v_pk_fma_f32 v[8:9], v[234:235], v[144:145], v[8:9] op_sel_hi:[0,1,1]
	v_pk_fma_f32 v[10:11], v[234:235], v[146:147], v[10:11] op_sel_hi:[0,1,1]
	v_pk_fma_f32 v[12:13], v[234:235], v[148:149], v[12:13] op_sel_hi:[0,1,1]
	v_pk_fma_f32 v[14:15], v[234:235], v[150:151], v[14:15] op_sel_hi:[0,1,1]
	v_pk_fma_f32 v[8:9], v[234:235], v[152:153], v[8:9] op_sel:[1,0,0] op_sel_hi:[1,1,1]
	v_pk_fma_f32 v[10:11], v[234:235], v[154:155], v[10:11] op_sel:[1,0,0] op_sel_hi:[1,1,1]
	v_pk_fma_f32 v[12:13], v[234:235], v[156:157], v[12:13] op_sel:[1,0,0] op_sel_hi:[1,1,1]
	v_pk_fma_f32 v[14:15], v[234:235], v[158:159], v[14:15] op_sel:[1,0,0] op_sel_hi:[1,1,1]
	v_pk_fma_f32 v[8:9], v[236:237], v[160:161], v[8:9] op_sel_hi:[0,1,1]
	v_pk_fma_f32 v[10:11], v[236:237], v[162:163], v[10:11] op_sel_hi:[0,1,1]
	v_pk_fma_f32 v[12:13], v[236:237], v[164:165], v[12:13] op_sel_hi:[0,1,1]
	v_pk_fma_f32 v[14:15], v[236:237], v[166:167], v[14:15] op_sel_hi:[0,1,1]
	v_pk_fma_f32 v[8:9], v[236:237], v[168:169], v[8:9] op_sel:[1,0,0] op_sel_hi:[1,1,1]
	v_pk_fma_f32 v[10:11], v[236:237], v[170:171], v[10:11] op_sel:[1,0,0] op_sel_hi:[1,1,1]
	v_pk_fma_f32 v[12:13], v[236:237], v[172:173], v[12:13] op_sel:[1,0,0] op_sel_hi:[1,1,1]
	v_pk_fma_f32 v[14:15], v[236:237], v[174:175], v[14:15] op_sel:[1,0,0] op_sel_hi:[1,1,1]
	v_pk_fma_f32 v[8:9], v[238:239], v[176:177], v[8:9] op_sel_hi:[0,1,1]
	v_pk_fma_f32 v[10:11], v[238:239], v[178:179], v[10:11] op_sel_hi:[0,1,1]
	v_pk_fma_f32 v[12:13], v[238:239], v[180:181], v[12:13] op_sel_hi:[0,1,1]
	v_pk_fma_f32 v[14:15], v[238:239], v[182:183], v[14:15] op_sel_hi:[0,1,1]
	v_pk_fma_f32 v[8:9], v[238:239], v[184:185], v[8:9] op_sel:[1,0,0] op_sel_hi:[1,1,1]
	v_pk_fma_f32 v[10:11], v[238:239], v[186:187], v[10:11] op_sel:[1,0,0] op_sel_hi:[1,1,1]
	v_pk_fma_f32 v[12:13], v[238:239], v[188:189], v[12:13] op_sel:[1,0,0] op_sel_hi:[1,1,1]
	v_pk_fma_f32 v[14:15], v[238:239], v[190:191], v[14:15] op_sel:[1,0,0] op_sel_hi:[1,1,1]
	v_lshlrev_b32_e32 v232, 16, v72
	v_and_b32_e32 v233, s15, v72
	v_lshlrev_b32_e32 v234, 16, v73
	v_and_b32_e32 v235, s15, v73
	v_lshlrev_b32_e32 v236, 16, v74
	v_and_b32_e32 v237, s15, v74
	v_lshlrev_b32_e32 v238, 16, v75
	v_and_b32_e32 v239, s15, v75
	v_pk_fma_f32 v[196:197], v[232:233], v[232:233], v[196:197]
	v_pk_fma_f32 v[196:197], v[234:235], v[234:235], v[196:197]
	v_pk_fma_f32 v[196:197], v[236:237], v[236:237], v[196:197]
	v_pk_fma_f32 v[196:197], v[238:239], v[238:239], v[196:197]
	v_pk_fma_f32 v[16:17], v[232:233], v[128:129], v[16:17] op_sel_hi:[0,1,1]
	v_pk_fma_f32 v[18:19], v[232:233], v[130:131], v[18:19] op_sel_hi:[0,1,1]
	v_pk_fma_f32 v[20:21], v[232:233], v[132:133], v[20:21] op_sel_hi:[0,1,1]
	v_pk_fma_f32 v[22:23], v[232:233], v[134:135], v[22:23] op_sel_hi:[0,1,1]
	v_pk_fma_f32 v[16:17], v[232:233], v[136:137], v[16:17] op_sel:[1,0,0] op_sel_hi:[1,1,1]
	v_pk_fma_f32 v[18:19], v[232:233], v[138:139], v[18:19] op_sel:[1,0,0] op_sel_hi:[1,1,1]
	v_pk_fma_f32 v[20:21], v[232:233], v[140:141], v[20:21] op_sel:[1,0,0] op_sel_hi:[1,1,1]
	v_pk_fma_f32 v[22:23], v[232:233], v[142:143], v[22:23] op_sel:[1,0,0] op_sel_hi:[1,1,1]
	v_pk_fma_f32 v[16:17], v[234:235], v[144:145], v[16:17] op_sel_hi:[0,1,1]
	v_pk_fma_f32 v[18:19], v[234:235], v[146:147], v[18:19] op_sel_hi:[0,1,1]
	v_pk_fma_f32 v[20:21], v[234:235], v[148:149], v[20:21] op_sel_hi:[0,1,1]
	v_pk_fma_f32 v[22:23], v[234:235], v[150:151], v[22:23] op_sel_hi:[0,1,1]
; #define LAS __attribute__((address_space(3)))
; __global__ void __launch_bounds__(NTHR, 2) fwd_kernel(Args args) {
;     ...
;             for (int i = 0; i < 16; ++i) { const int k = 2 * lane + 128 * i; f32x2 rv[8]; unsigned xw[8];
; #pragma unroll
;                 for (int e = 0; e < 8; ++e) rv[e] = *(const LAS f32x2*)(Rg + e * DM + k);
; #pragma unroll
;                 for (int q = 0; q < 8; ++q) xw[q] = *(const unsigned*)(XB + (size_t)(t0 + q) * DM + k);
; #pragma unroll
;                 for (int q = 0; q < 8; ++q) { const float x0 = bflo(xw[q]), x1 = bfhi(xw[q]); ssq[q] += x0 * x0 + x1 * x1;
; #pragma unroll
;                     for (int e = 0; e < 8; ++e) acc[q][e] += x0 * rv[e].x + x1 * rv[e].y; } }
	v_pk_fma_f32 v[16:17], v[234:235], v[152:153], v[16:17] op_sel:[1,0,0] op_sel_hi:[1,1,1]
	v_pk_fma_f32 v[18:19], v[234:235], v[154:155], v[18:19] op_sel:[1,0,0] op_sel_hi:[1,1,1]
	v_pk_fma_f32 v[20:21], v[234:235], v[156:157], v[20:21] op_sel:[1,0,0] op_sel_hi:[1,1,1]
	v_pk_fma_f32 v[22:23], v[234:235], v[158:159], v[22:23] op_sel:[1,0,0] op_sel_hi:[1,1,1]
	v_pk_fma_f32 v[16:17], v[236:237], v[160:161], v[16:17] op_sel_hi:[0,1,1]
	v_pk_fma_f32 v[18:19], v[236:237], v[162:163], v[18:19] op_sel_hi:[0,1,1]
	v_pk_fma_f32 v[20:21], v[236:237], v[164:165], v[20:21] op_sel_hi:[0,1,1]
	v_pk_fma_f32 v[22:23], v[236:237], v[166:167], v[22:23] op_sel_hi:[0,1,1]
	v_pk_fma_f32 v[16:17], v[236:237], v[168:169], v[16:17] op_sel:[1,0,0] op_sel_hi:[1,1,1]
	v_pk_fma_f32 v[18:19], v[236:237], v[170:171], v[18:19] op_sel:[1,0,0] op_sel_hi:[1,1,1]
	v_pk_fma_f32 v[20:21], v[236:237], v[172:173], v[20:21] op_sel:[1,0,0] op_sel_hi:[1,1,1]
	v_pk_fma_f32 v[22:23], v[236:237], v[174:175], v[22:23] op_sel:[1,0,0] op_sel_hi:[1,1,1]
	v_pk_fma_f32 v[16:17], v[238:239], v[176:177], v[16:17] op_sel_hi:[0,1,1]
	v_pk_fma_f32 v[18:19], v[238:239], v[178:179], v[18:19] op_sel_hi:[0,1,1]
	v_pk_fma_f32 v[20:21], v[238:239], v[180:181], v[20:21] op_sel_hi:[0,1,1]
	v_pk_fma_f32 v[22:23], v[238:239], v[182:183], v[22:23] op_sel_hi:[0,1,1]
	v_pk_fma_f32 v[16:17], v[238:239], v[184:185], v[16:17] op_sel:[1,0,0] op_sel_hi:[1,1,1]
	v_pk_fma_f32 v[18:19], v[238:239], v[186:187], v[18:19] op_sel:[1,0,0] op_sel_hi:[1,1,1]
	v_pk_fma_f32 v[20:21], v[238:239], v[188:189], v[20:21] op_sel:[1,0,0] op_sel_hi:[1,1,1]
	v_pk_fma_f32 v[22:23], v[238:239], v[190:191], v[22:23] op_sel:[1,0,0] op_sel_hi:[1,1,1]
	v_lshlrev_b32_e32 v232, 16, v76
	v_and_b32_e32 v233, s15, v76
	v_lshlrev_b32_e32 v234, 16, v77
	v_and_b32_e32 v235, s15, v77
	v_lshlrev_b32_e32 v236, 16, v78
	v_and_b32_e32 v237, s15, v78
	v_lshlrev_b32_e32 v238, 16, v79
	v_and_b32_e32 v239, s15, v79
	v_pk_fma_f32 v[198:199], v[232:233], v[232:233], v[198:199]
	v_pk_fma_f32 v[198:199], v[234:235], v[234:235], v[198:199]
	v_pk_fma_f32 v[198:199], v[236:237], v[236:237], v[198:199]
	v_pk_fma_f32 v[198:199], v[238:239], v[238:239], v[198:199]
	v_pk_fma_f32 v[24:25], v[232:233], v[128:129], v[24:25] op_sel_hi:[0,1,1]
	v_pk_fma_f32 v[26:27], v[232:233], v[130:131], v[26:27] op_sel_hi:[0,1,1]
	v_pk_fma_f32 v[28:29], v[232:233], v[132:133], v[28:29] op_sel_hi:[0,1,1]
	v_pk_fma_f32 v[30:31], v[232:233], v[134:135], v[30:31] op_sel_hi:[0,1,1]
	v_pk_fma_f32 v[24:25], v[232:233], v[136:137], v[24:25] op_sel:[1,0,0] op_sel_hi:[1,1,1]
	v_pk_fma_f32 v[26:27], v[232:233], v[138:139], v[26:27] op_sel:[1,0,0] op_sel_hi:[1,1,1]
	v_pk_fma_f32 v[28:29], v[232:233], v[140:141], v[28:29] op_sel:[1,0,0] op_sel_hi:[1,1,1]
	v_pk_fma_f32 v[30:31], v[232:233], v[142:143], v[30:31] op_sel:[1,0,0] op_sel_hi:[1,1,1]
	v_pk_fma_f32 v[24:25], v[234:235], v[144:145], v[24:25] op_sel_hi:[0,1,1]
	v_pk_fma_f32 v[26:27], v[234:235], v[146:147], v[26:27] op_sel_hi:[0,1,1]
	v_pk_fma_f32 v[28:29], v[234:235], v[148:149], v[28:29] op_sel_hi:[0,1,1]
	v_pk_fma_f32 v[30:31], v[234:235], v[150:151], v[30:31] op_sel_hi:[0,1,1]
	v_pk_fma_f32 v[24:25], v[234:235], v[152:153], v[24:25] op_sel:[1,0,0] op_sel_hi:[1,1,1]
	v_pk_fma_f32 v[26:27], v[234:235], v[154:155], v[26:27] op_sel:[1,0,0] op_sel_hi:[1,1,1]
	v_pk_fma_f32 v[28:29], v[234:235], v[156:157], v[28:29] op_sel:[1,0,0] op_sel_hi:[1,1,1]
	v_pk_fma_f32 v[30:31], v[234:235], v[158:159], v[30:31] op_sel:[1,0,0] op_sel_hi:[1,1,1]
	v_pk_fma_f32 v[24:25], v[236:237], v[160:161], v[24:25] op_sel_hi:[0,1,1]
	v_pk_fma_f32 v[26:27], v[236:237], v[162:163], v[26:27] op_sel_hi:[0,1,1]
	v_pk_fma_f32 v[28:29], v[236:237], v[164:165], v[28:29] op_sel_hi:[0,1,1]
	v_pk_fma_f32 v[30:31], v[236:237], v[166:167], v[30:31] op_sel_hi:[0,1,1]
	v_pk_fma_f32 v[24:25], v[236:237], v[168:169], v[24:25] op_sel:[1,0,0] op_sel_hi:[1,1,1]
	v_pk_fma_f32 v[26:27], v[236:237], v[170:171], v[26:27] op_sel:[1,0,0] op_sel_hi:[1,1,1]
	v_pk_fma_f32 v[28:29], v[236:237], v[172:173], v[28:29] op_sel:[1,0,0] op_sel_hi:[1,1,1]
	v_pk_fma_f32 v[30:31], v[236:237], v[174:175], v[30:31] op_sel:[1,0,0] op_sel_hi:[1,1,1]
	v_pk_fma_f32 v[24:25], v[238:239], v[176:177], v[24:25] op_sel_hi:[0,1,1]
	v_pk_fma_f32 v[26:27], v[238:239], v[178:179], v[26:27] op_sel_hi:[0,1,1]
	v_pk_fma_f32 v[28:29], v[238:239], v[180:181], v[28:29] op_sel_hi:[0,1,1]
	v_pk_fma_f32 v[30:31], v[238:239], v[182:183], v[30:31] op_sel_hi:[0,1,1]
	v_pk_fma_f32 v[24:25], v[238:239], v[184:185], v[24:25] op_sel:[1,0,0] op_sel_hi:[1,1,1]
	v_pk_fma_f32 v[26:27], v[238:239], v[186:187], v[26:27] op_sel:[1,0,0] op_sel_hi:[1,1,1]
	v_pk_fma_f32 v[28:29], v[238:239], v[188:189], v[28:29] op_sel:[1,0,0] op_sel_hi:[1,1,1]
	v_pk_fma_f32 v[30:31], v[238:239], v[190:191], v[30:31] op_sel:[1,0,0] op_sel_hi:[1,1,1]
	v_lshlrev_b32_e32 v232, 16, v80
	v_and_b32_e32 v233, s15, v80
	v_lshlrev_b32_e32 v234, 16, v81
	v_and_b32_e32 v235, s15, v81
	v_lshlrev_b32_e32 v236, 16, v82
	v_and_b32_e32 v237, s15, v82
	v_lshlrev_b32_e32 v238, 16, v83
	v_and_b32_e32 v239, s15, v83
	v_pk_fma_f32 v[200:201], v[232:233], v[232:233], v[200:201]
	v_pk_fma_f32 v[200:201], v[234:235], v[234:235], v[200:201]
	v_pk_fma_f32 v[200:201], v[236:237], v[236:237], v[200:201]
	v_pk_fma_f32 v[200:201], v[238:239], v[238:239], v[200:201]
	v_pk_fma_f32 v[32:33], v[232:233], v[128:129], v[32:33] op_sel_hi:[0,1,1]
	v_pk_fma_f32 v[34:35], v[232:233], v[130:131], v[34:35] op_sel_hi:[0,1,1]
	v_pk_fma_f32 v[36:37], v[232:233], v[132:133], v[36:37] op_sel_hi:[0,1,1]
	v_pk_fma_f32 v[38:39], v[232:233], v[134:135], v[38:39] op_sel_hi:[0,1,1]
; #define LAS __attribute__((address_space(3)))
; __global__ void __launch_bounds__(NTHR, 2) fwd_kernel(Args args) {
;     ...
;             for (int i = 0; i < 16; ++i) { const int k = 2 * lane + 128 * i; f32x2 rv[8]; unsigned xw[8];
; #pragma unroll
;                 for (int e = 0; e < 8; ++e) rv[e] = *(const LAS f32x2*)(Rg + e * DM + k);
; #pragma unroll
;                 for (int q = 0; q < 8; ++q) xw[q] = *(const unsigned*)(XB + (size_t)(t0 + q) * DM + k);
; #pragma unroll
;                 for (int q = 0; q < 8; ++q) { const float x0 = bflo(xw[q]), x1 = bfhi(xw[q]); ssq[q] += x0 * x0 + x1 * x1;
; #pragma unroll
;                     for (int e = 0; e < 8; ++e) acc[q][e] += x0 * rv[e].x + x1 * rv[e].y; } }
	v_pk_fma_f32 v[32:33], v[232:233], v[136:137], v[32:33] op_sel:[1,0,0] op_sel_hi:[1,1,1]
	v_pk_fma_f32 v[34:35], v[232:233], v[138:139], v[34:35] op_sel:[1,0,0] op_sel_hi:[1,1,1]
	v_pk_fma_f32 v[36:37], v[232:233], v[140:141], v[36:37] op_sel:[1,0,0] op_sel_hi:[1,1,1]
	v_pk_fma_f32 v[38:39], v[232:233], v[142:143], v[38:39] op_sel:[1,0,0] op_sel_hi:[1,1,1]
	v_pk_fma_f32 v[32:33], v[234:235], v[144:145], v[32:33] op_sel_hi:[0,1,1]
	v_pk_fma_f32 v[34:35], v[234:235], v[146:147], v[34:35] op_sel_hi:[0,1,1]
	v_pk_fma_f32 v[36:37], v[234:235], v[148:149], v[36:37] op_sel_hi:[0,1,1]
	v_pk_fma_f32 v[38:39], v[234:235], v[150:151], v[38:39] op_sel_hi:[0,1,1]
	v_pk_fma_f32 v[32:33], v[234:235], v[152:153], v[32:33] op_sel:[1,0,0] op_sel_hi:[1,1,1]
	v_pk_fma_f32 v[34:35], v[234:235], v[154:155], v[34:35] op_sel:[1,0,0] op_sel_hi:[1,1,1]
	v_pk_fma_f32 v[36:37], v[234:235], v[156:157], v[36:37] op_sel:[1,0,0] op_sel_hi:[1,1,1]
	v_pk_fma_f32 v[38:39], v[234:235], v[158:159], v[38:39] op_sel:[1,0,0] op_sel_hi:[1,1,1]
	v_pk_fma_f32 v[32:33], v[236:237], v[160:161], v[32:33] op_sel_hi:[0,1,1]
	v_pk_fma_f32 v[34:35], v[236:237], v[162:163], v[34:35] op_sel_hi:[0,1,1]
	v_pk_fma_f32 v[36:37], v[236:237], v[164:165], v[36:37] op_sel_hi:[0,1,1]
	v_pk_fma_f32 v[38:39], v[236:237], v[166:167], v[38:39] op_sel_hi:[0,1,1]
	v_pk_fma_f32 v[32:33], v[236:237], v[168:169], v[32:33] op_sel:[1,0,0] op_sel_hi:[1,1,1]
	v_pk_fma_f32 v[34:35], v[236:237], v[170:171], v[34:35] op_sel:[1,0,0] op_sel_hi:[1,1,1]
	v_pk_fma_f32 v[36:37], v[236:237], v[172:173], v[36:37] op_sel:[1,0,0] op_sel_hi:[1,1,1]
	v_pk_fma_f32 v[38:39], v[236:237], v[174:175], v[38:39] op_sel:[1,0,0] op_sel_hi:[1,1,1]
	v_pk_fma_f32 v[32:33], v[238:239], v[176:177], v[32:33] op_sel_hi:[0,1,1]
	v_pk_fma_f32 v[34:35], v[238:239], v[178:179], v[34:35] op_sel_hi:[0,1,1]
	v_pk_fma_f32 v[36:37], v[238:239], v[180:181], v[36:37] op_sel_hi:[0,1,1]
	v_pk_fma_f32 v[38:39], v[238:239], v[182:183], v[38:39] op_sel_hi:[0,1,1]
	v_pk_fma_f32 v[32:33], v[238:239], v[184:185], v[32:33] op_sel:[1,0,0] op_sel_hi:[1,1,1]
	v_pk_fma_f32 v[34:35], v[238:239], v[186:187], v[34:35] op_sel:[1,0,0] op_sel_hi:[1,1,1]
	v_pk_fma_f32 v[36:37], v[238:239], v[188:189], v[36:37] op_sel:[1,0,0] op_sel_hi:[1,1,1]
	v_pk_fma_f32 v[38:39], v[238:239], v[190:191], v[38:39] op_sel:[1,0,0] op_sel_hi:[1,1,1]
	v_lshlrev_b32_e32 v232, 16, v84
	v_and_b32_e32 v233, s15, v84
	v_lshlrev_b32_e32 v234, 16, v85
	v_and_b32_e32 v235, s15, v85
	v_lshlrev_b32_e32 v236, 16, v86
	v_and_b32_e32 v237, s15, v86
	v_lshlrev_b32_e32 v238, 16, v87
	v_and_b32_e32 v239, s15, v87
	v_pk_fma_f32 v[202:203], v[232:233], v[232:233], v[202:203]
	v_pk_fma_f32 v[202:203], v[234:235], v[234:235], v[202:203]
	v_pk_fma_f32 v[202:203], v[236:237], v[236:237], v[202:203]
	v_pk_fma_f32 v[202:203], v[238:239], v[238:239], v[202:203]
	v_pk_fma_f32 v[40:41], v[232:233], v[128:129], v[40:41] op_sel_hi:[0,1,1]
	v_pk_fma_f32 v[42:43], v[232:233], v[130:131], v[42:43] op_sel_hi:[0,1,1]
	v_pk_fma_f32 v[44:45], v[232:233], v[132:133], v[44:45] op_sel_hi:[0,1,1]
	v_pk_fma_f32 v[46:47], v[232:233], v[134:135], v[46:47] op_sel_hi:[0,1,1]
	v_pk_fma_f32 v[40:41], v[232:233], v[136:137], v[40:41] op_sel:[1,0,0] op_sel_hi:[1,1,1]
	v_pk_fma_f32 v[42:43], v[232:233], v[138:139], v[42:43] op_sel:[1,0,0] op_sel_hi:[1,1,1]
	v_pk_fma_f32 v[44:45], v[232:233], v[140:141], v[44:45] op_sel:[1,0,0] op_sel_hi:[1,1,1]
	v_pk_fma_f32 v[46:47], v[232:233], v[142:143], v[46:47] op_sel:[1,0,0] op_sel_hi:[1,1,1]
	v_pk_fma_f32 v[40:41], v[234:235], v[144:145], v[40:41] op_sel_hi:[0,1,1]
	v_pk_fma_f32 v[42:43], v[234:235], v[146:147], v[42:43] op_sel_hi:[0,1,1]
	v_pk_fma_f32 v[44:45], v[234:235], v[148:149], v[44:45] op_sel_hi:[0,1,1]
	v_pk_fma_f32 v[46:47], v[234:235], v[150:151], v[46:47] op_sel_hi:[0,1,1]
	v_pk_fma_f32 v[40:41], v[234:235], v[152:153], v[40:41] op_sel:[1,0,0] op_sel_hi:[1,1,1]
	v_pk_fma_f32 v[42:43], v[234:235], v[154:155], v[42:43] op_sel:[1,0,0] op_sel_hi:[1,1,1]
	v_pk_fma_f32 v[44:45], v[234:235], v[156:157], v[44:45] op_sel:[1,0,0] op_sel_hi:[1,1,1]
	v_pk_fma_f32 v[46:47], v[234:235], v[158:159], v[46:47] op_sel:[1,0,0] op_sel_hi:[1,1,1]
	v_pk_fma_f32 v[40:41], v[236:237], v[160:161], v[40:41] op_sel_hi:[0,1,1]
	v_pk_fma_f32 v[42:43], v[236:237], v[162:163], v[42:43] op_sel_hi:[0,1,1]
	v_pk_fma_f32 v[44:45], v[236:237], v[164:165], v[44:45] op_sel_hi:[0,1,1]
	v_pk_fma_f32 v[46:47], v[236:237], v[166:167], v[46:47] op_sel_hi:[0,1,1]
	v_pk_fma_f32 v[40:41], v[236:237], v[168:169], v[40:41] op_sel:[1,0,0] op_sel_hi:[1,1,1]
	v_pk_fma_f32 v[42:43], v[236:237], v[170:171], v[42:43] op_sel:[1,0,0] op_sel_hi:[1,1,1]
	v_pk_fma_f32 v[44:45], v[236:237], v[172:173], v[44:45] op_sel:[1,0,0] op_sel_hi:[1,1,1]
	v_pk_fma_f32 v[46:47], v[236:237], v[174:175], v[46:47] op_sel:[1,0,0] op_sel_hi:[1,1,1]
	v_pk_fma_f32 v[40:41], v[238:239], v[176:177], v[40:41] op_sel_hi:[0,1,1]
	v_pk_fma_f32 v[42:43], v[238:239], v[178:179], v[42:43] op_sel_hi:[0,1,1]
	v_pk_fma_f32 v[44:45], v[238:239], v[180:181], v[44:45] op_sel_hi:[0,1,1]
	v_pk_fma_f32 v[46:47], v[238:239], v[182:183], v[46:47] op_sel_hi:[0,1,1]
	v_pk_fma_f32 v[40:41], v[238:239], v[184:185], v[40:41] op_sel:[1,0,0] op_sel_hi:[1,1,1]
	v_pk_fma_f32 v[42:43], v[238:239], v[186:187], v[42:43] op_sel:[1,0,0] op_sel_hi:[1,1,1]
	v_pk_fma_f32 v[44:45], v[238:239], v[188:189], v[44:45] op_sel:[1,0,0] op_sel_hi:[1,1,1]
	v_pk_fma_f32 v[46:47], v[238:239], v[190:191], v[46:47] op_sel:[1,0,0] op_sel_hi:[1,1,1]
	v_lshlrev_b32_e32 v232, 16, v88
	v_and_b32_e32 v233, s15, v88
	v_lshlrev_b32_e32 v234, 16, v89
	v_and_b32_e32 v235, s15, v89
	v_lshlrev_b32_e32 v236, 16, v90
; #define LAS __attribute__((address_space(3)))
; __global__ void __launch_bounds__(NTHR, 2) fwd_kernel(Args args) {
;     ...
;             for (int i = 0; i < 16; ++i) { const int k = 2 * lane + 128 * i; f32x2 rv[8]; unsigned xw[8];
; #pragma unroll
;                 for (int e = 0; e < 8; ++e) rv[e] = *(const LAS f32x2*)(Rg + e * DM + k);
; #pragma unroll
;                 for (int q = 0; q < 8; ++q) xw[q] = *(const unsigned*)(XB + (size_t)(t0 + q) * DM + k);
; #pragma unroll
;                 for (int q = 0; q < 8; ++q) { const float x0 = bflo(xw[q]), x1 = bfhi(xw[q]); ssq[q] += x0 * x0 + x1 * x1;
; #pragma unroll
;                     for (int e = 0; e < 8; ++e) acc[q][e] += x0 * rv[e].x + x1 * rv[e].y; } }
	v_and_b32_e32 v237, s15, v90
	v_lshlrev_b32_e32 v238, 16, v91
	v_and_b32_e32 v239, s15, v91
	v_pk_fma_f32 v[204:205], v[232:233], v[232:233], v[204:205]
	v_pk_fma_f32 v[204:205], v[234:235], v[234:235], v[204:205]
	v_pk_fma_f32 v[204:205], v[236:237], v[236:237], v[204:205]
	v_pk_fma_f32 v[204:205], v[238:239], v[238:239], v[204:205]
	v_pk_fma_f32 v[48:49], v[232:233], v[128:129], v[48:49] op_sel_hi:[0,1,1]
	v_pk_fma_f32 v[50:51], v[232:233], v[130:131], v[50:51] op_sel_hi:[0,1,1]
	v_pk_fma_f32 v[52:53], v[232:233], v[132:133], v[52:53] op_sel_hi:[0,1,1]
	v_pk_fma_f32 v[54:55], v[232:233], v[134:135], v[54:55] op_sel_hi:[0,1,1]
	v_pk_fma_f32 v[48:49], v[232:233], v[136:137], v[48:49] op_sel:[1,0,0] op_sel_hi:[1,1,1]
	v_pk_fma_f32 v[50:51], v[232:233], v[138:139], v[50:51] op_sel:[1,0,0] op_sel_hi:[1,1,1]
	v_pk_fma_f32 v[52:53], v[232:233], v[140:141], v[52:53] op_sel:[1,0,0] op_sel_hi:[1,1,1]
	v_pk_fma_f32 v[54:55], v[232:233], v[142:143], v[54:55] op_sel:[1,0,0] op_sel_hi:[1,1,1]
	v_pk_fma_f32 v[48:49], v[234:235], v[144:145], v[48:49] op_sel_hi:[0,1,1]
	v_pk_fma_f32 v[50:51], v[234:235], v[146:147], v[50:51] op_sel_hi:[0,1,1]
	v_pk_fma_f32 v[52:53], v[234:235], v[148:149], v[52:53] op_sel_hi:[0,1,1]
	v_pk_fma_f32 v[54:55], v[234:235], v[150:151], v[54:55] op_sel_hi:[0,1,1]
	v_pk_fma_f32 v[48:49], v[234:235], v[152:153], v[48:49] op_sel:[1,0,0] op_sel_hi:[1,1,1]
	v_pk_fma_f32 v[50:51], v[234:235], v[154:155], v[50:51] op_sel:[1,0,0] op_sel_hi:[1,1,1]
	v_pk_fma_f32 v[52:53], v[234:235], v[156:157], v[52:53] op_sel:[1,0,0] op_sel_hi:[1,1,1]
	v_pk_fma_f32 v[54:55], v[234:235], v[158:159], v[54:55] op_sel:[1,0,0] op_sel_hi:[1,1,1]
	v_pk_fma_f32 v[48:49], v[236:237], v[160:161], v[48:49] op_sel_hi:[0,1,1]
	v_pk_fma_f32 v[50:51], v[236:237], v[162:163], v[50:51] op_sel_hi:[0,1,1]
	v_pk_fma_f32 v[52:53], v[236:237], v[164:165], v[52:53] op_sel_hi:[0,1,1]
	v_pk_fma_f32 v[54:55], v[236:237], v[166:167], v[54:55] op_sel_hi:[0,1,1]
	v_pk_fma_f32 v[48:49], v[236:237], v[168:169], v[48:49] op_sel:[1,0,0] op_sel_hi:[1,1,1]
	v_pk_fma_f32 v[50:51], v[236:237], v[170:171], v[50:51] op_sel:[1,0,0] op_sel_hi:[1,1,1]
	v_pk_fma_f32 v[52:53], v[236:237], v[172:173], v[52:53] op_sel:[1,0,0] op_sel_hi:[1,1,1]
	v_pk_fma_f32 v[54:55], v[236:237], v[174:175], v[54:55] op_sel:[1,0,0] op_sel_hi:[1,1,1]
	v_pk_fma_f32 v[48:49], v[238:239], v[176:177], v[48:49] op_sel_hi:[0,1,1]
	v_pk_fma_f32 v[50:51], v[238:239], v[178:179], v[50:51] op_sel_hi:[0,1,1]
	v_pk_fma_f32 v[52:53], v[238:239], v[180:181], v[52:53] op_sel_hi:[0,1,1]
	v_pk_fma_f32 v[54:55], v[238:239], v[182:183], v[54:55] op_sel_hi:[0,1,1]
	v_pk_fma_f32 v[48:49], v[238:239], v[184:185], v[48:49] op_sel:[1,0,0] op_sel_hi:[1,1,1]
	v_pk_fma_f32 v[50:51], v[238:239], v[186:187], v[50:51] op_sel:[1,0,0] op_sel_hi:[1,1,1]
	v_pk_fma_f32 v[52:53], v[238:239], v[188:189], v[52:53] op_sel:[1,0,0] op_sel_hi:[1,1,1]
	v_pk_fma_f32 v[54:55], v[238:239], v[190:191], v[54:55] op_sel:[1,0,0] op_sel_hi:[1,1,1]
	v_lshlrev_b32_e32 v232, 16, v92
	v_and_b32_e32 v233, s15, v92
	v_lshlrev_b32_e32 v234, 16, v93
	v_and_b32_e32 v235, s15, v93
	v_lshlrev_b32_e32 v236, 16, v94
	v_and_b32_e32 v237, s15, v94
	v_lshlrev_b32_e32 v238, 16, v95
	v_and_b32_e32 v239, s15, v95
	v_pk_fma_f32 v[206:207], v[232:233], v[232:233], v[206:207]
	v_pk_fma_f32 v[206:207], v[234:235], v[234:235], v[206:207]
	v_pk_fma_f32 v[206:207], v[236:237], v[236:237], v[206:207]
	v_pk_fma_f32 v[206:207], v[238:239], v[238:239], v[206:207]
	v_pk_fma_f32 v[56:57], v[232:233], v[128:129], v[56:57] op_sel_hi:[0,1,1]
	v_pk_fma_f32 v[58:59], v[232:233], v[130:131], v[58:59] op_sel_hi:[0,1,1]
	v_pk_fma_f32 v[60:61], v[232:233], v[132:133], v[60:61] op_sel_hi:[0,1,1]
	v_pk_fma_f32 v[62:63], v[232:233], v[134:135], v[62:63] op_sel_hi:[0,1,1]
	v_pk_fma_f32 v[56:57], v[232:233], v[136:137], v[56:57] op_sel:[1,0,0] op_sel_hi:[1,1,1]
	v_pk_fma_f32 v[58:59], v[232:233], v[138:139], v[58:59] op_sel:[1,0,0] op_sel_hi:[1,1,1]
	v_pk_fma_f32 v[60:61], v[232:233], v[140:141], v[60:61] op_sel:[1,0,0] op_sel_hi:[1,1,1]
	v_pk_fma_f32 v[62:63], v[232:233], v[142:143], v[62:63] op_sel:[1,0,0] op_sel_hi:[1,1,1]
	v_pk_fma_f32 v[56:57], v[234:235], v[144:145], v[56:57] op_sel_hi:[0,1,1]
	v_pk_fma_f32 v[58:59], v[234:235], v[146:147], v[58:59] op_sel_hi:[0,1,1]
	v_pk_fma_f32 v[60:61], v[234:235], v[148:149], v[60:61] op_sel_hi:[0,1,1]
	v_pk_fma_f32 v[62:63], v[234:235], v[150:151], v[62:63] op_sel_hi:[0,1,1]
	v_pk_fma_f32 v[56:57], v[234:235], v[152:153], v[56:57] op_sel:[1,0,0] op_sel_hi:[1,1,1]
	v_pk_fma_f32 v[58:59], v[234:235], v[154:155], v[58:59] op_sel:[1,0,0] op_sel_hi:[1,1,1]
	v_pk_fma_f32 v[60:61], v[234:235], v[156:157], v[60:61] op_sel:[1,0,0] op_sel_hi:[1,1,1]
	v_pk_fma_f32 v[62:63], v[234:235], v[158:159], v[62:63] op_sel:[1,0,0] op_sel_hi:[1,1,1]
	v_pk_fma_f32 v[56:57], v[236:237], v[160:161], v[56:57] op_sel_hi:[0,1,1]
	v_pk_fma_f32 v[58:59], v[236:237], v[162:163], v[58:59] op_sel_hi:[0,1,1]
	v_pk_fma_f32 v[60:61], v[236:237], v[164:165], v[60:61] op_sel_hi:[0,1,1]
	v_pk_fma_f32 v[62:63], v[236:237], v[166:167], v[62:63] op_sel_hi:[0,1,1]
	v_pk_fma_f32 v[56:57], v[236:237], v[168:169], v[56:57] op_sel:[1,0,0] op_sel_hi:[1,1,1]
	v_pk_fma_f32 v[58:59], v[236:237], v[170:171], v[58:59] op_sel:[1,0,0] op_sel_hi:[1,1,1]
	v_pk_fma_f32 v[60:61], v[236:237], v[172:173], v[60:61] op_sel:[1,0,0] op_sel_hi:[1,1,1]
	v_pk_fma_f32 v[62:63], v[236:237], v[174:175], v[62:63] op_sel:[1,0,0] op_sel_hi:[1,1,1]
	v_pk_fma_f32 v[56:57], v[238:239], v[176:177], v[56:57] op_sel_hi:[0,1,1]
	v_pk_fma_f32 v[58:59], v[238:239], v[178:179], v[58:59] op_sel_hi:[0,1,1]
	v_pk_fma_f32 v[60:61], v[238:239], v[180:181], v[60:61] op_sel_hi:[0,1,1]
	v_pk_fma_f32 v[62:63], v[238:239], v[182:183], v[62:63] op_sel_hi:[0,1,1]
	v_pk_fma_f32 v[56:57], v[238:239], v[184:185], v[56:57] op_sel:[1,0,0] op_sel_hi:[1,1,1]
	v_pk_fma_f32 v[58:59], v[238:239], v[186:187], v[58:59] op_sel:[1,0,0] op_sel_hi:[1,1,1]
	v_pk_fma_f32 v[60:61], v[238:239], v[188:189], v[60:61] op_sel:[1,0,0] op_sel_hi:[1,1,1]
	v_pk_fma_f32 v[62:63], v[238:239], v[190:191], v[62:63] op_sel:[1,0,0] op_sel_hi:[1,1,1]
	ds_read_b128 v[128:131], v208 offset:49152
	ds_read_b128 v[132:135], v208 offset:50176
	ds_read_b128 v[136:139], v208 offset:51200
	ds_read_b128 v[140:143], v208 offset:52224
	ds_read_b128 v[144:147], v208 offset:53248
	ds_read_b128 v[148:151], v208 offset:54272
	ds_read_b128 v[152:155], v208 offset:55296
	ds_read_b128 v[156:159], v208 offset:56320
	ds_read_b128 v[160:163], v208 offset:57344
	ds_read_b128 v[164:167], v208 offset:58368
	ds_read_b128 v[168:171], v208 offset:59392
	ds_read_b128 v[172:175], v208 offset:60416
	ds_read_b128 v[176:179], v208 offset:61440
	ds_read_b128 v[180:183], v208 offset:62464
	ds_read_b128 v[184:187], v208 offset:63488
	ds_read_b128 v[188:191], v208 offset:64512
	s_waitcnt vmcnt(0)
; #define LAS __attribute__((address_space(3)))
; __global__ void __launch_bounds__(NTHR, 2) fwd_kernel(Args args) {
;     ...
;             for (int i = 0; i < 16; ++i) { const int k = 2 * lane + 128 * i; f32x2 rv[8]; unsigned xw[8];
; #pragma unroll
;                 for (int e = 0; e < 8; ++e) rv[e] = *(const LAS f32x2*)(Rg + e * DM + k);
; #pragma unroll
;                 for (int q = 0; q < 8; ++q) xw[q] = *(const unsigned*)(XB + (size_t)(t0 + q) * DM + k);
; #pragma unroll
;                 for (int q = 0; q < 8; ++q) { const float x0 = bflo(xw[q]), x1 = bfhi(xw[q]); ssq[q] += x0 * x0 + x1 * x1;
; #pragma unroll
;                     for (int e = 0; e < 8; ++e) acc[q][e] += x0 * rv[e].x + x1 * rv[e].y; } }
	s_waitcnt lgkmcnt(0)
	v_lshlrev_b32_e32 v232, 16, v96
	v_and_b32_e32 v233, s15, v96
	v_lshlrev_b32_e32 v234, 16, v97
	v_and_b32_e32 v235, s15, v97
	v_lshlrev_b32_e32 v236, 16, v98
	v_and_b32_e32 v237, s15, v98
	v_lshlrev_b32_e32 v238, 16, v99
	v_and_b32_e32 v239, s15, v99
	v_pk_fma_f32 v[192:193], v[232:233], v[232:233], v[192:193]
	v_pk_fma_f32 v[192:193], v[234:235], v[234:235], v[192:193]
	v_pk_fma_f32 v[192:193], v[236:237], v[236:237], v[192:193]
	v_pk_fma_f32 v[192:193], v[238:239], v[238:239], v[192:193]
	v_pk_fma_f32 v[0:1], v[232:233], v[128:129], v[0:1] op_sel_hi:[0,1,1]
	v_pk_fma_f32 v[2:3], v[232:233], v[130:131], v[2:3] op_sel_hi:[0,1,1]
	v_pk_fma_f32 v[4:5], v[232:233], v[132:133], v[4:5] op_sel_hi:[0,1,1]
	v_pk_fma_f32 v[6:7], v[232:233], v[134:135], v[6:7] op_sel_hi:[0,1,1]
	v_pk_fma_f32 v[0:1], v[232:233], v[136:137], v[0:1] op_sel:[1,0,0] op_sel_hi:[1,1,1]
	v_pk_fma_f32 v[2:3], v[232:233], v[138:139], v[2:3] op_sel:[1,0,0] op_sel_hi:[1,1,1]
	v_pk_fma_f32 v[4:5], v[232:233], v[140:141], v[4:5] op_sel:[1,0,0] op_sel_hi:[1,1,1]
	v_pk_fma_f32 v[6:7], v[232:233], v[142:143], v[6:7] op_sel:[1,0,0] op_sel_hi:[1,1,1]
	v_pk_fma_f32 v[0:1], v[234:235], v[144:145], v[0:1] op_sel_hi:[0,1,1]
	v_pk_fma_f32 v[2:3], v[234:235], v[146:147], v[2:3] op_sel_hi:[0,1,1]
	v_pk_fma_f32 v[4:5], v[234:235], v[148:149], v[4:5] op_sel_hi:[0,1,1]
	v_pk_fma_f32 v[6:7], v[234:235], v[150:151], v[6:7] op_sel_hi:[0,1,1]
	v_pk_fma_f32 v[0:1], v[234:235], v[152:153], v[0:1] op_sel:[1,0,0] op_sel_hi:[1,1,1]
	v_pk_fma_f32 v[2:3], v[234:235], v[154:155], v[2:3] op_sel:[1,0,0] op_sel_hi:[1,1,1]
	v_pk_fma_f32 v[4:5], v[234:235], v[156:157], v[4:5] op_sel:[1,0,0] op_sel_hi:[1,1,1]
	v_pk_fma_f32 v[6:7], v[234:235], v[158:159], v[6:7] op_sel:[1,0,0] op_sel_hi:[1,1,1]
	v_pk_fma_f32 v[0:1], v[236:237], v[160:161], v[0:1] op_sel_hi:[0,1,1]
	v_pk_fma_f32 v[2:3], v[236:237], v[162:163], v[2:3] op_sel_hi:[0,1,1]
	v_pk_fma_f32 v[4:5], v[236:237], v[164:165], v[4:5] op_sel_hi:[0,1,1]
	v_pk_fma_f32 v[6:7], v[236:237], v[166:167], v[6:7] op_sel_hi:[0,1,1]
	v_pk_fma_f32 v[0:1], v[236:237], v[168:169], v[0:1] op_sel:[1,0,0] op_sel_hi:[1,1,1]
	v_pk_fma_f32 v[2:3], v[236:237], v[170:171], v[2:3] op_sel:[1,0,0] op_sel_hi:[1,1,1]
	v_pk_fma_f32 v[4:5], v[236:237], v[172:173], v[4:5] op_sel:[1,0,0] op_sel_hi:[1,1,1]
	v_pk_fma_f32 v[6:7], v[236:237], v[174:175], v[6:7] op_sel:[1,0,0] op_sel_hi:[1,1,1]
	v_pk_fma_f32 v[0:1], v[238:239], v[176:177], v[0:1] op_sel_hi:[0,1,1]
	v_pk_fma_f32 v[2:3], v[238:239], v[178:179], v[2:3] op_sel_hi:[0,1,1]
	v_pk_fma_f32 v[4:5], v[238:239], v[180:181], v[4:5] op_sel_hi:[0,1,1]
	v_pk_fma_f32 v[6:7], v[238:239], v[182:183], v[6:7] op_sel_hi:[0,1,1]
	v_pk_fma_f32 v[0:1], v[238:239], v[184:185], v[0:1] op_sel:[1,0,0] op_sel_hi:[1,1,1]
	v_pk_fma_f32 v[2:3], v[238:239], v[186:187], v[2:3] op_sel:[1,0,0] op_sel_hi:[1,1,1]
	v_pk_fma_f32 v[4:5], v[238:239], v[188:189], v[4:5] op_sel:[1,0,0] op_sel_hi:[1,1,1]
	v_pk_fma_f32 v[6:7], v[238:239], v[190:191], v[6:7] op_sel:[1,0,0] op_sel_hi:[1,1,1]
	v_lshlrev_b32_e32 v232, 16, v100
	v_and_b32_e32 v233, s15, v100
	v_lshlrev_b32_e32 v234, 16, v101
	v_and_b32_e32 v235, s15, v101
	v_lshlrev_b32_e32 v236, 16, v102
	v_and_b32_e32 v237, s15, v102
	v_lshlrev_b32_e32 v238, 16, v103
	v_and_b32_e32 v239, s15, v103
	v_pk_fma_f32 v[194:195], v[232:233], v[232:233], v[194:195]
	v_pk_fma_f32 v[194:195], v[234:235], v[234:235], v[194:195]
	v_pk_fma_f32 v[194:195], v[236:237], v[236:237], v[194:195]
	v_pk_fma_f32 v[194:195], v[238:239], v[238:239], v[194:195]
	v_pk_fma_f32 v[8:9], v[232:233], v[128:129], v[8:9] op_sel_hi:[0,1,1]
	v_pk_fma_f32 v[10:11], v[232:233], v[130:131], v[10:11] op_sel_hi:[0,1,1]
	v_pk_fma_f32 v[12:13], v[232:233], v[132:133], v[12:13] op_sel_hi:[0,1,1]
	v_pk_fma_f32 v[14:15], v[232:233], v[134:135], v[14:15] op_sel_hi:[0,1,1]
	v_pk_fma_f32 v[8:9], v[232:233], v[136:137], v[8:9] op_sel:[1,0,0] op_sel_hi:[1,1,1]
	v_pk_fma_f32 v[10:11], v[232:233], v[138:139], v[10:11] op_sel:[1,0,0] op_sel_hi:[1,1,1]
	v_pk_fma_f32 v[12:13], v[232:233], v[140:141], v[12:13] op_sel:[1,0,0] op_sel_hi:[1,1,1]
	v_pk_fma_f32 v[14:15], v[232:233], v[142:143], v[14:15] op_sel:[1,0,0] op_sel_hi:[1,1,1]
	v_pk_fma_f32 v[8:9], v[234:235], v[144:145], v[8:9] op_sel_hi:[0,1,1]
	v_pk_fma_f32 v[10:11], v[234:235], v[146:147], v[10:11] op_sel_hi:[0,1,1]
	v_pk_fma_f32 v[12:13], v[234:235], v[148:149], v[12:13] op_sel_hi:[0,1,1]
	v_pk_fma_f32 v[14:15], v[234:235], v[150:151], v[14:15] op_sel_hi:[0,1,1]
	v_pk_fma_f32 v[8:9], v[234:235], v[152:153], v[8:9] op_sel:[1,0,0] op_sel_hi:[1,1,1]
	v_pk_fma_f32 v[10:11], v[234:235], v[154:155], v[10:11] op_sel:[1,0,0] op_sel_hi:[1,1,1]
	v_pk_fma_f32 v[12:13], v[234:235], v[156:157], v[12:13] op_sel:[1,0,0] op_sel_hi:[1,1,1]
	v_pk_fma_f32 v[14:15], v[234:235], v[158:159], v[14:15] op_sel:[1,0,0] op_sel_hi:[1,1,1]
	v_pk_fma_f32 v[8:9], v[236:237], v[160:161], v[8:9] op_sel_hi:[0,1,1]
	v_pk_fma_f32 v[10:11], v[236:237], v[162:163], v[10:11] op_sel_hi:[0,1,1]
	v_pk_fma_f32 v[12:13], v[236:237], v[164:165], v[12:13] op_sel_hi:[0,1,1]
	v_pk_fma_f32 v[14:15], v[236:237], v[166:167], v[14:15] op_sel_hi:[0,1,1]
	v_pk_fma_f32 v[8:9], v[236:237], v[168:169], v[8:9] op_sel:[1,0,0] op_sel_hi:[1,1,1]
	v_pk_fma_f32 v[10:11], v[236:237], v[170:171], v[10:11] op_sel:[1,0,0] op_sel_hi:[1,1,1]
	v_pk_fma_f32 v[12:13], v[236:237], v[172:173], v[12:13] op_sel:[1,0,0] op_sel_hi:[1,1,1]
	v_pk_fma_f32 v[14:15], v[236:237], v[174:175], v[14:15] op_sel:[1,0,0] op_sel_hi:[1,1,1]
	v_pk_fma_f32 v[8:9], v[238:239], v[176:177], v[8:9] op_sel_hi:[0,1,1]
	v_pk_fma_f32 v[10:11], v[238:239], v[178:179], v[10:11] op_sel_hi:[0,1,1]
; #define LAS __attribute__((address_space(3)))
; __global__ void __launch_bounds__(NTHR, 2) fwd_kernel(Args args) {
;     ...
;             for (int i = 0; i < 16; ++i) { const int k = 2 * lane + 128 * i; f32x2 rv[8]; unsigned xw[8];
; #pragma unroll
;                 for (int e = 0; e < 8; ++e) rv[e] = *(const LAS f32x2*)(Rg + e * DM + k);
; #pragma unroll
;                 for (int q = 0; q < 8; ++q) xw[q] = *(const unsigned*)(XB + (size_t)(t0 + q) * DM + k);
; #pragma unroll
;                 for (int q = 0; q < 8; ++q) { const float x0 = bflo(xw[q]), x1 = bfhi(xw[q]); ssq[q] += x0 * x0 + x1 * x1;
; #pragma unroll
;                     for (int e = 0; e < 8; ++e) acc[q][e] += x0 * rv[e].x + x1 * rv[e].y; } }
	v_pk_fma_f32 v[12:13], v[238:239], v[180:181], v[12:13] op_sel_hi:[0,1,1]
	v_pk_fma_f32 v[14:15], v[238:239], v[182:183], v[14:15] op_sel_hi:[0,1,1]
	v_pk_fma_f32 v[8:9], v[238:239], v[184:185], v[8:9] op_sel:[1,0,0] op_sel_hi:[1,1,1]
	v_pk_fma_f32 v[10:11], v[238:239], v[186:187], v[10:11] op_sel:[1,0,0] op_sel_hi:[1,1,1]
	v_pk_fma_f32 v[12:13], v[238:239], v[188:189], v[12:13] op_sel:[1,0,0] op_sel_hi:[1,1,1]
	v_pk_fma_f32 v[14:15], v[238:239], v[190:191], v[14:15] op_sel:[1,0,0] op_sel_hi:[1,1,1]
	v_lshlrev_b32_e32 v232, 16, v104
	v_and_b32_e32 v233, s15, v104
	v_lshlrev_b32_e32 v234, 16, v105
	v_and_b32_e32 v235, s15, v105
	v_lshlrev_b32_e32 v236, 16, v106
	v_and_b32_e32 v237, s15, v106
	v_lshlrev_b32_e32 v238, 16, v107
	v_and_b32_e32 v239, s15, v107
	v_pk_fma_f32 v[196:197], v[232:233], v[232:233], v[196:197]
	v_pk_fma_f32 v[196:197], v[234:235], v[234:235], v[196:197]
	v_pk_fma_f32 v[196:197], v[236:237], v[236:237], v[196:197]
	v_pk_fma_f32 v[196:197], v[238:239], v[238:239], v[196:197]
	v_pk_fma_f32 v[16:17], v[232:233], v[128:129], v[16:17] op_sel_hi:[0,1,1]
	v_pk_fma_f32 v[18:19], v[232:233], v[130:131], v[18:19] op_sel_hi:[0,1,1]
	v_pk_fma_f32 v[20:21], v[232:233], v[132:133], v[20:21] op_sel_hi:[0,1,1]
	v_pk_fma_f32 v[22:23], v[232:233], v[134:135], v[22:23] op_sel_hi:[0,1,1]
	v_pk_fma_f32 v[16:17], v[232:233], v[136:137], v[16:17] op_sel:[1,0,0] op_sel_hi:[1,1,1]
	v_pk_fma_f32 v[18:19], v[232:233], v[138:139], v[18:19] op_sel:[1,0,0] op_sel_hi:[1,1,1]
	v_pk_fma_f32 v[20:21], v[232:233], v[140:141], v[20:21] op_sel:[1,0,0] op_sel_hi:[1,1,1]
	v_pk_fma_f32 v[22:23], v[232:233], v[142:143], v[22:23] op_sel:[1,0,0] op_sel_hi:[1,1,1]
	v_pk_fma_f32 v[16:17], v[234:235], v[144:145], v[16:17] op_sel_hi:[0,1,1]
	v_pk_fma_f32 v[18:19], v[234:235], v[146:147], v[18:19] op_sel_hi:[0,1,1]
	v_pk_fma_f32 v[20:21], v[234:235], v[148:149], v[20:21] op_sel_hi:[0,1,1]
	v_pk_fma_f32 v[22:23], v[234:235], v[150:151], v[22:23] op_sel_hi:[0,1,1]
	v_pk_fma_f32 v[16:17], v[234:235], v[152:153], v[16:17] op_sel:[1,0,0] op_sel_hi:[1,1,1]
	v_pk_fma_f32 v[18:19], v[234:235], v[154:155], v[18:19] op_sel:[1,0,0] op_sel_hi:[1,1,1]
	v_pk_fma_f32 v[20:21], v[234:235], v[156:157], v[20:21] op_sel:[1,0,0] op_sel_hi:[1,1,1]
	v_pk_fma_f32 v[22:23], v[234:235], v[158:159], v[22:23] op_sel:[1,0,0] op_sel_hi:[1,1,1]
	v_pk_fma_f32 v[16:17], v[236:237], v[160:161], v[16:17] op_sel_hi:[0,1,1]
	v_pk_fma_f32 v[18:19], v[236:237], v[162:163], v[18:19] op_sel_hi:[0,1,1]
	v_pk_fma_f32 v[20:21], v[236:237], v[164:165], v[20:21] op_sel_hi:[0,1,1]
	v_pk_fma_f32 v[22:23], v[236:237], v[166:167], v[22:23] op_sel_hi:[0,1,1]
	v_pk_fma_f32 v[16:17], v[236:237], v[168:169], v[16:17] op_sel:[1,0,0] op_sel_hi:[1,1,1]
	v_pk_fma_f32 v[18:19], v[236:237], v[170:171], v[18:19] op_sel:[1,0,0] op_sel_hi:[1,1,1]
	v_pk_fma_f32 v[20:21], v[236:237], v[172:173], v[20:21] op_sel:[1,0,0] op_sel_hi:[1,1,1]
	v_pk_fma_f32 v[22:23], v[236:237], v[174:175], v[22:23] op_sel:[1,0,0] op_sel_hi:[1,1,1]
	v_pk_fma_f32 v[16:17], v[238:239], v[176:177], v[16:17] op_sel_hi:[0,1,1]
	v_pk_fma_f32 v[18:19], v[238:239], v[178:179], v[18:19] op_sel_hi:[0,1,1]
	v_pk_fma_f32 v[20:21], v[238:239], v[180:181], v[20:21] op_sel_hi:[0,1,1]
	v_pk_fma_f32 v[22:23], v[238:239], v[182:183], v[22:23] op_sel_hi:[0,1,1]
	v_pk_fma_f32 v[16:17], v[238:239], v[184:185], v[16:17] op_sel:[1,0,0] op_sel_hi:[1,1,1]
	v_pk_fma_f32 v[18:19], v[238:239], v[186:187], v[18:19] op_sel:[1,0,0] op_sel_hi:[1,1,1]
	v_pk_fma_f32 v[20:21], v[238:239], v[188:189], v[20:21] op_sel:[1,0,0] op_sel_hi:[1,1,1]
	v_pk_fma_f32 v[22:23], v[238:239], v[190:191], v[22:23] op_sel:[1,0,0] op_sel_hi:[1,1,1]
	v_lshlrev_b32_e32 v232, 16, v108
	v_and_b32_e32 v233, s15, v108
	v_lshlrev_b32_e32 v234, 16, v109
	v_and_b32_e32 v235, s15, v109
	v_lshlrev_b32_e32 v236, 16, v110
	v_and_b32_e32 v237, s15, v110
	v_lshlrev_b32_e32 v238, 16, v111
	v_and_b32_e32 v239, s15, v111
	v_pk_fma_f32 v[198:199], v[232:233], v[232:233], v[198:199]
	v_pk_fma_f32 v[198:199], v[234:235], v[234:235], v[198:199]
	v_pk_fma_f32 v[198:199], v[236:237], v[236:237], v[198:199]
	v_pk_fma_f32 v[198:199], v[238:239], v[238:239], v[198:199]
	v_pk_fma_f32 v[24:25], v[232:233], v[128:129], v[24:25] op_sel_hi:[0,1,1]
	v_pk_fma_f32 v[26:27], v[232:233], v[130:131], v[26:27] op_sel_hi:[0,1,1]
	v_pk_fma_f32 v[28:29], v[232:233], v[132:133], v[28:29] op_sel_hi:[0,1,1]
	v_pk_fma_f32 v[30:31], v[232:233], v[134:135], v[30:31] op_sel_hi:[0,1,1]
	v_pk_fma_f32 v[24:25], v[232:233], v[136:137], v[24:25] op_sel:[1,0,0] op_sel_hi:[1,1,1]
	v_pk_fma_f32 v[26:27], v[232:233], v[138:139], v[26:27] op_sel:[1,0,0] op_sel_hi:[1,1,1]
	v_pk_fma_f32 v[28:29], v[232:233], v[140:141], v[28:29] op_sel:[1,0,0] op_sel_hi:[1,1,1]
	v_pk_fma_f32 v[30:31], v[232:233], v[142:143], v[30:31] op_sel:[1,0,0] op_sel_hi:[1,1,1]
	v_pk_fma_f32 v[24:25], v[234:235], v[144:145], v[24:25] op_sel_hi:[0,1,1]
	v_pk_fma_f32 v[26:27], v[234:235], v[146:147], v[26:27] op_sel_hi:[0,1,1]
	v_pk_fma_f32 v[28:29], v[234:235], v[148:149], v[28:29] op_sel_hi:[0,1,1]
	v_pk_fma_f32 v[30:31], v[234:235], v[150:151], v[30:31] op_sel_hi:[0,1,1]
	v_pk_fma_f32 v[24:25], v[234:235], v[152:153], v[24:25] op_sel:[1,0,0] op_sel_hi:[1,1,1]
	v_pk_fma_f32 v[26:27], v[234:235], v[154:155], v[26:27] op_sel:[1,0,0] op_sel_hi:[1,1,1]
	v_pk_fma_f32 v[28:29], v[234:235], v[156:157], v[28:29] op_sel:[1,0,0] op_sel_hi:[1,1,1]
	v_pk_fma_f32 v[30:31], v[234:235], v[158:159], v[30:31] op_sel:[1,0,0] op_sel_hi:[1,1,1]
	v_pk_fma_f32 v[24:25], v[236:237], v[160:161], v[24:25] op_sel_hi:[0,1,1]
	v_pk_fma_f32 v[26:27], v[236:237], v[162:163], v[26:27] op_sel_hi:[0,1,1]
; #define LAS __attribute__((address_space(3)))
; __global__ void __launch_bounds__(NTHR, 2) fwd_kernel(Args args) {
;     ...
;             for (int i = 0; i < 16; ++i) { const int k = 2 * lane + 128 * i; f32x2 rv[8]; unsigned xw[8];
; #pragma unroll
;                 for (int e = 0; e < 8; ++e) rv[e] = *(const LAS f32x2*)(Rg + e * DM + k);
; #pragma unroll
;                 for (int q = 0; q < 8; ++q) xw[q] = *(const unsigned*)(XB + (size_t)(t0 + q) * DM + k);
; #pragma unroll
;                 for (int q = 0; q < 8; ++q) { const float x0 = bflo(xw[q]), x1 = bfhi(xw[q]); ssq[q] += x0 * x0 + x1 * x1;
; #pragma unroll
;                     for (int e = 0; e < 8; ++e) acc[q][e] += x0 * rv[e].x + x1 * rv[e].y; } }
	v_pk_fma_f32 v[28:29], v[236:237], v[164:165], v[28:29] op_sel_hi:[0,1,1]
	v_pk_fma_f32 v[30:31], v[236:237], v[166:167], v[30:31] op_sel_hi:[0,1,1]
	v_pk_fma_f32 v[24:25], v[236:237], v[168:169], v[24:25] op_sel:[1,0,0] op_sel_hi:[1,1,1]
	v_pk_fma_f32 v[26:27], v[236:237], v[170:171], v[26:27] op_sel:[1,0,0] op_sel_hi:[1,1,1]
	v_pk_fma_f32 v[28:29], v[236:237], v[172:173], v[28:29] op_sel:[1,0,0] op_sel_hi:[1,1,1]
	v_pk_fma_f32 v[30:31], v[236:237], v[174:175], v[30:31] op_sel:[1,0,0] op_sel_hi:[1,1,1]
	v_pk_fma_f32 v[24:25], v[238:239], v[176:177], v[24:25] op_sel_hi:[0,1,1]
	v_pk_fma_f32 v[26:27], v[238:239], v[178:179], v[26:27] op_sel_hi:[0,1,1]
	v_pk_fma_f32 v[28:29], v[238:239], v[180:181], v[28:29] op_sel_hi:[0,1,1]
	v_pk_fma_f32 v[30:31], v[238:239], v[182:183], v[30:31] op_sel_hi:[0,1,1]
	v_pk_fma_f32 v[24:25], v[238:239], v[184:185], v[24:25] op_sel:[1,0,0] op_sel_hi:[1,1,1]
	v_pk_fma_f32 v[26:27], v[238:239], v[186:187], v[26:27] op_sel:[1,0,0] op_sel_hi:[1,1,1]
	v_pk_fma_f32 v[28:29], v[238:239], v[188:189], v[28:29] op_sel:[1,0,0] op_sel_hi:[1,1,1]
	v_pk_fma_f32 v[30:31], v[238:239], v[190:191], v[30:31] op_sel:[1,0,0] op_sel_hi:[1,1,1]
	v_lshlrev_b32_e32 v232, 16, v112
	v_and_b32_e32 v233, s15, v112
	v_lshlrev_b32_e32 v234, 16, v113
	v_and_b32_e32 v235, s15, v113
	v_lshlrev_b32_e32 v236, 16, v114
	v_and_b32_e32 v237, s15, v114
	v_lshlrev_b32_e32 v238, 16, v115
	v_and_b32_e32 v239, s15, v115
	v_pk_fma_f32 v[200:201], v[232:233], v[232:233], v[200:201]
	v_pk_fma_f32 v[200:201], v[234:235], v[234:235], v[200:201]
	v_pk_fma_f32 v[200:201], v[236:237], v[236:237], v[200:201]
	v_pk_fma_f32 v[200:201], v[238:239], v[238:239], v[200:201]
	v_pk_fma_f32 v[32:33], v[232:233], v[128:129], v[32:33] op_sel_hi:[0,1,1]
	v_pk_fma_f32 v[34:35], v[232:233], v[130:131], v[34:35] op_sel_hi:[0,1,1]
	v_pk_fma_f32 v[36:37], v[232:233], v[132:133], v[36:37] op_sel_hi:[0,1,1]
	v_pk_fma_f32 v[38:39], v[232:233], v[134:135], v[38:39] op_sel_hi:[0,1,1]
	v_pk_fma_f32 v[32:33], v[232:233], v[136:137], v[32:33] op_sel:[1,0,0] op_sel_hi:[1,1,1]
	v_pk_fma_f32 v[34:35], v[232:233], v[138:139], v[34:35] op_sel:[1,0,0] op_sel_hi:[1,1,1]
	v_pk_fma_f32 v[36:37], v[232:233], v[140:141], v[36:37] op_sel:[1,0,0] op_sel_hi:[1,1,1]
	v_pk_fma_f32 v[38:39], v[232:233], v[142:143], v[38:39] op_sel:[1,0,0] op_sel_hi:[1,1,1]
	v_pk_fma_f32 v[32:33], v[234:235], v[144:145], v[32:33] op_sel_hi:[0,1,1]
	v_pk_fma_f32 v[34:35], v[234:235], v[146:147], v[34:35] op_sel_hi:[0,1,1]
	v_pk_fma_f32 v[36:37], v[234:235], v[148:149], v[36:37] op_sel_hi:[0,1,1]
	v_pk_fma_f32 v[38:39], v[234:235], v[150:151], v[38:39] op_sel_hi:[0,1,1]
	v_pk_fma_f32 v[32:33], v[234:235], v[152:153], v[32:33] op_sel:[1,0,0] op_sel_hi:[1,1,1]
	v_pk_fma_f32 v[34:35], v[234:235], v[154:155], v[34:35] op_sel:[1,0,0] op_sel_hi:[1,1,1]
	v_pk_fma_f32 v[36:37], v[234:235], v[156:157], v[36:37] op_sel:[1,0,0] op_sel_hi:[1,1,1]
	v_pk_fma_f32 v[38:39], v[234:235], v[158:159], v[38:39] op_sel:[1,0,0] op_sel_hi:[1,1,1]
	v_pk_fma_f32 v[32:33], v[236:237], v[160:161], v[32:33] op_sel_hi:[0,1,1]
	v_pk_fma_f32 v[34:35], v[236:237], v[162:163], v[34:35] op_sel_hi:[0,1,1]
	v_pk_fma_f32 v[36:37], v[236:237], v[164:165], v[36:37] op_sel_hi:[0,1,1]
	v_pk_fma_f32 v[38:39], v[236:237], v[166:167], v[38:39] op_sel_hi:[0,1,1]
	v_pk_fma_f32 v[32:33], v[236:237], v[168:169], v[32:33] op_sel:[1,0,0] op_sel_hi:[1,1,1]
	v_pk_fma_f32 v[34:35], v[236:237], v[170:171], v[34:35] op_sel:[1,0,0] op_sel_hi:[1,1,1]
	v_pk_fma_f32 v[36:37], v[236:237], v[172:173], v[36:37] op_sel:[1,0,0] op_sel_hi:[1,1,1]
	v_pk_fma_f32 v[38:39], v[236:237], v[174:175], v[38:39] op_sel:[1,0,0] op_sel_hi:[1,1,1]
	v_pk_fma_f32 v[32:33], v[238:239], v[176:177], v[32:33] op_sel_hi:[0,1,1]
	v_pk_fma_f32 v[34:35], v[238:239], v[178:179], v[34:35] op_sel_hi:[0,1,1]
	v_pk_fma_f32 v[36:37], v[238:239], v[180:181], v[36:37] op_sel_hi:[0,1,1]
	v_pk_fma_f32 v[38:39], v[238:239], v[182:183], v[38:39] op_sel_hi:[0,1,1]
	v_pk_fma_f32 v[32:33], v[238:239], v[184:185], v[32:33] op_sel:[1,0,0] op_sel_hi:[1,1,1]
	v_pk_fma_f32 v[34:35], v[238:239], v[186:187], v[34:35] op_sel:[1,0,0] op_sel_hi:[1,1,1]
	v_pk_fma_f32 v[36:37], v[238:239], v[188:189], v[36:37] op_sel:[1,0,0] op_sel_hi:[1,1,1]
	v_pk_fma_f32 v[38:39], v[238:239], v[190:191], v[38:39] op_sel:[1,0,0] op_sel_hi:[1,1,1]
	v_lshlrev_b32_e32 v232, 16, v116
	v_and_b32_e32 v233, s15, v116
	v_lshlrev_b32_e32 v234, 16, v117
	v_and_b32_e32 v235, s15, v117
	v_lshlrev_b32_e32 v236, 16, v118
	v_and_b32_e32 v237, s15, v118
	v_lshlrev_b32_e32 v238, 16, v119
	v_and_b32_e32 v239, s15, v119
	v_pk_fma_f32 v[202:203], v[232:233], v[232:233], v[202:203]
	v_pk_fma_f32 v[202:203], v[234:235], v[234:235], v[202:203]
	v_pk_fma_f32 v[202:203], v[236:237], v[236:237], v[202:203]
	v_pk_fma_f32 v[202:203], v[238:239], v[238:239], v[202:203]
	v_pk_fma_f32 v[40:41], v[232:233], v[128:129], v[40:41] op_sel_hi:[0,1,1]
	v_pk_fma_f32 v[42:43], v[232:233], v[130:131], v[42:43] op_sel_hi:[0,1,1]
	v_pk_fma_f32 v[44:45], v[232:233], v[132:133], v[44:45] op_sel_hi:[0,1,1]
	v_pk_fma_f32 v[46:47], v[232:233], v[134:135], v[46:47] op_sel_hi:[0,1,1]
	v_pk_fma_f32 v[40:41], v[232:233], v[136:137], v[40:41] op_sel:[1,0,0] op_sel_hi:[1,1,1]
	v_pk_fma_f32 v[42:43], v[232:233], v[138:139], v[42:43] op_sel:[1,0,0] op_sel_hi:[1,1,1]
	v_pk_fma_f32 v[44:45], v[232:233], v[140:141], v[44:45] op_sel:[1,0,0] op_sel_hi:[1,1,1]
	v_pk_fma_f32 v[46:47], v[232:233], v[142:143], v[46:47] op_sel:[1,0,0] op_sel_hi:[1,1,1]
	v_pk_fma_f32 v[40:41], v[234:235], v[144:145], v[40:41] op_sel_hi:[0,1,1]
	v_pk_fma_f32 v[42:43], v[234:235], v[146:147], v[42:43] op_sel_hi:[0,1,1]
; #define LAS __attribute__((address_space(3)))
; __global__ void __launch_bounds__(NTHR, 2) fwd_kernel(Args args) {
;     ...
;             for (int i = 0; i < 16; ++i) { const int k = 2 * lane + 128 * i; f32x2 rv[8]; unsigned xw[8];
; #pragma unroll
;                 for (int e = 0; e < 8; ++e) rv[e] = *(const LAS f32x2*)(Rg + e * DM + k);
; #pragma unroll
;                 for (int q = 0; q < 8; ++q) xw[q] = *(const unsigned*)(XB + (size_t)(t0 + q) * DM + k);
; #pragma unroll
;                 for (int q = 0; q < 8; ++q) { const float x0 = bflo(xw[q]), x1 = bfhi(xw[q]); ssq[q] += x0 * x0 + x1 * x1;
; #pragma unroll
;                     for (int e = 0; e < 8; ++e) acc[q][e] += x0 * rv[e].x + x1 * rv[e].y; } }
	v_pk_fma_f32 v[44:45], v[234:235], v[148:149], v[44:45] op_sel_hi:[0,1,1]
	v_pk_fma_f32 v[46:47], v[234:235], v[150:151], v[46:47] op_sel_hi:[0,1,1]
	v_pk_fma_f32 v[40:41], v[234:235], v[152:153], v[40:41] op_sel:[1,0,0] op_sel_hi:[1,1,1]
	v_pk_fma_f32 v[42:43], v[234:235], v[154:155], v[42:43] op_sel:[1,0,0] op_sel_hi:[1,1,1]
	v_pk_fma_f32 v[44:45], v[234:235], v[156:157], v[44:45] op_sel:[1,0,0] op_sel_hi:[1,1,1]
	v_pk_fma_f32 v[46:47], v[234:235], v[158:159], v[46:47] op_sel:[1,0,0] op_sel_hi:[1,1,1]
	v_pk_fma_f32 v[40:41], v[236:237], v[160:161], v[40:41] op_sel_hi:[0,1,1]
	v_pk_fma_f32 v[42:43], v[236:237], v[162:163], v[42:43] op_sel_hi:[0,1,1]
	v_pk_fma_f32 v[44:45], v[236:237], v[164:165], v[44:45] op_sel_hi:[0,1,1]
	v_pk_fma_f32 v[46:47], v[236:237], v[166:167], v[46:47] op_sel_hi:[0,1,1]
	v_pk_fma_f32 v[40:41], v[236:237], v[168:169], v[40:41] op_sel:[1,0,0] op_sel_hi:[1,1,1]
	v_pk_fma_f32 v[42:43], v[236:237], v[170:171], v[42:43] op_sel:[1,0,0] op_sel_hi:[1,1,1]
	v_pk_fma_f32 v[44:45], v[236:237], v[172:173], v[44:45] op_sel:[1,0,0] op_sel_hi:[1,1,1]
	v_pk_fma_f32 v[46:47], v[236:237], v[174:175], v[46:47] op_sel:[1,0,0] op_sel_hi:[1,1,1]
	v_pk_fma_f32 v[40:41], v[238:239], v[176:177], v[40:41] op_sel_hi:[0,1,1]
	v_pk_fma_f32 v[42:43], v[238:239], v[178:179], v[42:43] op_sel_hi:[0,1,1]
	v_pk_fma_f32 v[44:45], v[238:239], v[180:181], v[44:45] op_sel_hi:[0,1,1]
	v_pk_fma_f32 v[46:47], v[238:239], v[182:183], v[46:47] op_sel_hi:[0,1,1]
	v_pk_fma_f32 v[40:41], v[238:239], v[184:185], v[40:41] op_sel:[1,0,0] op_sel_hi:[1,1,1]
	v_pk_fma_f32 v[42:43], v[238:239], v[186:187], v[42:43] op_sel:[1,0,0] op_sel_hi:[1,1,1]
	v_pk_fma_f32 v[44:45], v[238:239], v[188:189], v[44:45] op_sel:[1,0,0] op_sel_hi:[1,1,1]
	v_pk_fma_f32 v[46:47], v[238:239], v[190:191], v[46:47] op_sel:[1,0,0] op_sel_hi:[1,1,1]
	v_lshlrev_b32_e32 v232, 16, v120
	v_and_b32_e32 v233, s15, v120
	v_lshlrev_b32_e32 v234, 16, v121
	v_and_b32_e32 v235, s15, v121
	v_lshlrev_b32_e32 v236, 16, v122
	v_and_b32_e32 v237, s15, v122
	v_lshlrev_b32_e32 v238, 16, v123
	v_and_b32_e32 v239, s15, v123
	v_pk_fma_f32 v[204:205], v[232:233], v[232:233], v[204:205]
	v_pk_fma_f32 v[204:205], v[234:235], v[234:235], v[204:205]
	v_pk_fma_f32 v[204:205], v[236:237], v[236:237], v[204:205]
	v_pk_fma_f32 v[204:205], v[238:239], v[238:239], v[204:205]
	v_pk_fma_f32 v[48:49], v[232:233], v[128:129], v[48:49] op_sel_hi:[0,1,1]
	v_pk_fma_f32 v[50:51], v[232:233], v[130:131], v[50:51] op_sel_hi:[0,1,1]
	v_pk_fma_f32 v[52:53], v[232:233], v[132:133], v[52:53] op_sel_hi:[0,1,1]
	v_pk_fma_f32 v[54:55], v[232:233], v[134:135], v[54:55] op_sel_hi:[0,1,1]
	v_pk_fma_f32 v[48:49], v[232:233], v[136:137], v[48:49] op_sel:[1,0,0] op_sel_hi:[1,1,1]
	v_pk_fma_f32 v[50:51], v[232:233], v[138:139], v[50:51] op_sel:[1,0,0] op_sel_hi:[1,1,1]
	v_pk_fma_f32 v[52:53], v[232:233], v[140:141], v[52:53] op_sel:[1,0,0] op_sel_hi:[1,1,1]
	v_pk_fma_f32 v[54:55], v[232:233], v[142:143], v[54:55] op_sel:[1,0,0] op_sel_hi:[1,1,1]
	v_pk_fma_f32 v[48:49], v[234:235], v[144:145], v[48:49] op_sel_hi:[0,1,1]
	v_pk_fma_f32 v[50:51], v[234:235], v[146:147], v[50:51] op_sel_hi:[0,1,1]
	v_pk_fma_f32 v[52:53], v[234:235], v[148:149], v[52:53] op_sel_hi:[0,1,1]
	v_pk_fma_f32 v[54:55], v[234:235], v[150:151], v[54:55] op_sel_hi:[0,1,1]
	v_pk_fma_f32 v[48:49], v[234:235], v[152:153], v[48:49] op_sel:[1,0,0] op_sel_hi:[1,1,1]
	v_pk_fma_f32 v[50:51], v[234:235], v[154:155], v[50:51] op_sel:[1,0,0] op_sel_hi:[1,1,1]
	v_pk_fma_f32 v[52:53], v[234:235], v[156:157], v[52:53] op_sel:[1,0,0] op_sel_hi:[1,1,1]
	v_pk_fma_f32 v[54:55], v[234:235], v[158:159], v[54:55] op_sel:[1,0,0] op_sel_hi:[1,1,1]
	v_pk_fma_f32 v[48:49], v[236:237], v[160:161], v[48:49] op_sel_hi:[0,1,1]
	v_pk_fma_f32 v[50:51], v[236:237], v[162:163], v[50:51] op_sel_hi:[0,1,1]
	v_pk_fma_f32 v[52:53], v[236:237], v[164:165], v[52:53] op_sel_hi:[0,1,1]
	v_pk_fma_f32 v[54:55], v[236:237], v[166:167], v[54:55] op_sel_hi:[0,1,1]
	v_pk_fma_f32 v[48:49], v[236:237], v[168:169], v[48:49] op_sel:[1,0,0] op_sel_hi:[1,1,1]
	v_pk_fma_f32 v[50:51], v[236:237], v[170:171], v[50:51] op_sel:[1,0,0] op_sel_hi:[1,1,1]
	v_pk_fma_f32 v[52:53], v[236:237], v[172:173], v[52:53] op_sel:[1,0,0] op_sel_hi:[1,1,1]
	v_pk_fma_f32 v[54:55], v[236:237], v[174:175], v[54:55] op_sel:[1,0,0] op_sel_hi:[1,1,1]
	v_pk_fma_f32 v[48:49], v[238:239], v[176:177], v[48:49] op_sel_hi:[0,1,1]
	v_pk_fma_f32 v[50:51], v[238:239], v[178:179], v[50:51] op_sel_hi:[0,1,1]
	v_pk_fma_f32 v[52:53], v[238:239], v[180:181], v[52:53] op_sel_hi:[0,1,1]
	v_pk_fma_f32 v[54:55], v[238:239], v[182:183], v[54:55] op_sel_hi:[0,1,1]
	v_pk_fma_f32 v[48:49], v[238:239], v[184:185], v[48:49] op_sel:[1,0,0] op_sel_hi:[1,1,1]
	v_pk_fma_f32 v[50:51], v[238:239], v[186:187], v[50:51] op_sel:[1,0,0] op_sel_hi:[1,1,1]
	v_pk_fma_f32 v[52:53], v[238:239], v[188:189], v[52:53] op_sel:[1,0,0] op_sel_hi:[1,1,1]
	v_pk_fma_f32 v[54:55], v[238:239], v[190:191], v[54:55] op_sel:[1,0,0] op_sel_hi:[1,1,1]
	v_lshlrev_b32_e32 v232, 16, v124
	v_and_b32_e32 v233, s15, v124
	v_lshlrev_b32_e32 v234, 16, v125
	v_and_b32_e32 v235, s15, v125
	v_lshlrev_b32_e32 v236, 16, v126
	v_and_b32_e32 v237, s15, v126
	v_lshlrev_b32_e32 v238, 16, v127
	v_and_b32_e32 v239, s15, v127
	v_pk_fma_f32 v[206:207], v[232:233], v[232:233], v[206:207]
	v_pk_fma_f32 v[206:207], v[234:235], v[234:235], v[206:207]
	v_pk_fma_f32 v[206:207], v[236:237], v[236:237], v[206:207]
	v_pk_fma_f32 v[206:207], v[238:239], v[238:239], v[206:207]
	v_pk_fma_f32 v[56:57], v[232:233], v[128:129], v[56:57] op_sel_hi:[0,1,1]
	v_pk_fma_f32 v[58:59], v[232:233], v[130:131], v[58:59] op_sel_hi:[0,1,1]
; #define LAS __attribute__((address_space(3)))
; __global__ void __launch_bounds__(NTHR, 2) fwd_kernel(Args args) {
;     ...
;             for (int i = 0; i < 16; ++i) { const int k = 2 * lane + 128 * i; f32x2 rv[8]; unsigned xw[8];
; #pragma unroll
;                 for (int e = 0; e < 8; ++e) rv[e] = *(const LAS f32x2*)(Rg + e * DM + k);
; #pragma unroll
;                 for (int q = 0; q < 8; ++q) xw[q] = *(const unsigned*)(XB + (size_t)(t0 + q) * DM + k);
; #pragma unroll
;                 for (int q = 0; q < 8; ++q) { const float x0 = bflo(xw[q]), x1 = bfhi(xw[q]); ssq[q] += x0 * x0 + x1 * x1;
; #pragma unroll
;                     for (int e = 0; e < 8; ++e) acc[q][e] += x0 * rv[e].x + x1 * rv[e].y; } }
; #pragma unroll
;             for (int q = 0; q < 8; ++q) { const float sq = wave_sum(ssq[q]); const float rs = 1.0f / sqrtf(sq * (1.0f / DM) + EPS);
;                 float lg[8];
; #pragma unroll
;                 for (int e = 0; e < 8; ++e) lg[e] = wave_sum(acc[q][e]) * rs;
	v_pk_fma_f32 v[60:61], v[232:233], v[132:133], v[60:61] op_sel_hi:[0,1,1]
	v_pk_fma_f32 v[62:63], v[232:233], v[134:135], v[62:63] op_sel_hi:[0,1,1]
	v_pk_fma_f32 v[56:57], v[232:233], v[136:137], v[56:57] op_sel:[1,0,0] op_sel_hi:[1,1,1]
	v_pk_fma_f32 v[58:59], v[232:233], v[138:139], v[58:59] op_sel:[1,0,0] op_sel_hi:[1,1,1]
	v_pk_fma_f32 v[60:61], v[232:233], v[140:141], v[60:61] op_sel:[1,0,0] op_sel_hi:[1,1,1]
	v_pk_fma_f32 v[62:63], v[232:233], v[142:143], v[62:63] op_sel:[1,0,0] op_sel_hi:[1,1,1]
	v_pk_fma_f32 v[56:57], v[234:235], v[144:145], v[56:57] op_sel_hi:[0,1,1]
	v_pk_fma_f32 v[58:59], v[234:235], v[146:147], v[58:59] op_sel_hi:[0,1,1]
	v_pk_fma_f32 v[60:61], v[234:235], v[148:149], v[60:61] op_sel_hi:[0,1,1]
	v_pk_fma_f32 v[62:63], v[234:235], v[150:151], v[62:63] op_sel_hi:[0,1,1]
	v_pk_fma_f32 v[56:57], v[234:235], v[152:153], v[56:57] op_sel:[1,0,0] op_sel_hi:[1,1,1]
	v_pk_fma_f32 v[58:59], v[234:235], v[154:155], v[58:59] op_sel:[1,0,0] op_sel_hi:[1,1,1]
	v_pk_fma_f32 v[60:61], v[234:235], v[156:157], v[60:61] op_sel:[1,0,0] op_sel_hi:[1,1,1]
	v_pk_fma_f32 v[62:63], v[234:235], v[158:159], v[62:63] op_sel:[1,0,0] op_sel_hi:[1,1,1]
	v_pk_fma_f32 v[56:57], v[236:237], v[160:161], v[56:57] op_sel_hi:[0,1,1]
	v_pk_fma_f32 v[58:59], v[236:237], v[162:163], v[58:59] op_sel_hi:[0,1,1]
	v_pk_fma_f32 v[60:61], v[236:237], v[164:165], v[60:61] op_sel_hi:[0,1,1]
	v_pk_fma_f32 v[62:63], v[236:237], v[166:167], v[62:63] op_sel_hi:[0,1,1]
	v_pk_fma_f32 v[56:57], v[236:237], v[168:169], v[56:57] op_sel:[1,0,0] op_sel_hi:[1,1,1]
	v_pk_fma_f32 v[58:59], v[236:237], v[170:171], v[58:59] op_sel:[1,0,0] op_sel_hi:[1,1,1]
	v_pk_fma_f32 v[60:61], v[236:237], v[172:173], v[60:61] op_sel:[1,0,0] op_sel_hi:[1,1,1]
	v_pk_fma_f32 v[62:63], v[236:237], v[174:175], v[62:63] op_sel:[1,0,0] op_sel_hi:[1,1,1]
	v_pk_fma_f32 v[56:57], v[238:239], v[176:177], v[56:57] op_sel_hi:[0,1,1]
	v_pk_fma_f32 v[58:59], v[238:239], v[178:179], v[58:59] op_sel_hi:[0,1,1]
	v_pk_fma_f32 v[60:61], v[238:239], v[180:181], v[60:61] op_sel_hi:[0,1,1]
	v_pk_fma_f32 v[62:63], v[238:239], v[182:183], v[62:63] op_sel_hi:[0,1,1]
	v_pk_fma_f32 v[56:57], v[238:239], v[184:185], v[56:57] op_sel:[1,0,0] op_sel_hi:[1,1,1]
	v_pk_fma_f32 v[58:59], v[238:239], v[186:187], v[58:59] op_sel:[1,0,0] op_sel_hi:[1,1,1]
	v_pk_fma_f32 v[60:61], v[238:239], v[188:189], v[60:61] op_sel:[1,0,0] op_sel_hi:[1,1,1]
	v_pk_fma_f32 v[62:63], v[238:239], v[190:191], v[62:63] op_sel:[1,0,0] op_sel_hi:[1,1,1]
	v_add_f32_e32 v192, v192, v193
	v_add_f32_e32 v194, v194, v195
	v_add_f32_e32 v196, v196, v197
	v_add_f32_e32 v198, v198, v199
	v_add_f32_e32 v200, v200, v201
	v_add_f32_e32 v202, v202, v203
	v_add_f32_e32 v204, v204, v205
	v_add_f32_e32 v206, v206, v207
	v_add_f32_dpp v0, v0, v0 quad_perm:[1,0,3,2] row_mask:0xf bank_mask:0xf
	v_add_f32_dpp v1, v1, v1 quad_perm:[1,0,3,2] row_mask:0xf bank_mask:0xf
	v_add_f32_dpp v2, v2, v2 quad_perm:[1,0,3,2] row_mask:0xf bank_mask:0xf
	v_add_f32_dpp v3, v3, v3 quad_perm:[1,0,3,2] row_mask:0xf bank_mask:0xf
	v_add_f32_dpp v4, v4, v4 quad_perm:[1,0,3,2] row_mask:0xf bank_mask:0xf
	v_add_f32_dpp v5, v5, v5 quad_perm:[1,0,3,2] row_mask:0xf bank_mask:0xf
	v_add_f32_dpp v6, v6, v6 quad_perm:[1,0,3,2] row_mask:0xf bank_mask:0xf
	v_add_f32_dpp v7, v7, v7 quad_perm:[1,0,3,2] row_mask:0xf bank_mask:0xf
	v_add_f32_dpp v8, v8, v8 quad_perm:[1,0,3,2] row_mask:0xf bank_mask:0xf
	v_add_f32_dpp v9, v9, v9 quad_perm:[1,0,3,2] row_mask:0xf bank_mask:0xf
	v_add_f32_dpp v10, v10, v10 quad_perm:[1,0,3,2] row_mask:0xf bank_mask:0xf
	v_add_f32_dpp v11, v11, v11 quad_perm:[1,0,3,2] row_mask:0xf bank_mask:0xf
	v_add_f32_dpp v12, v12, v12 quad_perm:[1,0,3,2] row_mask:0xf bank_mask:0xf
	v_add_f32_dpp v13, v13, v13 quad_perm:[1,0,3,2] row_mask:0xf bank_mask:0xf
	v_add_f32_dpp v14, v14, v14 quad_perm:[1,0,3,2] row_mask:0xf bank_mask:0xf
	v_add_f32_dpp v15, v15, v15 quad_perm:[1,0,3,2] row_mask:0xf bank_mask:0xf
	v_add_f32_dpp v16, v16, v16 quad_perm:[1,0,3,2] row_mask:0xf bank_mask:0xf
	v_add_f32_dpp v17, v17, v17 quad_perm:[1,0,3,2] row_mask:0xf bank_mask:0xf
	v_add_f32_dpp v18, v18, v18 quad_perm:[1,0,3,2] row_mask:0xf bank_mask:0xf
	v_add_f32_dpp v19, v19, v19 quad_perm:[1,0,3,2] row_mask:0xf bank_mask:0xf
	v_add_f32_dpp v20, v20, v20 quad_perm:[1,0,3,2] row_mask:0xf bank_mask:0xf
	v_add_f32_dpp v21, v21, v21 quad_perm:[1,0,3,2] row_mask:0xf bank_mask:0xf
	v_add_f32_dpp v22, v22, v22 quad_perm:[1,0,3,2] row_mask:0xf bank_mask:0xf
	v_add_f32_dpp v23, v23, v23 quad_perm:[1,0,3,2] row_mask:0xf bank_mask:0xf
	v_add_f32_dpp v24, v24, v24 quad_perm:[1,0,3,2] row_mask:0xf bank_mask:0xf
	v_add_f32_dpp v25, v25, v25 quad_perm:[1,0,3,2] row_mask:0xf bank_mask:0xf
	v_add_f32_dpp v26, v26, v26 quad_perm:[1,0,3,2] row_mask:0xf bank_mask:0xf
	v_add_f32_dpp v27, v27, v27 quad_perm:[1,0,3,2] row_mask:0xf bank_mask:0xf
	v_add_f32_dpp v28, v28, v28 quad_perm:[1,0,3,2] row_mask:0xf bank_mask:0xf
	v_add_f32_dpp v29, v29, v29 quad_perm:[1,0,3,2] row_mask:0xf bank_mask:0xf
	v_add_f32_dpp v30, v30, v30 quad_perm:[1,0,3,2] row_mask:0xf bank_mask:0xf
	v_add_f32_dpp v31, v31, v31 quad_perm:[1,0,3,2] row_mask:0xf bank_mask:0xf
	v_add_f32_dpp v32, v32, v32 quad_perm:[1,0,3,2] row_mask:0xf bank_mask:0xf
	v_add_f32_dpp v33, v33, v33 quad_perm:[1,0,3,2] row_mask:0xf bank_mask:0xf
	v_add_f32_dpp v34, v34, v34 quad_perm:[1,0,3,2] row_mask:0xf bank_mask:0xf
	v_add_f32_dpp v35, v35, v35 quad_perm:[1,0,3,2] row_mask:0xf bank_mask:0xf
	v_add_f32_dpp v36, v36, v36 quad_perm:[1,0,3,2] row_mask:0xf bank_mask:0xf
	v_add_f32_dpp v37, v37, v37 quad_perm:[1,0,3,2] row_mask:0xf bank_mask:0xf
; __global__ void __launch_bounds__(NTHR, 2) fwd_kernel(Args args) {
;     ...
;             for (int q = 0; q < 8; ++q) { const float sq = wave_sum(ssq[q]); const float rs = 1.0f / sqrtf(sq * (1.0f / DM) + EPS);
;                 float lg[8];
; #pragma unroll
;                 for (int e = 0; e < 8; ++e) lg[e] = wave_sum(acc[q][e]) * rs;
	v_add_f32_dpp v38, v38, v38 quad_perm:[1,0,3,2] row_mask:0xf bank_mask:0xf
	v_add_f32_dpp v39, v39, v39 quad_perm:[1,0,3,2] row_mask:0xf bank_mask:0xf
	v_add_f32_dpp v40, v40, v40 quad_perm:[1,0,3,2] row_mask:0xf bank_mask:0xf
	v_add_f32_dpp v41, v41, v41 quad_perm:[1,0,3,2] row_mask:0xf bank_mask:0xf
	v_add_f32_dpp v42, v42, v42 quad_perm:[1,0,3,2] row_mask:0xf bank_mask:0xf
	v_add_f32_dpp v43, v43, v43 quad_perm:[1,0,3,2] row_mask:0xf bank_mask:0xf
	v_add_f32_dpp v44, v44, v44 quad_perm:[1,0,3,2] row_mask:0xf bank_mask:0xf
	v_add_f32_dpp v45, v45, v45 quad_perm:[1,0,3,2] row_mask:0xf bank_mask:0xf
	v_add_f32_dpp v46, v46, v46 quad_perm:[1,0,3,2] row_mask:0xf bank_mask:0xf
	v_add_f32_dpp v47, v47, v47 quad_perm:[1,0,3,2] row_mask:0xf bank_mask:0xf
	v_add_f32_dpp v48, v48, v48 quad_perm:[1,0,3,2] row_mask:0xf bank_mask:0xf
	v_add_f32_dpp v49, v49, v49 quad_perm:[1,0,3,2] row_mask:0xf bank_mask:0xf
	v_add_f32_dpp v50, v50, v50 quad_perm:[1,0,3,2] row_mask:0xf bank_mask:0xf
	v_add_f32_dpp v51, v51, v51 quad_perm:[1,0,3,2] row_mask:0xf bank_mask:0xf
	v_add_f32_dpp v52, v52, v52 quad_perm:[1,0,3,2] row_mask:0xf bank_mask:0xf
	v_add_f32_dpp v53, v53, v53 quad_perm:[1,0,3,2] row_mask:0xf bank_mask:0xf
	v_add_f32_dpp v54, v54, v54 quad_perm:[1,0,3,2] row_mask:0xf bank_mask:0xf
	v_add_f32_dpp v55, v55, v55 quad_perm:[1,0,3,2] row_mask:0xf bank_mask:0xf
	v_add_f32_dpp v56, v56, v56 quad_perm:[1,0,3,2] row_mask:0xf bank_mask:0xf
	v_add_f32_dpp v57, v57, v57 quad_perm:[1,0,3,2] row_mask:0xf bank_mask:0xf
	v_add_f32_dpp v58, v58, v58 quad_perm:[1,0,3,2] row_mask:0xf bank_mask:0xf
	v_add_f32_dpp v59, v59, v59 quad_perm:[1,0,3,2] row_mask:0xf bank_mask:0xf
	v_add_f32_dpp v60, v60, v60 quad_perm:[1,0,3,2] row_mask:0xf bank_mask:0xf
	v_add_f32_dpp v61, v61, v61 quad_perm:[1,0,3,2] row_mask:0xf bank_mask:0xf
	v_add_f32_dpp v62, v62, v62 quad_perm:[1,0,3,2] row_mask:0xf bank_mask:0xf
	v_add_f32_dpp v63, v63, v63 quad_perm:[1,0,3,2] row_mask:0xf bank_mask:0xf
	v_add_f32_dpp v192, v192, v192 quad_perm:[1,0,3,2] row_mask:0xf bank_mask:0xf
	v_add_f32_dpp v194, v194, v194 quad_perm:[1,0,3,2] row_mask:0xf bank_mask:0xf
	v_add_f32_dpp v196, v196, v196 quad_perm:[1,0,3,2] row_mask:0xf bank_mask:0xf
	v_add_f32_dpp v198, v198, v198 quad_perm:[1,0,3,2] row_mask:0xf bank_mask:0xf
	v_add_f32_dpp v200, v200, v200 quad_perm:[1,0,3,2] row_mask:0xf bank_mask:0xf
	v_add_f32_dpp v202, v202, v202 quad_perm:[1,0,3,2] row_mask:0xf bank_mask:0xf
	v_add_f32_dpp v204, v204, v204 quad_perm:[1,0,3,2] row_mask:0xf bank_mask:0xf
	v_add_f32_dpp v206, v206, v206 quad_perm:[1,0,3,2] row_mask:0xf bank_mask:0xf
	v_add_f32_dpp v0, v0, v0 quad_perm:[2,3,0,1] row_mask:0xf bank_mask:0xf
	v_add_f32_dpp v1, v1, v1 quad_perm:[2,3,0,1] row_mask:0xf bank_mask:0xf
	v_add_f32_dpp v2, v2, v2 quad_perm:[2,3,0,1] row_mask:0xf bank_mask:0xf
	v_add_f32_dpp v3, v3, v3 quad_perm:[2,3,0,1] row_mask:0xf bank_mask:0xf
	v_add_f32_dpp v4, v4, v4 quad_perm:[2,3,0,1] row_mask:0xf bank_mask:0xf
	v_add_f32_dpp v5, v5, v5 quad_perm:[2,3,0,1] row_mask:0xf bank_mask:0xf
	v_add_f32_dpp v6, v6, v6 quad_perm:[2,3,0,1] row_mask:0xf bank_mask:0xf
	v_add_f32_dpp v7, v7, v7 quad_perm:[2,3,0,1] row_mask:0xf bank_mask:0xf
	v_add_f32_dpp v8, v8, v8 quad_perm:[2,3,0,1] row_mask:0xf bank_mask:0xf
	v_add_f32_dpp v9, v9, v9 quad_perm:[2,3,0,1] row_mask:0xf bank_mask:0xf
	v_add_f32_dpp v10, v10, v10 quad_perm:[2,3,0,1] row_mask:0xf bank_mask:0xf
	v_add_f32_dpp v11, v11, v11 quad_perm:[2,3,0,1] row_mask:0xf bank_mask:0xf
	v_add_f32_dpp v12, v12, v12 quad_perm:[2,3,0,1] row_mask:0xf bank_mask:0xf
	v_add_f32_dpp v13, v13, v13 quad_perm:[2,3,0,1] row_mask:0xf bank_mask:0xf
	v_add_f32_dpp v14, v14, v14 quad_perm:[2,3,0,1] row_mask:0xf bank_mask:0xf
	v_add_f32_dpp v15, v15, v15 quad_perm:[2,3,0,1] row_mask:0xf bank_mask:0xf
	v_add_f32_dpp v16, v16, v16 quad_perm:[2,3,0,1] row_mask:0xf bank_mask:0xf
	v_add_f32_dpp v17, v17, v17 quad_perm:[2,3,0,1] row_mask:0xf bank_mask:0xf
	v_add_f32_dpp v18, v18, v18 quad_perm:[2,3,0,1] row_mask:0xf bank_mask:0xf
	v_add_f32_dpp v19, v19, v19 quad_perm:[2,3,0,1] row_mask:0xf bank_mask:0xf
	v_add_f32_dpp v20, v20, v20 quad_perm:[2,3,0,1] row_mask:0xf bank_mask:0xf
	v_add_f32_dpp v21, v21, v21 quad_perm:[2,3,0,1] row_mask:0xf bank_mask:0xf
	v_add_f32_dpp v22, v22, v22 quad_perm:[2,3,0,1] row_mask:0xf bank_mask:0xf
	v_add_f32_dpp v23, v23, v23 quad_perm:[2,3,0,1] row_mask:0xf bank_mask:0xf
	v_add_f32_dpp v24, v24, v24 quad_perm:[2,3,0,1] row_mask:0xf bank_mask:0xf
	v_add_f32_dpp v25, v25, v25 quad_perm:[2,3,0,1] row_mask:0xf bank_mask:0xf
	v_add_f32_dpp v26, v26, v26 quad_perm:[2,3,0,1] row_mask:0xf bank_mask:0xf
	v_add_f32_dpp v27, v27, v27 quad_perm:[2,3,0,1] row_mask:0xf bank_mask:0xf
	v_add_f32_dpp v28, v28, v28 quad_perm:[2,3,0,1] row_mask:0xf bank_mask:0xf
	v_add_f32_dpp v29, v29, v29 quad_perm:[2,3,0,1] row_mask:0xf bank_mask:0xf
	v_add_f32_dpp v30, v30, v30 quad_perm:[2,3,0,1] row_mask:0xf bank_mask:0xf
	v_add_f32_dpp v31, v31, v31 quad_perm:[2,3,0,1] row_mask:0xf bank_mask:0xf
	v_add_f32_dpp v32, v32, v32 quad_perm:[2,3,0,1] row_mask:0xf bank_mask:0xf
	v_add_f32_dpp v33, v33, v33 quad_perm:[2,3,0,1] row_mask:0xf bank_mask:0xf
	v_add_f32_dpp v34, v34, v34 quad_perm:[2,3,0,1] row_mask:0xf bank_mask:0xf
	v_add_f32_dpp v35, v35, v35 quad_perm:[2,3,0,1] row_mask:0xf bank_mask:0xf
	v_add_f32_dpp v36, v36, v36 quad_perm:[2,3,0,1] row_mask:0xf bank_mask:0xf
	v_add_f32_dpp v37, v37, v37 quad_perm:[2,3,0,1] row_mask:0xf bank_mask:0xf
	v_add_f32_dpp v38, v38, v38 quad_perm:[2,3,0,1] row_mask:0xf bank_mask:0xf
	v_add_f32_dpp v39, v39, v39 quad_perm:[2,3,0,1] row_mask:0xf bank_mask:0xf
; __global__ void __launch_bounds__(NTHR, 2) fwd_kernel(Args args) {
;     ...
;             for (int q = 0; q < 8; ++q) { const float sq = wave_sum(ssq[q]); const float rs = 1.0f / sqrtf(sq * (1.0f / DM) + EPS);
;                 float lg[8];
; #pragma unroll
;                 for (int e = 0; e < 8; ++e) lg[e] = wave_sum(acc[q][e]) * rs;
	v_add_f32_dpp v40, v40, v40 quad_perm:[2,3,0,1] row_mask:0xf bank_mask:0xf
	v_add_f32_dpp v41, v41, v41 quad_perm:[2,3,0,1] row_mask:0xf bank_mask:0xf
	v_add_f32_dpp v42, v42, v42 quad_perm:[2,3,0,1] row_mask:0xf bank_mask:0xf
	v_add_f32_dpp v43, v43, v43 quad_perm:[2,3,0,1] row_mask:0xf bank_mask:0xf
	v_add_f32_dpp v44, v44, v44 quad_perm:[2,3,0,1] row_mask:0xf bank_mask:0xf
	v_add_f32_dpp v45, v45, v45 quad_perm:[2,3,0,1] row_mask:0xf bank_mask:0xf
	v_add_f32_dpp v46, v46, v46 quad_perm:[2,3,0,1] row_mask:0xf bank_mask:0xf
	v_add_f32_dpp v47, v47, v47 quad_perm:[2,3,0,1] row_mask:0xf bank_mask:0xf
	v_add_f32_dpp v48, v48, v48 quad_perm:[2,3,0,1] row_mask:0xf bank_mask:0xf
	v_add_f32_dpp v49, v49, v49 quad_perm:[2,3,0,1] row_mask:0xf bank_mask:0xf
	v_add_f32_dpp v50, v50, v50 quad_perm:[2,3,0,1] row_mask:0xf bank_mask:0xf
	v_add_f32_dpp v51, v51, v51 quad_perm:[2,3,0,1] row_mask:0xf bank_mask:0xf
	v_add_f32_dpp v52, v52, v52 quad_perm:[2,3,0,1] row_mask:0xf bank_mask:0xf
	v_add_f32_dpp v53, v53, v53 quad_perm:[2,3,0,1] row_mask:0xf bank_mask:0xf
	v_add_f32_dpp v54, v54, v54 quad_perm:[2,3,0,1] row_mask:0xf bank_mask:0xf
	v_add_f32_dpp v55, v55, v55 quad_perm:[2,3,0,1] row_mask:0xf bank_mask:0xf
	v_add_f32_dpp v56, v56, v56 quad_perm:[2,3,0,1] row_mask:0xf bank_mask:0xf
	v_add_f32_dpp v57, v57, v57 quad_perm:[2,3,0,1] row_mask:0xf bank_mask:0xf
	v_add_f32_dpp v58, v58, v58 quad_perm:[2,3,0,1] row_mask:0xf bank_mask:0xf
	v_add_f32_dpp v59, v59, v59 quad_perm:[2,3,0,1] row_mask:0xf bank_mask:0xf
	v_add_f32_dpp v60, v60, v60 quad_perm:[2,3,0,1] row_mask:0xf bank_mask:0xf
	v_add_f32_dpp v61, v61, v61 quad_perm:[2,3,0,1] row_mask:0xf bank_mask:0xf
	v_add_f32_dpp v62, v62, v62 quad_perm:[2,3,0,1] row_mask:0xf bank_mask:0xf
	v_add_f32_dpp v63, v63, v63 quad_perm:[2,3,0,1] row_mask:0xf bank_mask:0xf
	v_add_f32_dpp v192, v192, v192 quad_perm:[2,3,0,1] row_mask:0xf bank_mask:0xf
	v_add_f32_dpp v194, v194, v194 quad_perm:[2,3,0,1] row_mask:0xf bank_mask:0xf
	v_add_f32_dpp v196, v196, v196 quad_perm:[2,3,0,1] row_mask:0xf bank_mask:0xf
	v_add_f32_dpp v198, v198, v198 quad_perm:[2,3,0,1] row_mask:0xf bank_mask:0xf
	v_add_f32_dpp v200, v200, v200 quad_perm:[2,3,0,1] row_mask:0xf bank_mask:0xf
	v_add_f32_dpp v202, v202, v202 quad_perm:[2,3,0,1] row_mask:0xf bank_mask:0xf
	v_add_f32_dpp v204, v204, v204 quad_perm:[2,3,0,1] row_mask:0xf bank_mask:0xf
	v_add_f32_dpp v206, v206, v206 quad_perm:[2,3,0,1] row_mask:0xf bank_mask:0xf
	v_add_f32_dpp v0, v0, v0 row_half_mirror row_mask:0xf bank_mask:0xf
	v_add_f32_dpp v1, v1, v1 row_half_mirror row_mask:0xf bank_mask:0xf
	v_add_f32_dpp v2, v2, v2 row_half_mirror row_mask:0xf bank_mask:0xf
	v_add_f32_dpp v3, v3, v3 row_half_mirror row_mask:0xf bank_mask:0xf
	v_add_f32_dpp v4, v4, v4 row_half_mirror row_mask:0xf bank_mask:0xf
	v_add_f32_dpp v5, v5, v5 row_half_mirror row_mask:0xf bank_mask:0xf
	v_add_f32_dpp v6, v6, v6 row_half_mirror row_mask:0xf bank_mask:0xf
	v_add_f32_dpp v7, v7, v7 row_half_mirror row_mask:0xf bank_mask:0xf
	v_add_f32_dpp v8, v8, v8 row_half_mirror row_mask:0xf bank_mask:0xf
	v_add_f32_dpp v9, v9, v9 row_half_mirror row_mask:0xf bank_mask:0xf
	v_add_f32_dpp v10, v10, v10 row_half_mirror row_mask:0xf bank_mask:0xf
	v_add_f32_dpp v11, v11, v11 row_half_mirror row_mask:0xf bank_mask:0xf
	v_add_f32_dpp v12, v12, v12 row_half_mirror row_mask:0xf bank_mask:0xf
	v_add_f32_dpp v13, v13, v13 row_half_mirror row_mask:0xf bank_mask:0xf
	v_add_f32_dpp v14, v14, v14 row_half_mirror row_mask:0xf bank_mask:0xf
	v_add_f32_dpp v15, v15, v15 row_half_mirror row_mask:0xf bank_mask:0xf
	v_add_f32_dpp v16, v16, v16 row_half_mirror row_mask:0xf bank_mask:0xf
	v_add_f32_dpp v17, v17, v17 row_half_mirror row_mask:0xf bank_mask:0xf
	v_add_f32_dpp v18, v18, v18 row_half_mirror row_mask:0xf bank_mask:0xf
	v_add_f32_dpp v19, v19, v19 row_half_mirror row_mask:0xf bank_mask:0xf
	v_add_f32_dpp v20, v20, v20 row_half_mirror row_mask:0xf bank_mask:0xf
	v_add_f32_dpp v21, v21, v21 row_half_mirror row_mask:0xf bank_mask:0xf
	v_add_f32_dpp v22, v22, v22 row_half_mirror row_mask:0xf bank_mask:0xf
	v_add_f32_dpp v23, v23, v23 row_half_mirror row_mask:0xf bank_mask:0xf
	v_add_f32_dpp v24, v24, v24 row_half_mirror row_mask:0xf bank_mask:0xf
	v_add_f32_dpp v25, v25, v25 row_half_mirror row_mask:0xf bank_mask:0xf
	v_add_f32_dpp v26, v26, v26 row_half_mirror row_mask:0xf bank_mask:0xf
	v_add_f32_dpp v27, v27, v27 row_half_mirror row_mask:0xf bank_mask:0xf
	v_add_f32_dpp v28, v28, v28 row_half_mirror row_mask:0xf bank_mask:0xf
	v_add_f32_dpp v29, v29, v29 row_half_mirror row_mask:0xf bank_mask:0xf
	v_add_f32_dpp v30, v30, v30 row_half_mirror row_mask:0xf bank_mask:0xf
	v_add_f32_dpp v31, v31, v31 row_half_mirror row_mask:0xf bank_mask:0xf
	v_add_f32_dpp v32, v32, v32 row_half_mirror row_mask:0xf bank_mask:0xf
	v_add_f32_dpp v33, v33, v33 row_half_mirror row_mask:0xf bank_mask:0xf
	v_add_f32_dpp v34, v34, v34 row_half_mirror row_mask:0xf bank_mask:0xf
	v_add_f32_dpp v35, v35, v35 row_half_mirror row_mask:0xf bank_mask:0xf
	v_add_f32_dpp v36, v36, v36 row_half_mirror row_mask:0xf bank_mask:0xf
	v_add_f32_dpp v37, v37, v37 row_half_mirror row_mask:0xf bank_mask:0xf
	v_add_f32_dpp v38, v38, v38 row_half_mirror row_mask:0xf bank_mask:0xf
	v_add_f32_dpp v39, v39, v39 row_half_mirror row_mask:0xf bank_mask:0xf
	v_add_f32_dpp v40, v40, v40 row_half_mirror row_mask:0xf bank_mask:0xf
	v_add_f32_dpp v41, v41, v41 row_half_mirror row_mask:0xf bank_mask:0xf
	v_add_f32_dpp v42, v42, v42 row_half_mirror row_mask:0xf bank_mask:0xf
	v_add_f32_dpp v43, v43, v43 row_half_mirror row_mask:0xf bank_mask:0xf
	v_add_f32_dpp v44, v44, v44 row_half_mirror row_mask:0xf bank_mask:0xf
; __global__ void __launch_bounds__(NTHR, 2) fwd_kernel(Args args) {
;     ...
;             for (int q = 0; q < 8; ++q) { const float sq = wave_sum(ssq[q]); const float rs = 1.0f / sqrtf(sq * (1.0f / DM) + EPS);
;                 float lg[8];
; #pragma unroll
;                 for (int e = 0; e < 8; ++e) lg[e] = wave_sum(acc[q][e]) * rs;
	v_add_f32_dpp v45, v45, v45 row_half_mirror row_mask:0xf bank_mask:0xf
	v_add_f32_dpp v46, v46, v46 row_half_mirror row_mask:0xf bank_mask:0xf
	v_add_f32_dpp v47, v47, v47 row_half_mirror row_mask:0xf bank_mask:0xf
	v_add_f32_dpp v48, v48, v48 row_half_mirror row_mask:0xf bank_mask:0xf
	v_add_f32_dpp v49, v49, v49 row_half_mirror row_mask:0xf bank_mask:0xf
	v_add_f32_dpp v50, v50, v50 row_half_mirror row_mask:0xf bank_mask:0xf
	v_add_f32_dpp v51, v51, v51 row_half_mirror row_mask:0xf bank_mask:0xf
	v_add_f32_dpp v52, v52, v52 row_half_mirror row_mask:0xf bank_mask:0xf
	v_add_f32_dpp v53, v53, v53 row_half_mirror row_mask:0xf bank_mask:0xf
	v_add_f32_dpp v54, v54, v54 row_half_mirror row_mask:0xf bank_mask:0xf
	v_add_f32_dpp v55, v55, v55 row_half_mirror row_mask:0xf bank_mask:0xf
	v_add_f32_dpp v56, v56, v56 row_half_mirror row_mask:0xf bank_mask:0xf
	v_add_f32_dpp v57, v57, v57 row_half_mirror row_mask:0xf bank_mask:0xf
	v_add_f32_dpp v58, v58, v58 row_half_mirror row_mask:0xf bank_mask:0xf
	v_add_f32_dpp v59, v59, v59 row_half_mirror row_mask:0xf bank_mask:0xf
	v_add_f32_dpp v60, v60, v60 row_half_mirror row_mask:0xf bank_mask:0xf
	v_add_f32_dpp v61, v61, v61 row_half_mirror row_mask:0xf bank_mask:0xf
	v_add_f32_dpp v62, v62, v62 row_half_mirror row_mask:0xf bank_mask:0xf
	v_add_f32_dpp v63, v63, v63 row_half_mirror row_mask:0xf bank_mask:0xf
	v_add_f32_dpp v192, v192, v192 row_half_mirror row_mask:0xf bank_mask:0xf
	v_add_f32_dpp v194, v194, v194 row_half_mirror row_mask:0xf bank_mask:0xf
	v_add_f32_dpp v196, v196, v196 row_half_mirror row_mask:0xf bank_mask:0xf
	v_add_f32_dpp v198, v198, v198 row_half_mirror row_mask:0xf bank_mask:0xf
	v_add_f32_dpp v200, v200, v200 row_half_mirror row_mask:0xf bank_mask:0xf
	v_add_f32_dpp v202, v202, v202 row_half_mirror row_mask:0xf bank_mask:0xf
	v_add_f32_dpp v204, v204, v204 row_half_mirror row_mask:0xf bank_mask:0xf
	v_add_f32_dpp v206, v206, v206 row_half_mirror row_mask:0xf bank_mask:0xf
	v_add_f32_dpp v0, v0, v0 row_mirror row_mask:0xf bank_mask:0xf
	v_add_f32_dpp v1, v1, v1 row_mirror row_mask:0xf bank_mask:0xf
	v_add_f32_dpp v2, v2, v2 row_mirror row_mask:0xf bank_mask:0xf
	v_add_f32_dpp v3, v3, v3 row_mirror row_mask:0xf bank_mask:0xf
	v_add_f32_dpp v4, v4, v4 row_mirror row_mask:0xf bank_mask:0xf
	v_add_f32_dpp v5, v5, v5 row_mirror row_mask:0xf bank_mask:0xf
	v_add_f32_dpp v6, v6, v6 row_mirror row_mask:0xf bank_mask:0xf
	v_add_f32_dpp v7, v7, v7 row_mirror row_mask:0xf bank_mask:0xf
	v_add_f32_dpp v8, v8, v8 row_mirror row_mask:0xf bank_mask:0xf
	v_add_f32_dpp v9, v9, v9 row_mirror row_mask:0xf bank_mask:0xf
	v_add_f32_dpp v10, v10, v10 row_mirror row_mask:0xf bank_mask:0xf
	v_add_f32_dpp v11, v11, v11 row_mirror row_mask:0xf bank_mask:0xf
	v_add_f32_dpp v12, v12, v12 row_mirror row_mask:0xf bank_mask:0xf
	v_add_f32_dpp v13, v13, v13 row_mirror row_mask:0xf bank_mask:0xf
	v_add_f32_dpp v14, v14, v14 row_mirror row_mask:0xf bank_mask:0xf
	v_add_f32_dpp v15, v15, v15 row_mirror row_mask:0xf bank_mask:0xf
	v_add_f32_dpp v16, v16, v16 row_mirror row_mask:0xf bank_mask:0xf
	v_add_f32_dpp v17, v17, v17 row_mirror row_mask:0xf bank_mask:0xf
	v_add_f32_dpp v18, v18, v18 row_mirror row_mask:0xf bank_mask:0xf
	v_add_f32_dpp v19, v19, v19 row_mirror row_mask:0xf bank_mask:0xf
	v_add_f32_dpp v20, v20, v20 row_mirror row_mask:0xf bank_mask:0xf
	v_add_f32_dpp v21, v21, v21 row_mirror row_mask:0xf bank_mask:0xf
	v_add_f32_dpp v22, v22, v22 row_mirror row_mask:0xf bank_mask:0xf
	v_add_f32_dpp v23, v23, v23 row_mirror row_mask:0xf bank_mask:0xf
	v_add_f32_dpp v24, v24, v24 row_mirror row_mask:0xf bank_mask:0xf
	v_add_f32_dpp v25, v25, v25 row_mirror row_mask:0xf bank_mask:0xf
	v_add_f32_dpp v26, v26, v26 row_mirror row_mask:0xf bank_mask:0xf
	v_add_f32_dpp v27, v27, v27 row_mirror row_mask:0xf bank_mask:0xf
	v_add_f32_dpp v28, v28, v28 row_mirror row_mask:0xf bank_mask:0xf
	v_add_f32_dpp v29, v29, v29 row_mirror row_mask:0xf bank_mask:0xf
	v_add_f32_dpp v30, v30, v30 row_mirror row_mask:0xf bank_mask:0xf
	v_add_f32_dpp v31, v31, v31 row_mirror row_mask:0xf bank_mask:0xf
	v_add_f32_dpp v32, v32, v32 row_mirror row_mask:0xf bank_mask:0xf
	v_add_f32_dpp v33, v33, v33 row_mirror row_mask:0xf bank_mask:0xf
	v_add_f32_dpp v34, v34, v34 row_mirror row_mask:0xf bank_mask:0xf
	v_add_f32_dpp v35, v35, v35 row_mirror row_mask:0xf bank_mask:0xf
	v_add_f32_dpp v36, v36, v36 row_mirror row_mask:0xf bank_mask:0xf
	v_add_f32_dpp v37, v37, v37 row_mirror row_mask:0xf bank_mask:0xf
	v_add_f32_dpp v38, v38, v38 row_mirror row_mask:0xf bank_mask:0xf
	v_add_f32_dpp v39, v39, v39 row_mirror row_mask:0xf bank_mask:0xf
	v_add_f32_dpp v40, v40, v40 row_mirror row_mask:0xf bank_mask:0xf
	v_add_f32_dpp v41, v41, v41 row_mirror row_mask:0xf bank_mask:0xf
	v_add_f32_dpp v42, v42, v42 row_mirror row_mask:0xf bank_mask:0xf
	v_add_f32_dpp v43, v43, v43 row_mirror row_mask:0xf bank_mask:0xf
	v_add_f32_dpp v44, v44, v44 row_mirror row_mask:0xf bank_mask:0xf
	v_add_f32_dpp v45, v45, v45 row_mirror row_mask:0xf bank_mask:0xf
	v_add_f32_dpp v46, v46, v46 row_mirror row_mask:0xf bank_mask:0xf
	v_add_f32_dpp v47, v47, v47 row_mirror row_mask:0xf bank_mask:0xf
	v_add_f32_dpp v48, v48, v48 row_mirror row_mask:0xf bank_mask:0xf
	v_add_f32_dpp v49, v49, v49 row_mirror row_mask:0xf bank_mask:0xf
	v_add_f32_dpp v50, v50, v50 row_mirror row_mask:0xf bank_mask:0xf
	v_add_f32_dpp v51, v51, v51 row_mirror row_mask:0xf bank_mask:0xf
	v_add_f32_dpp v52, v52, v52 row_mirror row_mask:0xf bank_mask:0xf
	v_add_f32_dpp v53, v53, v53 row_mirror row_mask:0xf bank_mask:0xf
	v_add_f32_dpp v54, v54, v54 row_mirror row_mask:0xf bank_mask:0xf
; __global__ void __launch_bounds__(NTHR, 2) fwd_kernel(Args args) {
;     ...
;             for (int q = 0; q < 8; ++q) { const float sq = wave_sum(ssq[q]); const float rs = 1.0f / sqrtf(sq * (1.0f / DM) + EPS);
;                 float lg[8];
; #pragma unroll
;                 for (int e = 0; e < 8; ++e) lg[e] = wave_sum(acc[q][e]) * rs;
	v_add_f32_dpp v55, v55, v55 row_mirror row_mask:0xf bank_mask:0xf
	v_add_f32_dpp v56, v56, v56 row_mirror row_mask:0xf bank_mask:0xf
	v_add_f32_dpp v57, v57, v57 row_mirror row_mask:0xf bank_mask:0xf
	v_add_f32_dpp v58, v58, v58 row_mirror row_mask:0xf bank_mask:0xf
	v_add_f32_dpp v59, v59, v59 row_mirror row_mask:0xf bank_mask:0xf
	v_add_f32_dpp v60, v60, v60 row_mirror row_mask:0xf bank_mask:0xf
	v_add_f32_dpp v61, v61, v61 row_mirror row_mask:0xf bank_mask:0xf
	v_add_f32_dpp v62, v62, v62 row_mirror row_mask:0xf bank_mask:0xf
	v_add_f32_dpp v63, v63, v63 row_mirror row_mask:0xf bank_mask:0xf
	v_add_f32_dpp v192, v192, v192 row_mirror row_mask:0xf bank_mask:0xf
	v_add_f32_dpp v194, v194, v194 row_mirror row_mask:0xf bank_mask:0xf
	v_add_f32_dpp v196, v196, v196 row_mirror row_mask:0xf bank_mask:0xf
	v_add_f32_dpp v198, v198, v198 row_mirror row_mask:0xf bank_mask:0xf
	v_add_f32_dpp v200, v200, v200 row_mirror row_mask:0xf bank_mask:0xf
	v_add_f32_dpp v202, v202, v202 row_mirror row_mask:0xf bank_mask:0xf
	v_add_f32_dpp v204, v204, v204 row_mirror row_mask:0xf bank_mask:0xf
	v_add_f32_dpp v206, v206, v206 row_mirror row_mask:0xf bank_mask:0xf
	v_add_f32_dpp v0, v0, v0 row_bcast:15 row_mask:0xa bank_mask:0xf
	v_add_f32_dpp v1, v1, v1 row_bcast:15 row_mask:0xa bank_mask:0xf
	v_add_f32_dpp v2, v2, v2 row_bcast:15 row_mask:0xa bank_mask:0xf
	v_add_f32_dpp v3, v3, v3 row_bcast:15 row_mask:0xa bank_mask:0xf
	v_add_f32_dpp v4, v4, v4 row_bcast:15 row_mask:0xa bank_mask:0xf
	v_add_f32_dpp v5, v5, v5 row_bcast:15 row_mask:0xa bank_mask:0xf
	v_add_f32_dpp v6, v6, v6 row_bcast:15 row_mask:0xa bank_mask:0xf
	v_add_f32_dpp v7, v7, v7 row_bcast:15 row_mask:0xa bank_mask:0xf
	v_add_f32_dpp v8, v8, v8 row_bcast:15 row_mask:0xa bank_mask:0xf
	v_add_f32_dpp v9, v9, v9 row_bcast:15 row_mask:0xa bank_mask:0xf
	v_add_f32_dpp v10, v10, v10 row_bcast:15 row_mask:0xa bank_mask:0xf
	v_add_f32_dpp v11, v11, v11 row_bcast:15 row_mask:0xa bank_mask:0xf
	v_add_f32_dpp v12, v12, v12 row_bcast:15 row_mask:0xa bank_mask:0xf
	v_add_f32_dpp v13, v13, v13 row_bcast:15 row_mask:0xa bank_mask:0xf
	v_add_f32_dpp v14, v14, v14 row_bcast:15 row_mask:0xa bank_mask:0xf
	v_add_f32_dpp v15, v15, v15 row_bcast:15 row_mask:0xa bank_mask:0xf
	v_add_f32_dpp v16, v16, v16 row_bcast:15 row_mask:0xa bank_mask:0xf
	v_add_f32_dpp v17, v17, v17 row_bcast:15 row_mask:0xa bank_mask:0xf
	v_add_f32_dpp v18, v18, v18 row_bcast:15 row_mask:0xa bank_mask:0xf
	v_add_f32_dpp v19, v19, v19 row_bcast:15 row_mask:0xa bank_mask:0xf
	v_add_f32_dpp v20, v20, v20 row_bcast:15 row_mask:0xa bank_mask:0xf
	v_add_f32_dpp v21, v21, v21 row_bcast:15 row_mask:0xa bank_mask:0xf
	v_add_f32_dpp v22, v22, v22 row_bcast:15 row_mask:0xa bank_mask:0xf
	v_add_f32_dpp v23, v23, v23 row_bcast:15 row_mask:0xa bank_mask:0xf
	v_add_f32_dpp v24, v24, v24 row_bcast:15 row_mask:0xa bank_mask:0xf
	v_add_f32_dpp v25, v25, v25 row_bcast:15 row_mask:0xa bank_mask:0xf
	v_add_f32_dpp v26, v26, v26 row_bcast:15 row_mask:0xa bank_mask:0xf
	v_add_f32_dpp v27, v27, v27 row_bcast:15 row_mask:0xa bank_mask:0xf
	v_add_f32_dpp v28, v28, v28 row_bcast:15 row_mask:0xa bank_mask:0xf
	v_add_f32_dpp v29, v29, v29 row_bcast:15 row_mask:0xa bank_mask:0xf
	v_add_f32_dpp v30, v30, v30 row_bcast:15 row_mask:0xa bank_mask:0xf
	v_add_f32_dpp v31, v31, v31 row_bcast:15 row_mask:0xa bank_mask:0xf
	v_add_f32_dpp v32, v32, v32 row_bcast:15 row_mask:0xa bank_mask:0xf
	v_add_f32_dpp v33, v33, v33 row_bcast:15 row_mask:0xa bank_mask:0xf
	v_add_f32_dpp v34, v34, v34 row_bcast:15 row_mask:0xa bank_mask:0xf
	v_add_f32_dpp v35, v35, v35 row_bcast:15 row_mask:0xa bank_mask:0xf
	v_add_f32_dpp v36, v36, v36 row_bcast:15 row_mask:0xa bank_mask:0xf
	v_add_f32_dpp v37, v37, v37 row_bcast:15 row_mask:0xa bank_mask:0xf
	v_add_f32_dpp v38, v38, v38 row_bcast:15 row_mask:0xa bank_mask:0xf
	v_add_f32_dpp v39, v39, v39 row_bcast:15 row_mask:0xa bank_mask:0xf
	v_add_f32_dpp v40, v40, v40 row_bcast:15 row_mask:0xa bank_mask:0xf
	v_add_f32_dpp v41, v41, v41 row_bcast:15 row_mask:0xa bank_mask:0xf
	v_add_f32_dpp v42, v42, v42 row_bcast:15 row_mask:0xa bank_mask:0xf
	v_add_f32_dpp v43, v43, v43 row_bcast:15 row_mask:0xa bank_mask:0xf
	v_add_f32_dpp v44, v44, v44 row_bcast:15 row_mask:0xa bank_mask:0xf
	v_add_f32_dpp v45, v45, v45 row_bcast:15 row_mask:0xa bank_mask:0xf
	v_add_f32_dpp v46, v46, v46 row_bcast:15 row_mask:0xa bank_mask:0xf
	v_add_f32_dpp v47, v47, v47 row_bcast:15 row_mask:0xa bank_mask:0xf
	v_add_f32_dpp v48, v48, v48 row_bcast:15 row_mask:0xa bank_mask:0xf
	v_add_f32_dpp v49, v49, v49 row_bcast:15 row_mask:0xa bank_mask:0xf
	v_add_f32_dpp v50, v50, v50 row_bcast:15 row_mask:0xa bank_mask:0xf
	v_add_f32_dpp v51, v51, v51 row_bcast:15 row_mask:0xa bank_mask:0xf
	v_add_f32_dpp v52, v52, v52 row_bcast:15 row_mask:0xa bank_mask:0xf
	v_add_f32_dpp v53, v53, v53 row_bcast:15 row_mask:0xa bank_mask:0xf
	v_add_f32_dpp v54, v54, v54 row_bcast:15 row_mask:0xa bank_mask:0xf
	v_add_f32_dpp v55, v55, v55 row_bcast:15 row_mask:0xa bank_mask:0xf
	v_add_f32_dpp v56, v56, v56 row_bcast:15 row_mask:0xa bank_mask:0xf
	v_add_f32_dpp v57, v57, v57 row_bcast:15 row_mask:0xa bank_mask:0xf
	v_add_f32_dpp v58, v58, v58 row_bcast:15 row_mask:0xa bank_mask:0xf
	v_add_f32_dpp v59, v59, v59 row_bcast:15 row_mask:0xa bank_mask:0xf
	v_add_f32_dpp v60, v60, v60 row_bcast:15 row_mask:0xa bank_mask:0xf
	v_add_f32_dpp v61, v61, v61 row_bcast:15 row_mask:0xa bank_mask:0xf
	v_add_f32_dpp v62, v62, v62 row_bcast:15 row_mask:0xa bank_mask:0xf
	v_add_f32_dpp v63, v63, v63 row_bcast:15 row_mask:0xa bank_mask:0xf
	v_add_f32_dpp v192, v192, v192 row_bcast:15 row_mask:0xa bank_mask:0xf
; __global__ void __launch_bounds__(NTHR, 2) fwd_kernel(Args args) {
;     ...
;             for (int q = 0; q < 8; ++q) { const float sq = wave_sum(ssq[q]); const float rs = 1.0f / sqrtf(sq * (1.0f / DM) + EPS);
	v_add_f32_dpp v194, v194, v194 row_bcast:15 row_mask:0xa bank_mask:0xf
	v_add_f32_dpp v196, v196, v196 row_bcast:15 row_mask:0xa bank_mask:0xf
	v_add_f32_dpp v198, v198, v198 row_bcast:15 row_mask:0xa bank_mask:0xf
	v_add_f32_dpp v200, v200, v200 row_bcast:15 row_mask:0xa bank_mask:0xf
	v_add_f32_dpp v202, v202, v202 row_bcast:15 row_mask:0xa bank_mask:0xf
	v_add_f32_dpp v204, v204, v204 row_bcast:15 row_mask:0xa bank_mask:0xf
	v_add_f32_dpp v206, v206, v206 row_bcast:15 row_mask:0xa bank_mask:0xf
	v_add_f32_dpp v0, v0, v0 row_bcast:31 row_mask:0xc bank_mask:0xf
	v_add_f32_dpp v1, v1, v1 row_bcast:31 row_mask:0xc bank_mask:0xf
	v_add_f32_dpp v2, v2, v2 row_bcast:31 row_mask:0xc bank_mask:0xf
	v_add_f32_dpp v3, v3, v3 row_bcast:31 row_mask:0xc bank_mask:0xf
	v_add_f32_dpp v4, v4, v4 row_bcast:31 row_mask:0xc bank_mask:0xf
	v_add_f32_dpp v5, v5, v5 row_bcast:31 row_mask:0xc bank_mask:0xf
	v_add_f32_dpp v6, v6, v6 row_bcast:31 row_mask:0xc bank_mask:0xf
	v_add_f32_dpp v7, v7, v7 row_bcast:31 row_mask:0xc bank_mask:0xf
	v_add_f32_dpp v8, v8, v8 row_bcast:31 row_mask:0xc bank_mask:0xf
	v_add_f32_dpp v9, v9, v9 row_bcast:31 row_mask:0xc bank_mask:0xf
	v_add_f32_dpp v10, v10, v10 row_bcast:31 row_mask:0xc bank_mask:0xf
	v_add_f32_dpp v11, v11, v11 row_bcast:31 row_mask:0xc bank_mask:0xf
	v_add_f32_dpp v12, v12, v12 row_bcast:31 row_mask:0xc bank_mask:0xf
	v_add_f32_dpp v13, v13, v13 row_bcast:31 row_mask:0xc bank_mask:0xf
	v_add_f32_dpp v14, v14, v14 row_bcast:31 row_mask:0xc bank_mask:0xf
	v_add_f32_dpp v15, v15, v15 row_bcast:31 row_mask:0xc bank_mask:0xf
	v_add_f32_dpp v16, v16, v16 row_bcast:31 row_mask:0xc bank_mask:0xf
	v_add_f32_dpp v17, v17, v17 row_bcast:31 row_mask:0xc bank_mask:0xf
	v_add_f32_dpp v18, v18, v18 row_bcast:31 row_mask:0xc bank_mask:0xf
	v_add_f32_dpp v19, v19, v19 row_bcast:31 row_mask:0xc bank_mask:0xf
	v_add_f32_dpp v20, v20, v20 row_bcast:31 row_mask:0xc bank_mask:0xf
	v_add_f32_dpp v21, v21, v21 row_bcast:31 row_mask:0xc bank_mask:0xf
	v_add_f32_dpp v22, v22, v22 row_bcast:31 row_mask:0xc bank_mask:0xf
	v_add_f32_dpp v23, v23, v23 row_bcast:31 row_mask:0xc bank_mask:0xf
	v_add_f32_dpp v24, v24, v24 row_bcast:31 row_mask:0xc bank_mask:0xf
	v_add_f32_dpp v25, v25, v25 row_bcast:31 row_mask:0xc bank_mask:0xf
	v_add_f32_dpp v26, v26, v26 row_bcast:31 row_mask:0xc bank_mask:0xf
	v_add_f32_dpp v27, v27, v27 row_bcast:31 row_mask:0xc bank_mask:0xf
	v_add_f32_dpp v28, v28, v28 row_bcast:31 row_mask:0xc bank_mask:0xf
	v_add_f32_dpp v29, v29, v29 row_bcast:31 row_mask:0xc bank_mask:0xf
	v_add_f32_dpp v30, v30, v30 row_bcast:31 row_mask:0xc bank_mask:0xf
	v_add_f32_dpp v31, v31, v31 row_bcast:31 row_mask:0xc bank_mask:0xf
	v_add_f32_dpp v32, v32, v32 row_bcast:31 row_mask:0xc bank_mask:0xf
	v_add_f32_dpp v33, v33, v33 row_bcast:31 row_mask:0xc bank_mask:0xf
	v_add_f32_dpp v34, v34, v34 row_bcast:31 row_mask:0xc bank_mask:0xf
	v_add_f32_dpp v35, v35, v35 row_bcast:31 row_mask:0xc bank_mask:0xf
	v_add_f32_dpp v36, v36, v36 row_bcast:31 row_mask:0xc bank_mask:0xf
	v_add_f32_dpp v37, v37, v37 row_bcast:31 row_mask:0xc bank_mask:0xf
	v_add_f32_dpp v38, v38, v38 row_bcast:31 row_mask:0xc bank_mask:0xf
	v_add_f32_dpp v39, v39, v39 row_bcast:31 row_mask:0xc bank_mask:0xf
	v_add_f32_dpp v40, v40, v40 row_bcast:31 row_mask:0xc bank_mask:0xf
	v_add_f32_dpp v41, v41, v41 row_bcast:31 row_mask:0xc bank_mask:0xf
	v_add_f32_dpp v42, v42, v42 row_bcast:31 row_mask:0xc bank_mask:0xf
	v_add_f32_dpp v43, v43, v43 row_bcast:31 row_mask:0xc bank_mask:0xf
	v_add_f32_dpp v44, v44, v44 row_bcast:31 row_mask:0xc bank_mask:0xf
	v_add_f32_dpp v45, v45, v45 row_bcast:31 row_mask:0xc bank_mask:0xf
	v_add_f32_dpp v46, v46, v46 row_bcast:31 row_mask:0xc bank_mask:0xf
	v_add_f32_dpp v47, v47, v47 row_bcast:31 row_mask:0xc bank_mask:0xf
	v_add_f32_dpp v48, v48, v48 row_bcast:31 row_mask:0xc bank_mask:0xf
	v_add_f32_dpp v49, v49, v49 row_bcast:31 row_mask:0xc bank_mask:0xf
	v_add_f32_dpp v50, v50, v50 row_bcast:31 row_mask:0xc bank_mask:0xf
	v_add_f32_dpp v51, v51, v51 row_bcast:31 row_mask:0xc bank_mask:0xf
	v_add_f32_dpp v52, v52, v52 row_bcast:31 row_mask:0xc bank_mask:0xf
	v_add_f32_dpp v53, v53, v53 row_bcast:31 row_mask:0xc bank_mask:0xf
	v_add_f32_dpp v54, v54, v54 row_bcast:31 row_mask:0xc bank_mask:0xf
	v_add_f32_dpp v55, v55, v55 row_bcast:31 row_mask:0xc bank_mask:0xf
	v_add_f32_dpp v56, v56, v56 row_bcast:31 row_mask:0xc bank_mask:0xf
	v_add_f32_dpp v57, v57, v57 row_bcast:31 row_mask:0xc bank_mask:0xf
	v_add_f32_dpp v58, v58, v58 row_bcast:31 row_mask:0xc bank_mask:0xf
	v_add_f32_dpp v59, v59, v59 row_bcast:31 row_mask:0xc bank_mask:0xf
	v_add_f32_dpp v60, v60, v60 row_bcast:31 row_mask:0xc bank_mask:0xf
	v_add_f32_dpp v61, v61, v61 row_bcast:31 row_mask:0xc bank_mask:0xf
	v_add_f32_dpp v62, v62, v62 row_bcast:31 row_mask:0xc bank_mask:0xf
	v_add_f32_dpp v63, v63, v63 row_bcast:31 row_mask:0xc bank_mask:0xf
	v_add_f32_dpp v192, v192, v192 row_bcast:31 row_mask:0xc bank_mask:0xf
	v_add_f32_dpp v194, v194, v194 row_bcast:31 row_mask:0xc bank_mask:0xf
	v_add_f32_dpp v196, v196, v196 row_bcast:31 row_mask:0xc bank_mask:0xf
	v_add_f32_dpp v198, v198, v198 row_bcast:31 row_mask:0xc bank_mask:0xf
	v_add_f32_dpp v200, v200, v200 row_bcast:31 row_mask:0xc bank_mask:0xf
	v_add_f32_dpp v202, v202, v202 row_bcast:31 row_mask:0xc bank_mask:0xf
	v_add_f32_dpp v204, v204, v204 row_bcast:31 row_mask:0xc bank_mask:0xf
	v_add_f32_dpp v206, v206, v206 row_bcast:31 row_mask:0xc bank_mask:0xf
	v_fmamk_f32 v232, v192, 0x3a000000, v222
	v_mul_f32_e32 v233, 0x4f800000, v232
	v_cmp_gt_f32_e32 vcc, s63, v232
	s_nop 1
	v_cndmask_b32_e32 v232, v232, v233, vcc
; __global__ void __launch_bounds__(NTHR, 2) fwd_kernel(Args args) {
;     ...
;             for (int q = 0; q < 8; ++q) { const float sq = wave_sum(ssq[q]); const float rs = 1.0f / sqrtf(sq * (1.0f / DM) + EPS);
;                 float lg[8];
; #pragma unroll
;                 for (int e = 0; e < 8; ++e) lg[e] = wave_sum(acc[q][e]) * rs;
;                 int i0 = 0; float v0 = lg[0];
; #pragma unroll
;                 for (int e = 1; e < 8; ++e) if (lg[e] > v0) { v0 = lg[e]; i0 = e; }
;                 int i1 = -1; float v1 = -__builtin_inff();
; #pragma unroll
;                 for (int e = 0; e < 8; ++e) if (e != i0 && lg[e] > v1) { v1 = lg[e]; i1 = e; }
;                 if (lane == 0) { const int t = t0 + q; const float w0 = 1.0f / (1.0f + expf(v1 - v0));
;                     tok_e[t] = i0 | (i1 << 8); tok_w[2 * t] = w0; tok_w[2 * t + 1] = 1.0f - w0; rstd3[t] = rs;
;                     atomicAdd((int*)&lcnt[i0], 1); atomicAdd((int*)&lcnt[i1], 1); } }
	v_sqrt_f32_e32 v233, v232
	s_nop 0
	v_add_u32_e32 v234, -1, v233
	v_add_u32_e32 v235, 1, v233
	v_fma_f32 v236, -v234, v233, v232
	v_fma_f32 v237, -v235, v233, v232
	v_cmp_ge_f32_e64 s[68:69], 0, v236
	s_nop 1
	v_cndmask_b32_e64 v233, v233, v234, s[68:69]
	v_cmp_lt_f32_e64 s[68:69], 0, v237
	s_nop 1
	v_cndmask_b32_e64 v233, v233, v235, s[68:69]
	v_mul_f32_e32 v234, 0x37800000, v233
	v_cndmask_b32_e32 v233, v233, v234, vcc
	v_cmp_class_f32_e32 vcc, v232, v223
	s_nop 1
	v_cndmask_b32_e32 v232, v233, v232, vcc
	v_div_scale_f32 v233, s[68:69], v232, v232, 1.0
	v_rcp_f32_e32 v234, v233
	s_nop 0
	v_fma_f32 v235, -v233, v234, 1.0
	v_fmac_f32_e32 v234, v235, v234
	v_div_scale_f32 v235, vcc, 1.0, v232, 1.0
	v_mul_f32_e32 v236, v235, v234
	v_fma_f32 v237, -v233, v236, v235
	v_fmac_f32_e32 v236, v237, v234
	v_fma_f32 v233, -v233, v236, v235
	s_nop 0
	v_div_fmas_f32 v233, v233, v234, v236
	v_div_fixup_f32 v112, v233, v232, 1.0
	v_mul_f32_e32 v0, v112, v0
	v_mul_f32_e32 v1, v112, v1
	v_mul_f32_e32 v2, v112, v2
	v_mul_f32_e32 v3, v112, v3
	v_mul_f32_e32 v4, v112, v4
	v_mul_f32_e32 v5, v112, v5
	v_mul_f32_e32 v6, v112, v6
	v_mul_f32_e32 v7, v112, v7
	v_mov_b32_e32 v238, v0
	v_mov_b32_e32 v64, 0
	v_cmp_gt_f32_e32 vcc, v1, v238
	s_nop 1
	v_cndmask_b32_e32 v238, v238, v1, vcc
	v_cndmask_b32_e64 v64, v64, 1, vcc
	v_cmp_gt_f32_e32 vcc, v2, v238
	s_nop 1
	v_cndmask_b32_e32 v238, v238, v2, vcc
	v_cndmask_b32_e64 v64, v64, 2, vcc
	v_cmp_gt_f32_e32 vcc, v3, v238
	s_nop 1
	v_cndmask_b32_e32 v238, v238, v3, vcc
	v_cndmask_b32_e64 v64, v64, 3, vcc
	v_cmp_gt_f32_e32 vcc, v4, v238
	s_nop 1
	v_cndmask_b32_e32 v238, v238, v4, vcc
	v_cndmask_b32_e64 v64, v64, 4, vcc
	v_cmp_gt_f32_e32 vcc, v5, v238
	s_nop 1
	v_cndmask_b32_e32 v238, v238, v5, vcc
	v_cndmask_b32_e64 v64, v64, 5, vcc
	v_cmp_gt_f32_e32 vcc, v6, v238
	s_nop 1
	v_cndmask_b32_e32 v238, v238, v6, vcc
	v_cndmask_b32_e64 v64, v64, 6, vcc
	v_cmp_gt_f32_e32 vcc, v7, v238
	s_nop 1
	v_cndmask_b32_e32 v238, v238, v7, vcc
	v_cndmask_b32_e64 v64, v64, 7, vcc
	v_mov_b32_e32 v239, v224
	v_mov_b32_e32 v65, -1
	v_cmp_ne_u32_e64 s[68:69], 0, v64
	v_cmp_gt_f32_e32 vcc, v0, v239
	s_and_b64 vcc, vcc, s[68:69]
	v_cndmask_b32_e32 v239, v239, v0, vcc
	v_cndmask_b32_e64 v65, v65, 0, vcc
	v_cmp_ne_u32_e64 s[68:69], 1, v64
	v_cmp_gt_f32_e32 vcc, v1, v239
	s_and_b64 vcc, vcc, s[68:69]
	v_cndmask_b32_e32 v239, v239, v1, vcc
	v_cndmask_b32_e64 v65, v65, 1, vcc
	v_cmp_ne_u32_e64 s[68:69], 2, v64
	v_cmp_gt_f32_e32 vcc, v2, v239
	s_and_b64 vcc, vcc, s[68:69]
	v_cndmask_b32_e32 v239, v239, v2, vcc
	v_cndmask_b32_e64 v65, v65, 2, vcc
	v_cmp_ne_u32_e64 s[68:69], 3, v64
	v_cmp_gt_f32_e32 vcc, v3, v239
	s_and_b64 vcc, vcc, s[68:69]
	v_cndmask_b32_e32 v239, v239, v3, vcc
	v_cndmask_b32_e64 v65, v65, 3, vcc
	v_cmp_ne_u32_e64 s[68:69], 4, v64
	v_cmp_gt_f32_e32 vcc, v4, v239
	s_and_b64 vcc, vcc, s[68:69]
	v_cndmask_b32_e32 v239, v239, v4, vcc
	v_cndmask_b32_e64 v65, v65, 4, vcc
	v_cmp_ne_u32_e64 s[68:69], 5, v64
	v_cmp_gt_f32_e32 vcc, v5, v239
	s_and_b64 vcc, vcc, s[68:69]
	v_cndmask_b32_e32 v239, v239, v5, vcc
	v_cndmask_b32_e64 v65, v65, 5, vcc
	v_cmp_ne_u32_e64 s[68:69], 6, v64
	v_cmp_gt_f32_e32 vcc, v6, v239
	s_and_b64 vcc, vcc, s[68:69]
	v_cndmask_b32_e32 v239, v239, v6, vcc
	v_cndmask_b32_e64 v65, v65, 6, vcc
	v_cmp_ne_u32_e64 s[68:69], 7, v64
	v_cmp_gt_f32_e32 vcc, v7, v239
	s_and_b64 vcc, vcc, s[68:69]
	v_cndmask_b32_e32 v239, v239, v7, vcc
	v_cndmask_b32_e64 v65, v65, 7, vcc
	v_sub_f32_e32 v232, v239, v238
	v_mul_f32_e32 v233, 0x3fb8aa3b, v232
	v_fma_f32 v234, v232, s65, -v233
	v_rndne_f32_e32 v235, v233
	v_fmac_f32_e32 v234, 0x32a5705f, v232
	v_sub_f32_e32 v233, v233, v235
	v_add_f32_e32 v233, v233, v234
	v_exp_f32_e32 v233, v233
	v_cvt_i32_f32_e32 v234, v235
	v_cmp_ngt_f32_e32 vcc, s66, v232
	v_ldexp_f32 v233, v233, v234
	s_nop 0
	v_cndmask_b32_e32 v233, 0, v233, vcc
	v_cmp_nlt_f32_e32 vcc, s67, v232
	s_nop 1
	v_cndmask_b32_e32 v232, v225, v233, vcc
	v_add_f32_e32 v232, 1.0, v232
	v_div_scale_f32 v233, s[68:69], v232, v232, 1.0
	v_rcp_f32_e32 v234, v233
	s_nop 0
	v_fma_f32 v235, -v233, v234, 1.0
	v_fmac_f32_e32 v234, v235, v234
	v_div_scale_f32 v235, vcc, 1.0, v232, 1.0
	v_mul_f32_e32 v236, v235, v234
	v_fma_f32 v237, -v233, v236, v235
	v_fmac_f32_e32 v236, v237, v234
	v_fma_f32 v233, -v233, v236, v235
	s_nop 0
	v_div_fmas_f32 v233, v233, v234, v236
	v_div_fixup_f32 v66, v233, v232, 1.0
	v_sub_f32_e32 v67, 1.0, v66
	v_lshl_add_u32 v68, v65, 8, v64
	v_fmamk_f32 v232, v194, 0x3a000000, v222
	v_mul_f32_e32 v233, 0x4f800000, v232
	v_cmp_gt_f32_e32 vcc, s63, v232
	s_nop 1
	v_cndmask_b32_e32 v232, v232, v233, vcc
	v_sqrt_f32_e32 v233, v232
	s_nop 0
	v_add_u32_e32 v234, -1, v233
	v_add_u32_e32 v235, 1, v233
	v_fma_f32 v236, -v234, v233, v232
	v_fma_f32 v237, -v235, v233, v232
	v_cmp_ge_f32_e64 s[68:69], 0, v236
	s_nop 1
	v_cndmask_b32_e64 v233, v233, v234, s[68:69]
	v_cmp_lt_f32_e64 s[68:69], 0, v237
	s_nop 1
	v_cndmask_b32_e64 v233, v233, v235, s[68:69]
	v_mul_f32_e32 v234, 0x37800000, v233
	v_cndmask_b32_e32 v233, v233, v234, vcc
	v_cmp_class_f32_e32 vcc, v232, v223
	s_nop 1
	v_cndmask_b32_e32 v232, v233, v232, vcc
	v_div_scale_f32 v233, s[68:69], v232, v232, 1.0
	v_rcp_f32_e32 v234, v233
	s_nop 0
	v_fma_f32 v235, -v233, v234, 1.0
	v_fmac_f32_e32 v234, v235, v234
	v_div_scale_f32 v235, vcc, 1.0, v232, 1.0
	v_mul_f32_e32 v236, v235, v234
	v_fma_f32 v237, -v233, v236, v235
	v_fmac_f32_e32 v236, v237, v234
	v_fma_f32 v233, -v233, v236, v235
	s_nop 0
	v_div_fmas_f32 v233, v233, v234, v236
	v_div_fixup_f32 v113, v233, v232, 1.0
	v_mul_f32_e32 v8, v113, v8
	v_mul_f32_e32 v9, v113, v9
	v_mul_f32_e32 v10, v113, v10
	v_mul_f32_e32 v11, v113, v11
; __global__ void __launch_bounds__(NTHR, 2) fwd_kernel(Args args) {
;     ...
;             for (int q = 0; q < 8; ++q) { const float sq = wave_sum(ssq[q]); const float rs = 1.0f / sqrtf(sq * (1.0f / DM) + EPS);
;                 float lg[8];
; #pragma unroll
;                 for (int e = 0; e < 8; ++e) lg[e] = wave_sum(acc[q][e]) * rs;
;                 int i0 = 0; float v0 = lg[0];
; #pragma unroll
;                 for (int e = 1; e < 8; ++e) if (lg[e] > v0) { v0 = lg[e]; i0 = e; }
;                 int i1 = -1; float v1 = -__builtin_inff();
; #pragma unroll
;                 for (int e = 0; e < 8; ++e) if (e != i0 && lg[e] > v1) { v1 = lg[e]; i1 = e; }
;                 if (lane == 0) { const int t = t0 + q; const float w0 = 1.0f / (1.0f + expf(v1 - v0));
;                     tok_e[t] = i0 | (i1 << 8); tok_w[2 * t] = w0; tok_w[2 * t + 1] = 1.0f - w0; rstd3[t] = rs;
;                     atomicAdd((int*)&lcnt[i0], 1); atomicAdd((int*)&lcnt[i1], 1); } }
	v_mul_f32_e32 v12, v113, v12
	v_mul_f32_e32 v13, v113, v13
	v_mul_f32_e32 v14, v113, v14
	v_mul_f32_e32 v15, v113, v15
	v_mov_b32_e32 v238, v8
	v_mov_b32_e32 v70, 0
	v_cmp_gt_f32_e32 vcc, v9, v238
	s_nop 1
	v_cndmask_b32_e32 v238, v238, v9, vcc
	v_cndmask_b32_e64 v70, v70, 1, vcc
	v_cmp_gt_f32_e32 vcc, v10, v238
	s_nop 1
	v_cndmask_b32_e32 v238, v238, v10, vcc
	v_cndmask_b32_e64 v70, v70, 2, vcc
	v_cmp_gt_f32_e32 vcc, v11, v238
	s_nop 1
	v_cndmask_b32_e32 v238, v238, v11, vcc
	v_cndmask_b32_e64 v70, v70, 3, vcc
	v_cmp_gt_f32_e32 vcc, v12, v238
	s_nop 1
	v_cndmask_b32_e32 v238, v238, v12, vcc
	v_cndmask_b32_e64 v70, v70, 4, vcc
	v_cmp_gt_f32_e32 vcc, v13, v238
	s_nop 1
	v_cndmask_b32_e32 v238, v238, v13, vcc
	v_cndmask_b32_e64 v70, v70, 5, vcc
	v_cmp_gt_f32_e32 vcc, v14, v238
	s_nop 1
	v_cndmask_b32_e32 v238, v238, v14, vcc
	v_cndmask_b32_e64 v70, v70, 6, vcc
	v_cmp_gt_f32_e32 vcc, v15, v238
	s_nop 1
	v_cndmask_b32_e32 v238, v238, v15, vcc
	v_cndmask_b32_e64 v70, v70, 7, vcc
	v_mov_b32_e32 v239, v224
	v_mov_b32_e32 v71, -1
	v_cmp_ne_u32_e64 s[68:69], 0, v70
	v_cmp_gt_f32_e32 vcc, v8, v239
	s_and_b64 vcc, vcc, s[68:69]
	v_cndmask_b32_e32 v239, v239, v8, vcc
	v_cndmask_b32_e64 v71, v71, 0, vcc
	v_cmp_ne_u32_e64 s[68:69], 1, v70
	v_cmp_gt_f32_e32 vcc, v9, v239
	s_and_b64 vcc, vcc, s[68:69]
	v_cndmask_b32_e32 v239, v239, v9, vcc
	v_cndmask_b32_e64 v71, v71, 1, vcc
	v_cmp_ne_u32_e64 s[68:69], 2, v70
	v_cmp_gt_f32_e32 vcc, v10, v239
	s_and_b64 vcc, vcc, s[68:69]
	v_cndmask_b32_e32 v239, v239, v10, vcc
	v_cndmask_b32_e64 v71, v71, 2, vcc
	v_cmp_ne_u32_e64 s[68:69], 3, v70
	v_cmp_gt_f32_e32 vcc, v11, v239
	s_and_b64 vcc, vcc, s[68:69]
	v_cndmask_b32_e32 v239, v239, v11, vcc
	v_cndmask_b32_e64 v71, v71, 3, vcc
	v_cmp_ne_u32_e64 s[68:69], 4, v70
	v_cmp_gt_f32_e32 vcc, v12, v239
	s_and_b64 vcc, vcc, s[68:69]
	v_cndmask_b32_e32 v239, v239, v12, vcc
	v_cndmask_b32_e64 v71, v71, 4, vcc
	v_cmp_ne_u32_e64 s[68:69], 5, v70
	v_cmp_gt_f32_e32 vcc, v13, v239
	s_and_b64 vcc, vcc, s[68:69]
	v_cndmask_b32_e32 v239, v239, v13, vcc
	v_cndmask_b32_e64 v71, v71, 5, vcc
	v_cmp_ne_u32_e64 s[68:69], 6, v70
	v_cmp_gt_f32_e32 vcc, v14, v239
	s_and_b64 vcc, vcc, s[68:69]
	v_cndmask_b32_e32 v239, v239, v14, vcc
	v_cndmask_b32_e64 v71, v71, 6, vcc
	v_cmp_ne_u32_e64 s[68:69], 7, v70
	v_cmp_gt_f32_e32 vcc, v15, v239
	s_and_b64 vcc, vcc, s[68:69]
	v_cndmask_b32_e32 v239, v239, v15, vcc
	v_cndmask_b32_e64 v71, v71, 7, vcc
	v_sub_f32_e32 v232, v239, v238
	v_mul_f32_e32 v233, 0x3fb8aa3b, v232
	v_fma_f32 v234, v232, s65, -v233
	v_rndne_f32_e32 v235, v233
	v_fmac_f32_e32 v234, 0x32a5705f, v232
	v_sub_f32_e32 v233, v233, v235
	v_add_f32_e32 v233, v233, v234
	v_exp_f32_e32 v233, v233
	v_cvt_i32_f32_e32 v234, v235
	v_cmp_ngt_f32_e32 vcc, s66, v232
	v_ldexp_f32 v233, v233, v234
	s_nop 0
	v_cndmask_b32_e32 v233, 0, v233, vcc
	v_cmp_nlt_f32_e32 vcc, s67, v232
	s_nop 1
	v_cndmask_b32_e32 v232, v225, v233, vcc
	v_add_f32_e32 v232, 1.0, v232
	v_div_scale_f32 v233, s[68:69], v232, v232, 1.0
	v_rcp_f32_e32 v234, v233
	s_nop 0
	v_fma_f32 v235, -v233, v234, 1.0
	v_fmac_f32_e32 v234, v235, v234
	v_div_scale_f32 v235, vcc, 1.0, v232, 1.0
	v_mul_f32_e32 v236, v235, v234
	v_fma_f32 v237, -v233, v236, v235
	v_fmac_f32_e32 v236, v237, v234
	v_fma_f32 v233, -v233, v236, v235
	s_nop 0
	v_div_fmas_f32 v233, v233, v234, v236
	v_div_fixup_f32 v72, v233, v232, 1.0
	v_sub_f32_e32 v73, 1.0, v72
	v_lshl_add_u32 v74, v71, 8, v70
	v_fmamk_f32 v232, v196, 0x3a000000, v222
	v_mul_f32_e32 v233, 0x4f800000, v232
	v_cmp_gt_f32_e32 vcc, s63, v232
	s_nop 1
	v_cndmask_b32_e32 v232, v232, v233, vcc
	v_sqrt_f32_e32 v233, v232
	s_nop 0
	v_add_u32_e32 v234, -1, v233
	v_add_u32_e32 v235, 1, v233
	v_fma_f32 v236, -v234, v233, v232
	v_fma_f32 v237, -v235, v233, v232
	v_cmp_ge_f32_e64 s[68:69], 0, v236
	s_nop 1
	v_cndmask_b32_e64 v233, v233, v234, s[68:69]
	v_cmp_lt_f32_e64 s[68:69], 0, v237
	s_nop 1
	v_cndmask_b32_e64 v233, v233, v235, s[68:69]
	v_mul_f32_e32 v234, 0x37800000, v233
	v_cndmask_b32_e32 v233, v233, v234, vcc
	v_cmp_class_f32_e32 vcc, v232, v223
	s_nop 1
	v_cndmask_b32_e32 v232, v233, v232, vcc
	v_div_scale_f32 v233, s[68:69], v232, v232, 1.0
	v_rcp_f32_e32 v234, v233
	s_nop 0
	v_fma_f32 v235, -v233, v234, 1.0
	v_fmac_f32_e32 v234, v235, v234
	v_div_scale_f32 v235, vcc, 1.0, v232, 1.0
	v_mul_f32_e32 v236, v235, v234
	v_fma_f32 v237, -v233, v236, v235
	v_fmac_f32_e32 v236, v237, v234
	v_fma_f32 v233, -v233, v236, v235
	s_nop 0
	v_div_fmas_f32 v233, v233, v234, v236
	v_div_fixup_f32 v114, v233, v232, 1.0
	v_mul_f32_e32 v16, v114, v16
	v_mul_f32_e32 v17, v114, v17
	v_mul_f32_e32 v18, v114, v18
	v_mul_f32_e32 v19, v114, v19
	v_mul_f32_e32 v20, v114, v20
	v_mul_f32_e32 v21, v114, v21
	v_mul_f32_e32 v22, v114, v22
	v_mul_f32_e32 v23, v114, v23
	v_mov_b32_e32 v238, v16
	v_mov_b32_e32 v76, 0
	v_cmp_gt_f32_e32 vcc, v17, v238
	s_nop 1
	v_cndmask_b32_e32 v238, v238, v17, vcc
	v_cndmask_b32_e64 v76, v76, 1, vcc
	v_cmp_gt_f32_e32 vcc, v18, v238
	s_nop 1
	v_cndmask_b32_e32 v238, v238, v18, vcc
	v_cndmask_b32_e64 v76, v76, 2, vcc
	v_cmp_gt_f32_e32 vcc, v19, v238
	s_nop 1
	v_cndmask_b32_e32 v238, v238, v19, vcc
	v_cndmask_b32_e64 v76, v76, 3, vcc
	v_cmp_gt_f32_e32 vcc, v20, v238
	s_nop 1
	v_cndmask_b32_e32 v238, v238, v20, vcc
	v_cndmask_b32_e64 v76, v76, 4, vcc
	v_cmp_gt_f32_e32 vcc, v21, v238
	s_nop 1
	v_cndmask_b32_e32 v238, v238, v21, vcc
	v_cndmask_b32_e64 v76, v76, 5, vcc
	v_cmp_gt_f32_e32 vcc, v22, v238
	s_nop 1
	v_cndmask_b32_e32 v238, v238, v22, vcc
	v_cndmask_b32_e64 v76, v76, 6, vcc
	v_cmp_gt_f32_e32 vcc, v23, v238
	s_nop 1
	v_cndmask_b32_e32 v238, v238, v23, vcc
	v_cndmask_b32_e64 v76, v76, 7, vcc
	v_mov_b32_e32 v239, v224
; __global__ void __launch_bounds__(NTHR, 2) fwd_kernel(Args args) {
;     ...
;             for (int q = 0; q < 8; ++q) { const float sq = wave_sum(ssq[q]); const float rs = 1.0f / sqrtf(sq * (1.0f / DM) + EPS);
;                 float lg[8];
; #pragma unroll
;                 for (int e = 0; e < 8; ++e) lg[e] = wave_sum(acc[q][e]) * rs;
;                 int i0 = 0; float v0 = lg[0];
; #pragma unroll
;                 for (int e = 1; e < 8; ++e) if (lg[e] > v0) { v0 = lg[e]; i0 = e; }
;                 int i1 = -1; float v1 = -__builtin_inff();
; #pragma unroll
;                 for (int e = 0; e < 8; ++e) if (e != i0 && lg[e] > v1) { v1 = lg[e]; i1 = e; }
;                 if (lane == 0) { const int t = t0 + q; const float w0 = 1.0f / (1.0f + expf(v1 - v0));
;                     tok_e[t] = i0 | (i1 << 8); tok_w[2 * t] = w0; tok_w[2 * t + 1] = 1.0f - w0; rstd3[t] = rs;
;                     atomicAdd((int*)&lcnt[i0], 1); atomicAdd((int*)&lcnt[i1], 1); } }
	v_mov_b32_e32 v77, -1
	v_cmp_ne_u32_e64 s[68:69], 0, v76
	v_cmp_gt_f32_e32 vcc, v16, v239
	s_and_b64 vcc, vcc, s[68:69]
	v_cndmask_b32_e32 v239, v239, v16, vcc
	v_cndmask_b32_e64 v77, v77, 0, vcc
	v_cmp_ne_u32_e64 s[68:69], 1, v76
	v_cmp_gt_f32_e32 vcc, v17, v239
	s_and_b64 vcc, vcc, s[68:69]
	v_cndmask_b32_e32 v239, v239, v17, vcc
	v_cndmask_b32_e64 v77, v77, 1, vcc
	v_cmp_ne_u32_e64 s[68:69], 2, v76
	v_cmp_gt_f32_e32 vcc, v18, v239
	s_and_b64 vcc, vcc, s[68:69]
	v_cndmask_b32_e32 v239, v239, v18, vcc
	v_cndmask_b32_e64 v77, v77, 2, vcc
	v_cmp_ne_u32_e64 s[68:69], 3, v76
	v_cmp_gt_f32_e32 vcc, v19, v239
	s_and_b64 vcc, vcc, s[68:69]
	v_cndmask_b32_e32 v239, v239, v19, vcc
	v_cndmask_b32_e64 v77, v77, 3, vcc
	v_cmp_ne_u32_e64 s[68:69], 4, v76
	v_cmp_gt_f32_e32 vcc, v20, v239
	s_and_b64 vcc, vcc, s[68:69]
	v_cndmask_b32_e32 v239, v239, v20, vcc
	v_cndmask_b32_e64 v77, v77, 4, vcc
	v_cmp_ne_u32_e64 s[68:69], 5, v76
	v_cmp_gt_f32_e32 vcc, v21, v239
	s_and_b64 vcc, vcc, s[68:69]
	v_cndmask_b32_e32 v239, v239, v21, vcc
	v_cndmask_b32_e64 v77, v77, 5, vcc
	v_cmp_ne_u32_e64 s[68:69], 6, v76
	v_cmp_gt_f32_e32 vcc, v22, v239
	s_and_b64 vcc, vcc, s[68:69]
	v_cndmask_b32_e32 v239, v239, v22, vcc
	v_cndmask_b32_e64 v77, v77, 6, vcc
	v_cmp_ne_u32_e64 s[68:69], 7, v76
	v_cmp_gt_f32_e32 vcc, v23, v239
	s_and_b64 vcc, vcc, s[68:69]
	v_cndmask_b32_e32 v239, v239, v23, vcc
	v_cndmask_b32_e64 v77, v77, 7, vcc
	v_sub_f32_e32 v232, v239, v238
	v_mul_f32_e32 v233, 0x3fb8aa3b, v232
	v_fma_f32 v234, v232, s65, -v233
	v_rndne_f32_e32 v235, v233
	v_fmac_f32_e32 v234, 0x32a5705f, v232
	v_sub_f32_e32 v233, v233, v235
	v_add_f32_e32 v233, v233, v234
	v_exp_f32_e32 v233, v233
	v_cvt_i32_f32_e32 v234, v235
	v_cmp_ngt_f32_e32 vcc, s66, v232
	v_ldexp_f32 v233, v233, v234
	s_nop 0
	v_cndmask_b32_e32 v233, 0, v233, vcc
	v_cmp_nlt_f32_e32 vcc, s67, v232
	s_nop 1
	v_cndmask_b32_e32 v232, v225, v233, vcc
	v_add_f32_e32 v232, 1.0, v232
	v_div_scale_f32 v233, s[68:69], v232, v232, 1.0
	v_rcp_f32_e32 v234, v233
	s_nop 0
	v_fma_f32 v235, -v233, v234, 1.0
	v_fmac_f32_e32 v234, v235, v234
	v_div_scale_f32 v235, vcc, 1.0, v232, 1.0
	v_mul_f32_e32 v236, v235, v234
	v_fma_f32 v237, -v233, v236, v235
	v_fmac_f32_e32 v236, v237, v234
	v_fma_f32 v233, -v233, v236, v235
	s_nop 0
	v_div_fmas_f32 v233, v233, v234, v236
	v_div_fixup_f32 v78, v233, v232, 1.0
	v_sub_f32_e32 v79, 1.0, v78
	v_lshl_add_u32 v80, v77, 8, v76
	v_fmamk_f32 v232, v198, 0x3a000000, v222
	v_mul_f32_e32 v233, 0x4f800000, v232
	v_cmp_gt_f32_e32 vcc, s63, v232
	s_nop 1
	v_cndmask_b32_e32 v232, v232, v233, vcc
	v_sqrt_f32_e32 v233, v232
	s_nop 0
	v_add_u32_e32 v234, -1, v233
	v_add_u32_e32 v235, 1, v233
	v_fma_f32 v236, -v234, v233, v232
	v_fma_f32 v237, -v235, v233, v232
	v_cmp_ge_f32_e64 s[68:69], 0, v236
	s_nop 1
	v_cndmask_b32_e64 v233, v233, v234, s[68:69]
	v_cmp_lt_f32_e64 s[68:69], 0, v237
	s_nop 1
	v_cndmask_b32_e64 v233, v233, v235, s[68:69]
	v_mul_f32_e32 v234, 0x37800000, v233
	v_cndmask_b32_e32 v233, v233, v234, vcc
	v_cmp_class_f32_e32 vcc, v232, v223
	s_nop 1
	v_cndmask_b32_e32 v232, v233, v232, vcc
	v_div_scale_f32 v233, s[68:69], v232, v232, 1.0
	v_rcp_f32_e32 v234, v233
	s_nop 0
	v_fma_f32 v235, -v233, v234, 1.0
	v_fmac_f32_e32 v234, v235, v234
	v_div_scale_f32 v235, vcc, 1.0, v232, 1.0
	v_mul_f32_e32 v236, v235, v234
	v_fma_f32 v237, -v233, v236, v235
	v_fmac_f32_e32 v236, v237, v234
	v_fma_f32 v233, -v233, v236, v235
	s_nop 0
	v_div_fmas_f32 v233, v233, v234, v236
	v_div_fixup_f32 v115, v233, v232, 1.0
	v_mul_f32_e32 v24, v115, v24
	v_mul_f32_e32 v25, v115, v25
	v_mul_f32_e32 v26, v115, v26
	v_mul_f32_e32 v27, v115, v27
	v_mul_f32_e32 v28, v115, v28
	v_mul_f32_e32 v29, v115, v29
	v_mul_f32_e32 v30, v115, v30
	v_mul_f32_e32 v31, v115, v31
	v_mov_b32_e32 v238, v24
	v_mov_b32_e32 v82, 0
	v_cmp_gt_f32_e32 vcc, v25, v238
	s_nop 1
	v_cndmask_b32_e32 v238, v238, v25, vcc
	v_cndmask_b32_e64 v82, v82, 1, vcc
	v_cmp_gt_f32_e32 vcc, v26, v238
	s_nop 1
	v_cndmask_b32_e32 v238, v238, v26, vcc
	v_cndmask_b32_e64 v82, v82, 2, vcc
	v_cmp_gt_f32_e32 vcc, v27, v238
	s_nop 1
	v_cndmask_b32_e32 v238, v238, v27, vcc
	v_cndmask_b32_e64 v82, v82, 3, vcc
	v_cmp_gt_f32_e32 vcc, v28, v238
	s_nop 1
	v_cndmask_b32_e32 v238, v238, v28, vcc
	v_cndmask_b32_e64 v82, v82, 4, vcc
	v_cmp_gt_f32_e32 vcc, v29, v238
	s_nop 1
	v_cndmask_b32_e32 v238, v238, v29, vcc
	v_cndmask_b32_e64 v82, v82, 5, vcc
	v_cmp_gt_f32_e32 vcc, v30, v238
	s_nop 1
	v_cndmask_b32_e32 v238, v238, v30, vcc
	v_cndmask_b32_e64 v82, v82, 6, vcc
	v_cmp_gt_f32_e32 vcc, v31, v238
	s_nop 1
	v_cndmask_b32_e32 v238, v238, v31, vcc
	v_cndmask_b32_e64 v82, v82, 7, vcc
	v_mov_b32_e32 v239, v224
	v_mov_b32_e32 v83, -1
	v_cmp_ne_u32_e64 s[68:69], 0, v82
	v_cmp_gt_f32_e32 vcc, v24, v239
	s_and_b64 vcc, vcc, s[68:69]
	v_cndmask_b32_e32 v239, v239, v24, vcc
	v_cndmask_b32_e64 v83, v83, 0, vcc
	v_cmp_ne_u32_e64 s[68:69], 1, v82
	v_cmp_gt_f32_e32 vcc, v25, v239
	s_and_b64 vcc, vcc, s[68:69]
	v_cndmask_b32_e32 v239, v239, v25, vcc
	v_cndmask_b32_e64 v83, v83, 1, vcc
	v_cmp_ne_u32_e64 s[68:69], 2, v82
	v_cmp_gt_f32_e32 vcc, v26, v239
	s_and_b64 vcc, vcc, s[68:69]
	v_cndmask_b32_e32 v239, v239, v26, vcc
	v_cndmask_b32_e64 v83, v83, 2, vcc
	v_cmp_ne_u32_e64 s[68:69], 3, v82
	v_cmp_gt_f32_e32 vcc, v27, v239
	s_and_b64 vcc, vcc, s[68:69]
	v_cndmask_b32_e32 v239, v239, v27, vcc
	v_cndmask_b32_e64 v83, v83, 3, vcc
	v_cmp_ne_u32_e64 s[68:69], 4, v82
	v_cmp_gt_f32_e32 vcc, v28, v239
	s_and_b64 vcc, vcc, s[68:69]
	v_cndmask_b32_e32 v239, v239, v28, vcc
	v_cndmask_b32_e64 v83, v83, 4, vcc
	v_cmp_ne_u32_e64 s[68:69], 5, v82
	v_cmp_gt_f32_e32 vcc, v29, v239
	s_and_b64 vcc, vcc, s[68:69]
; __global__ void __launch_bounds__(NTHR, 2) fwd_kernel(Args args) {
;     ...
;             for (int q = 0; q < 8; ++q) { const float sq = wave_sum(ssq[q]); const float rs = 1.0f / sqrtf(sq * (1.0f / DM) + EPS);
;                 float lg[8];
; #pragma unroll
;                 for (int e = 0; e < 8; ++e) lg[e] = wave_sum(acc[q][e]) * rs;
;                 int i0 = 0; float v0 = lg[0];
; #pragma unroll
;                 for (int e = 1; e < 8; ++e) if (lg[e] > v0) { v0 = lg[e]; i0 = e; }
;                 int i1 = -1; float v1 = -__builtin_inff();
; #pragma unroll
;                 for (int e = 0; e < 8; ++e) if (e != i0 && lg[e] > v1) { v1 = lg[e]; i1 = e; }
;                 if (lane == 0) { const int t = t0 + q; const float w0 = 1.0f / (1.0f + expf(v1 - v0));
;                     tok_e[t] = i0 | (i1 << 8); tok_w[2 * t] = w0; tok_w[2 * t + 1] = 1.0f - w0; rstd3[t] = rs;
;                     atomicAdd((int*)&lcnt[i0], 1); atomicAdd((int*)&lcnt[i1], 1); } }
	v_cndmask_b32_e32 v239, v239, v29, vcc
	v_cndmask_b32_e64 v83, v83, 5, vcc
	v_cmp_ne_u32_e64 s[68:69], 6, v82
	v_cmp_gt_f32_e32 vcc, v30, v239
	s_and_b64 vcc, vcc, s[68:69]
	v_cndmask_b32_e32 v239, v239, v30, vcc
	v_cndmask_b32_e64 v83, v83, 6, vcc
	v_cmp_ne_u32_e64 s[68:69], 7, v82
	v_cmp_gt_f32_e32 vcc, v31, v239
	s_and_b64 vcc, vcc, s[68:69]
	v_cndmask_b32_e32 v239, v239, v31, vcc
	v_cndmask_b32_e64 v83, v83, 7, vcc
	v_sub_f32_e32 v232, v239, v238
	v_mul_f32_e32 v233, 0x3fb8aa3b, v232
	v_fma_f32 v234, v232, s65, -v233
	v_rndne_f32_e32 v235, v233
	v_fmac_f32_e32 v234, 0x32a5705f, v232
	v_sub_f32_e32 v233, v233, v235
	v_add_f32_e32 v233, v233, v234
	v_exp_f32_e32 v233, v233
	v_cvt_i32_f32_e32 v234, v235
	v_cmp_ngt_f32_e32 vcc, s66, v232
	v_ldexp_f32 v233, v233, v234
	s_nop 0
	v_cndmask_b32_e32 v233, 0, v233, vcc
	v_cmp_nlt_f32_e32 vcc, s67, v232
	s_nop 1
	v_cndmask_b32_e32 v232, v225, v233, vcc
	v_add_f32_e32 v232, 1.0, v232
	v_div_scale_f32 v233, s[68:69], v232, v232, 1.0
	v_rcp_f32_e32 v234, v233
	s_nop 0
	v_fma_f32 v235, -v233, v234, 1.0
	v_fmac_f32_e32 v234, v235, v234
	v_div_scale_f32 v235, vcc, 1.0, v232, 1.0
	v_mul_f32_e32 v236, v235, v234
	v_fma_f32 v237, -v233, v236, v235
	v_fmac_f32_e32 v236, v237, v234
	v_fma_f32 v233, -v233, v236, v235
	s_nop 0
	v_div_fmas_f32 v233, v233, v234, v236
	v_div_fixup_f32 v84, v233, v232, 1.0
	v_sub_f32_e32 v85, 1.0, v84
	v_lshl_add_u32 v86, v83, 8, v82
	v_fmamk_f32 v232, v200, 0x3a000000, v222
	v_mul_f32_e32 v233, 0x4f800000, v232
	v_cmp_gt_f32_e32 vcc, s63, v232
	s_nop 1
	v_cndmask_b32_e32 v232, v232, v233, vcc
	v_sqrt_f32_e32 v233, v232
	s_nop 0
	v_add_u32_e32 v234, -1, v233
	v_add_u32_e32 v235, 1, v233
	v_fma_f32 v236, -v234, v233, v232
	v_fma_f32 v237, -v235, v233, v232
	v_cmp_ge_f32_e64 s[68:69], 0, v236
	s_nop 1
	v_cndmask_b32_e64 v233, v233, v234, s[68:69]
	v_cmp_lt_f32_e64 s[68:69], 0, v237
	s_nop 1
	v_cndmask_b32_e64 v233, v233, v235, s[68:69]
	v_mul_f32_e32 v234, 0x37800000, v233
	v_cndmask_b32_e32 v233, v233, v234, vcc
	v_cmp_class_f32_e32 vcc, v232, v223
	s_nop 1
	v_cndmask_b32_e32 v232, v233, v232, vcc
	v_div_scale_f32 v233, s[68:69], v232, v232, 1.0
	v_rcp_f32_e32 v234, v233
	s_nop 0
	v_fma_f32 v235, -v233, v234, 1.0
	v_fmac_f32_e32 v234, v235, v234
	v_div_scale_f32 v235, vcc, 1.0, v232, 1.0
	v_mul_f32_e32 v236, v235, v234
	v_fma_f32 v237, -v233, v236, v235
	v_fmac_f32_e32 v236, v237, v234
	v_fma_f32 v233, -v233, v236, v235
	s_nop 0
	v_div_fmas_f32 v233, v233, v234, v236
	v_div_fixup_f32 v116, v233, v232, 1.0
	v_mul_f32_e32 v32, v116, v32
	v_mul_f32_e32 v33, v116, v33
	v_mul_f32_e32 v34, v116, v34
	v_mul_f32_e32 v35, v116, v35
	v_mul_f32_e32 v36, v116, v36
	v_mul_f32_e32 v37, v116, v37
	v_mul_f32_e32 v38, v116, v38
	v_mul_f32_e32 v39, v116, v39
	v_mov_b32_e32 v238, v32
	v_mov_b32_e32 v88, 0
	v_cmp_gt_f32_e32 vcc, v33, v238
	s_nop 1
	v_cndmask_b32_e32 v238, v238, v33, vcc
	v_cndmask_b32_e64 v88, v88, 1, vcc
	v_cmp_gt_f32_e32 vcc, v34, v238
	s_nop 1
	v_cndmask_b32_e32 v238, v238, v34, vcc
	v_cndmask_b32_e64 v88, v88, 2, vcc
	v_cmp_gt_f32_e32 vcc, v35, v238
	s_nop 1
	v_cndmask_b32_e32 v238, v238, v35, vcc
	v_cndmask_b32_e64 v88, v88, 3, vcc
	v_cmp_gt_f32_e32 vcc, v36, v238
	s_nop 1
	v_cndmask_b32_e32 v238, v238, v36, vcc
	v_cndmask_b32_e64 v88, v88, 4, vcc
	v_cmp_gt_f32_e32 vcc, v37, v238
	s_nop 1
	v_cndmask_b32_e32 v238, v238, v37, vcc
	v_cndmask_b32_e64 v88, v88, 5, vcc
	v_cmp_gt_f32_e32 vcc, v38, v238
	s_nop 1
	v_cndmask_b32_e32 v238, v238, v38, vcc
	v_cndmask_b32_e64 v88, v88, 6, vcc
	v_cmp_gt_f32_e32 vcc, v39, v238
	s_nop 1
	v_cndmask_b32_e32 v238, v238, v39, vcc
	v_cndmask_b32_e64 v88, v88, 7, vcc
	v_mov_b32_e32 v239, v224
	v_mov_b32_e32 v89, -1
	v_cmp_ne_u32_e64 s[68:69], 0, v88
	v_cmp_gt_f32_e32 vcc, v32, v239
	s_and_b64 vcc, vcc, s[68:69]
	v_cndmask_b32_e32 v239, v239, v32, vcc
	v_cndmask_b32_e64 v89, v89, 0, vcc
	v_cmp_ne_u32_e64 s[68:69], 1, v88
	v_cmp_gt_f32_e32 vcc, v33, v239
	s_and_b64 vcc, vcc, s[68:69]
	v_cndmask_b32_e32 v239, v239, v33, vcc
	v_cndmask_b32_e64 v89, v89, 1, vcc
	v_cmp_ne_u32_e64 s[68:69], 2, v88
	v_cmp_gt_f32_e32 vcc, v34, v239
	s_and_b64 vcc, vcc, s[68:69]
	v_cndmask_b32_e32 v239, v239, v34, vcc
	v_cndmask_b32_e64 v89, v89, 2, vcc
	v_cmp_ne_u32_e64 s[68:69], 3, v88
	v_cmp_gt_f32_e32 vcc, v35, v239
	s_and_b64 vcc, vcc, s[68:69]
	v_cndmask_b32_e32 v239, v239, v35, vcc
	v_cndmask_b32_e64 v89, v89, 3, vcc
	v_cmp_ne_u32_e64 s[68:69], 4, v88
	v_cmp_gt_f32_e32 vcc, v36, v239
	s_and_b64 vcc, vcc, s[68:69]
	v_cndmask_b32_e32 v239, v239, v36, vcc
	v_cndmask_b32_e64 v89, v89, 4, vcc
	v_cmp_ne_u32_e64 s[68:69], 5, v88
	v_cmp_gt_f32_e32 vcc, v37, v239
	s_and_b64 vcc, vcc, s[68:69]
	v_cndmask_b32_e32 v239, v239, v37, vcc
	v_cndmask_b32_e64 v89, v89, 5, vcc
	v_cmp_ne_u32_e64 s[68:69], 6, v88
	v_cmp_gt_f32_e32 vcc, v38, v239
	s_and_b64 vcc, vcc, s[68:69]
	v_cndmask_b32_e32 v239, v239, v38, vcc
	v_cndmask_b32_e64 v89, v89, 6, vcc
	v_cmp_ne_u32_e64 s[68:69], 7, v88
	v_cmp_gt_f32_e32 vcc, v39, v239
	s_and_b64 vcc, vcc, s[68:69]
	v_cndmask_b32_e32 v239, v239, v39, vcc
	v_cndmask_b32_e64 v89, v89, 7, vcc
	v_sub_f32_e32 v232, v239, v238
	v_mul_f32_e32 v233, 0x3fb8aa3b, v232
	v_fma_f32 v234, v232, s65, -v233
	v_rndne_f32_e32 v235, v233
	v_fmac_f32_e32 v234, 0x32a5705f, v232
	v_sub_f32_e32 v233, v233, v235
	v_add_f32_e32 v233, v233, v234
	v_exp_f32_e32 v233, v233
	v_cvt_i32_f32_e32 v234, v235
	v_cmp_ngt_f32_e32 vcc, s66, v232
	v_ldexp_f32 v233, v233, v234
	s_nop 0
	v_cndmask_b32_e32 v233, 0, v233, vcc
	v_cmp_nlt_f32_e32 vcc, s67, v232
	s_nop 1
	v_cndmask_b32_e32 v232, v225, v233, vcc
	v_add_f32_e32 v232, 1.0, v232
	v_div_scale_f32 v233, s[68:69], v232, v232, 1.0
; __global__ void __launch_bounds__(NTHR, 2) fwd_kernel(Args args) {
;     ...
;             for (int q = 0; q < 8; ++q) { const float sq = wave_sum(ssq[q]); const float rs = 1.0f / sqrtf(sq * (1.0f / DM) + EPS);
;                 float lg[8];
; #pragma unroll
;                 for (int e = 0; e < 8; ++e) lg[e] = wave_sum(acc[q][e]) * rs;
;                 int i0 = 0; float v0 = lg[0];
; #pragma unroll
;                 for (int e = 1; e < 8; ++e) if (lg[e] > v0) { v0 = lg[e]; i0 = e; }
;                 int i1 = -1; float v1 = -__builtin_inff();
; #pragma unroll
;                 for (int e = 0; e < 8; ++e) if (e != i0 && lg[e] > v1) { v1 = lg[e]; i1 = e; }
;                 if (lane == 0) { const int t = t0 + q; const float w0 = 1.0f / (1.0f + expf(v1 - v0));
;                     tok_e[t] = i0 | (i1 << 8); tok_w[2 * t] = w0; tok_w[2 * t + 1] = 1.0f - w0; rstd3[t] = rs;
;                     atomicAdd((int*)&lcnt[i0], 1); atomicAdd((int*)&lcnt[i1], 1); } }
	v_rcp_f32_e32 v234, v233
	s_nop 0
	v_fma_f32 v235, -v233, v234, 1.0
	v_fmac_f32_e32 v234, v235, v234
	v_div_scale_f32 v235, vcc, 1.0, v232, 1.0
	v_mul_f32_e32 v236, v235, v234
	v_fma_f32 v237, -v233, v236, v235
	v_fmac_f32_e32 v236, v237, v234
	v_fma_f32 v233, -v233, v236, v235
	s_nop 0
	v_div_fmas_f32 v233, v233, v234, v236
	v_div_fixup_f32 v90, v233, v232, 1.0
	v_sub_f32_e32 v91, 1.0, v90
	v_lshl_add_u32 v92, v89, 8, v88
	v_fmamk_f32 v232, v202, 0x3a000000, v222
	v_mul_f32_e32 v233, 0x4f800000, v232
	v_cmp_gt_f32_e32 vcc, s63, v232
	s_nop 1
	v_cndmask_b32_e32 v232, v232, v233, vcc
	v_sqrt_f32_e32 v233, v232
	s_nop 0
	v_add_u32_e32 v234, -1, v233
	v_add_u32_e32 v235, 1, v233
	v_fma_f32 v236, -v234, v233, v232
	v_fma_f32 v237, -v235, v233, v232
	v_cmp_ge_f32_e64 s[68:69], 0, v236
	s_nop 1
	v_cndmask_b32_e64 v233, v233, v234, s[68:69]
	v_cmp_lt_f32_e64 s[68:69], 0, v237
	s_nop 1
	v_cndmask_b32_e64 v233, v233, v235, s[68:69]
	v_mul_f32_e32 v234, 0x37800000, v233
	v_cndmask_b32_e32 v233, v233, v234, vcc
	v_cmp_class_f32_e32 vcc, v232, v223
	s_nop 1
	v_cndmask_b32_e32 v232, v233, v232, vcc
	v_div_scale_f32 v233, s[68:69], v232, v232, 1.0
	v_rcp_f32_e32 v234, v233
	s_nop 0
	v_fma_f32 v235, -v233, v234, 1.0
	v_fmac_f32_e32 v234, v235, v234
	v_div_scale_f32 v235, vcc, 1.0, v232, 1.0
	v_mul_f32_e32 v236, v235, v234
	v_fma_f32 v237, -v233, v236, v235
	v_fmac_f32_e32 v236, v237, v234
	v_fma_f32 v233, -v233, v236, v235
	s_nop 0
	v_div_fmas_f32 v233, v233, v234, v236
	v_div_fixup_f32 v117, v233, v232, 1.0
	v_mul_f32_e32 v40, v117, v40
	v_mul_f32_e32 v41, v117, v41
	v_mul_f32_e32 v42, v117, v42
	v_mul_f32_e32 v43, v117, v43
	v_mul_f32_e32 v44, v117, v44
	v_mul_f32_e32 v45, v117, v45
	v_mul_f32_e32 v46, v117, v46
	v_mul_f32_e32 v47, v117, v47
	v_mov_b32_e32 v238, v40
	v_mov_b32_e32 v94, 0
	v_cmp_gt_f32_e32 vcc, v41, v238
	s_nop 1
	v_cndmask_b32_e32 v238, v238, v41, vcc
	v_cndmask_b32_e64 v94, v94, 1, vcc
	v_cmp_gt_f32_e32 vcc, v42, v238
	s_nop 1
	v_cndmask_b32_e32 v238, v238, v42, vcc
	v_cndmask_b32_e64 v94, v94, 2, vcc
	v_cmp_gt_f32_e32 vcc, v43, v238
	s_nop 1
	v_cndmask_b32_e32 v238, v238, v43, vcc
	v_cndmask_b32_e64 v94, v94, 3, vcc
	v_cmp_gt_f32_e32 vcc, v44, v238
	s_nop 1
	v_cndmask_b32_e32 v238, v238, v44, vcc
	v_cndmask_b32_e64 v94, v94, 4, vcc
	v_cmp_gt_f32_e32 vcc, v45, v238
	s_nop 1
	v_cndmask_b32_e32 v238, v238, v45, vcc
	v_cndmask_b32_e64 v94, v94, 5, vcc
	v_cmp_gt_f32_e32 vcc, v46, v238
	s_nop 1
	v_cndmask_b32_e32 v238, v238, v46, vcc
	v_cndmask_b32_e64 v94, v94, 6, vcc
	v_cmp_gt_f32_e32 vcc, v47, v238
	s_nop 1
	v_cndmask_b32_e32 v238, v238, v47, vcc
	v_cndmask_b32_e64 v94, v94, 7, vcc
	v_mov_b32_e32 v239, v224
	v_mov_b32_e32 v95, -1
	v_cmp_ne_u32_e64 s[68:69], 0, v94
	v_cmp_gt_f32_e32 vcc, v40, v239
	s_and_b64 vcc, vcc, s[68:69]
	v_cndmask_b32_e32 v239, v239, v40, vcc
	v_cndmask_b32_e64 v95, v95, 0, vcc
	v_cmp_ne_u32_e64 s[68:69], 1, v94
	v_cmp_gt_f32_e32 vcc, v41, v239
	s_and_b64 vcc, vcc, s[68:69]
	v_cndmask_b32_e32 v239, v239, v41, vcc
	v_cndmask_b32_e64 v95, v95, 1, vcc
	v_cmp_ne_u32_e64 s[68:69], 2, v94
	v_cmp_gt_f32_e32 vcc, v42, v239
	s_and_b64 vcc, vcc, s[68:69]
	v_cndmask_b32_e32 v239, v239, v42, vcc
	v_cndmask_b32_e64 v95, v95, 2, vcc
	v_cmp_ne_u32_e64 s[68:69], 3, v94
	v_cmp_gt_f32_e32 vcc, v43, v239
	s_and_b64 vcc, vcc, s[68:69]
	v_cndmask_b32_e32 v239, v239, v43, vcc
	v_cndmask_b32_e64 v95, v95, 3, vcc
	v_cmp_ne_u32_e64 s[68:69], 4, v94
	v_cmp_gt_f32_e32 vcc, v44, v239
	s_and_b64 vcc, vcc, s[68:69]
	v_cndmask_b32_e32 v239, v239, v44, vcc
	v_cndmask_b32_e64 v95, v95, 4, vcc
	v_cmp_ne_u32_e64 s[68:69], 5, v94
	v_cmp_gt_f32_e32 vcc, v45, v239
	s_and_b64 vcc, vcc, s[68:69]
	v_cndmask_b32_e32 v239, v239, v45, vcc
	v_cndmask_b32_e64 v95, v95, 5, vcc
	v_cmp_ne_u32_e64 s[68:69], 6, v94
	v_cmp_gt_f32_e32 vcc, v46, v239
	s_and_b64 vcc, vcc, s[68:69]
	v_cndmask_b32_e32 v239, v239, v46, vcc
	v_cndmask_b32_e64 v95, v95, 6, vcc
	v_cmp_ne_u32_e64 s[68:69], 7, v94
	v_cmp_gt_f32_e32 vcc, v47, v239
	s_and_b64 vcc, vcc, s[68:69]
	v_cndmask_b32_e32 v239, v239, v47, vcc
	v_cndmask_b32_e64 v95, v95, 7, vcc
	v_sub_f32_e32 v232, v239, v238
	v_mul_f32_e32 v233, 0x3fb8aa3b, v232
	v_fma_f32 v234, v232, s65, -v233
	v_rndne_f32_e32 v235, v233
	v_fmac_f32_e32 v234, 0x32a5705f, v232
	v_sub_f32_e32 v233, v233, v235
	v_add_f32_e32 v233, v233, v234
	v_exp_f32_e32 v233, v233
	v_cvt_i32_f32_e32 v234, v235
	v_cmp_ngt_f32_e32 vcc, s66, v232
	v_ldexp_f32 v233, v233, v234
	s_nop 0
	v_cndmask_b32_e32 v233, 0, v233, vcc
	v_cmp_nlt_f32_e32 vcc, s67, v232
	s_nop 1
	v_cndmask_b32_e32 v232, v225, v233, vcc
	v_add_f32_e32 v232, 1.0, v232
	v_div_scale_f32 v233, s[68:69], v232, v232, 1.0
	v_rcp_f32_e32 v234, v233
	s_nop 0
	v_fma_f32 v235, -v233, v234, 1.0
	v_fmac_f32_e32 v234, v235, v234
	v_div_scale_f32 v235, vcc, 1.0, v232, 1.0
	v_mul_f32_e32 v236, v235, v234
	v_fma_f32 v237, -v233, v236, v235
	v_fmac_f32_e32 v236, v237, v234
	v_fma_f32 v233, -v233, v236, v235
	s_nop 0
	v_div_fmas_f32 v233, v233, v234, v236
	v_div_fixup_f32 v96, v233, v232, 1.0
	v_sub_f32_e32 v97, 1.0, v96
	v_lshl_add_u32 v98, v95, 8, v94
	v_fmamk_f32 v232, v204, 0x3a000000, v222
	v_mul_f32_e32 v233, 0x4f800000, v232
	v_cmp_gt_f32_e32 vcc, s63, v232
	s_nop 1
	v_cndmask_b32_e32 v232, v232, v233, vcc
	v_sqrt_f32_e32 v233, v232
	s_nop 0
	v_add_u32_e32 v234, -1, v233
	v_add_u32_e32 v235, 1, v233
	v_fma_f32 v236, -v234, v233, v232
	v_fma_f32 v237, -v235, v233, v232
	v_cmp_ge_f32_e64 s[68:69], 0, v236
	s_nop 1
	v_cndmask_b32_e64 v233, v233, v234, s[68:69]
	v_cmp_lt_f32_e64 s[68:69], 0, v237
	s_nop 1
	v_cndmask_b32_e64 v233, v233, v235, s[68:69]
	v_mul_f32_e32 v234, 0x37800000, v233
	v_cndmask_b32_e32 v233, v233, v234, vcc
; __global__ void __launch_bounds__(NTHR, 2) fwd_kernel(Args args) {
;     ...
;             for (int q = 0; q < 8; ++q) { const float sq = wave_sum(ssq[q]); const float rs = 1.0f / sqrtf(sq * (1.0f / DM) + EPS);
;                 float lg[8];
; #pragma unroll
;                 for (int e = 0; e < 8; ++e) lg[e] = wave_sum(acc[q][e]) * rs;
;                 int i0 = 0; float v0 = lg[0];
; #pragma unroll
;                 for (int e = 1; e < 8; ++e) if (lg[e] > v0) { v0 = lg[e]; i0 = e; }
;                 int i1 = -1; float v1 = -__builtin_inff();
; #pragma unroll
;                 for (int e = 0; e < 8; ++e) if (e != i0 && lg[e] > v1) { v1 = lg[e]; i1 = e; }
;                 if (lane == 0) { const int t = t0 + q; const float w0 = 1.0f / (1.0f + expf(v1 - v0));
;                     tok_e[t] = i0 | (i1 << 8); tok_w[2 * t] = w0; tok_w[2 * t + 1] = 1.0f - w0; rstd3[t] = rs;
;                     atomicAdd((int*)&lcnt[i0], 1); atomicAdd((int*)&lcnt[i1], 1); } }
	v_cmp_class_f32_e32 vcc, v232, v223
	s_nop 1
	v_cndmask_b32_e32 v232, v233, v232, vcc
	v_div_scale_f32 v233, s[68:69], v232, v232, 1.0
	v_rcp_f32_e32 v234, v233
	s_nop 0
	v_fma_f32 v235, -v233, v234, 1.0
	v_fmac_f32_e32 v234, v235, v234
	v_div_scale_f32 v235, vcc, 1.0, v232, 1.0
	v_mul_f32_e32 v236, v235, v234
	v_fma_f32 v237, -v233, v236, v235
	v_fmac_f32_e32 v236, v237, v234
	v_fma_f32 v233, -v233, v236, v235
	s_nop 0
	v_div_fmas_f32 v233, v233, v234, v236
	v_div_fixup_f32 v118, v233, v232, 1.0
	v_mul_f32_e32 v48, v118, v48
	v_mul_f32_e32 v49, v118, v49
	v_mul_f32_e32 v50, v118, v50
	v_mul_f32_e32 v51, v118, v51
	v_mul_f32_e32 v52, v118, v52
	v_mul_f32_e32 v53, v118, v53
	v_mul_f32_e32 v54, v118, v54
	v_mul_f32_e32 v55, v118, v55
	v_mov_b32_e32 v238, v48
	v_mov_b32_e32 v100, 0
	v_cmp_gt_f32_e32 vcc, v49, v238
	s_nop 1
	v_cndmask_b32_e32 v238, v238, v49, vcc
	v_cndmask_b32_e64 v100, v100, 1, vcc
	v_cmp_gt_f32_e32 vcc, v50, v238
	s_nop 1
	v_cndmask_b32_e32 v238, v238, v50, vcc
	v_cndmask_b32_e64 v100, v100, 2, vcc
	v_cmp_gt_f32_e32 vcc, v51, v238
	s_nop 1
	v_cndmask_b32_e32 v238, v238, v51, vcc
	v_cndmask_b32_e64 v100, v100, 3, vcc
	v_cmp_gt_f32_e32 vcc, v52, v238
	s_nop 1
	v_cndmask_b32_e32 v238, v238, v52, vcc
	v_cndmask_b32_e64 v100, v100, 4, vcc
	v_cmp_gt_f32_e32 vcc, v53, v238
	s_nop 1
	v_cndmask_b32_e32 v238, v238, v53, vcc
	v_cndmask_b32_e64 v100, v100, 5, vcc
	v_cmp_gt_f32_e32 vcc, v54, v238
	s_nop 1
	v_cndmask_b32_e32 v238, v238, v54, vcc
	v_cndmask_b32_e64 v100, v100, 6, vcc
	v_cmp_gt_f32_e32 vcc, v55, v238
	s_nop 1
	v_cndmask_b32_e32 v238, v238, v55, vcc
	v_cndmask_b32_e64 v100, v100, 7, vcc
	v_mov_b32_e32 v239, v224
	v_mov_b32_e32 v101, -1
	v_cmp_ne_u32_e64 s[68:69], 0, v100
	v_cmp_gt_f32_e32 vcc, v48, v239
	s_and_b64 vcc, vcc, s[68:69]
	v_cndmask_b32_e32 v239, v239, v48, vcc
	v_cndmask_b32_e64 v101, v101, 0, vcc
	v_cmp_ne_u32_e64 s[68:69], 1, v100
	v_cmp_gt_f32_e32 vcc, v49, v239
	s_and_b64 vcc, vcc, s[68:69]
	v_cndmask_b32_e32 v239, v239, v49, vcc
	v_cndmask_b32_e64 v101, v101, 1, vcc
	v_cmp_ne_u32_e64 s[68:69], 2, v100
	v_cmp_gt_f32_e32 vcc, v50, v239
	s_and_b64 vcc, vcc, s[68:69]
	v_cndmask_b32_e32 v239, v239, v50, vcc
	v_cndmask_b32_e64 v101, v101, 2, vcc
	v_cmp_ne_u32_e64 s[68:69], 3, v100
	v_cmp_gt_f32_e32 vcc, v51, v239
	s_and_b64 vcc, vcc, s[68:69]
	v_cndmask_b32_e32 v239, v239, v51, vcc
	v_cndmask_b32_e64 v101, v101, 3, vcc
	v_cmp_ne_u32_e64 s[68:69], 4, v100
	v_cmp_gt_f32_e32 vcc, v52, v239
	s_and_b64 vcc, vcc, s[68:69]
	v_cndmask_b32_e32 v239, v239, v52, vcc
	v_cndmask_b32_e64 v101, v101, 4, vcc
	v_cmp_ne_u32_e64 s[68:69], 5, v100
	v_cmp_gt_f32_e32 vcc, v53, v239
	s_and_b64 vcc, vcc, s[68:69]
	v_cndmask_b32_e32 v239, v239, v53, vcc
	v_cndmask_b32_e64 v101, v101, 5, vcc
	v_cmp_ne_u32_e64 s[68:69], 6, v100
	v_cmp_gt_f32_e32 vcc, v54, v239
	s_and_b64 vcc, vcc, s[68:69]
	v_cndmask_b32_e32 v239, v239, v54, vcc
	v_cndmask_b32_e64 v101, v101, 6, vcc
	v_cmp_ne_u32_e64 s[68:69], 7, v100
	v_cmp_gt_f32_e32 vcc, v55, v239
	s_and_b64 vcc, vcc, s[68:69]
	v_cndmask_b32_e32 v239, v239, v55, vcc
	v_cndmask_b32_e64 v101, v101, 7, vcc
	v_sub_f32_e32 v232, v239, v238
	v_mul_f32_e32 v233, 0x3fb8aa3b, v232
	v_fma_f32 v234, v232, s65, -v233
	v_rndne_f32_e32 v235, v233
	v_fmac_f32_e32 v234, 0x32a5705f, v232
	v_sub_f32_e32 v233, v233, v235
	v_add_f32_e32 v233, v233, v234
	v_exp_f32_e32 v233, v233
	v_cvt_i32_f32_e32 v234, v235
	v_cmp_ngt_f32_e32 vcc, s66, v232
	v_ldexp_f32 v233, v233, v234
	s_nop 0
	v_cndmask_b32_e32 v233, 0, v233, vcc
	v_cmp_nlt_f32_e32 vcc, s67, v232
	s_nop 1
	v_cndmask_b32_e32 v232, v225, v233, vcc
	v_add_f32_e32 v232, 1.0, v232
	v_div_scale_f32 v233, s[68:69], v232, v232, 1.0
	v_rcp_f32_e32 v234, v233
	s_nop 0
	v_fma_f32 v235, -v233, v234, 1.0
	v_fmac_f32_e32 v234, v235, v234
	v_div_scale_f32 v235, vcc, 1.0, v232, 1.0
	v_mul_f32_e32 v236, v235, v234
	v_fma_f32 v237, -v233, v236, v235
	v_fmac_f32_e32 v236, v237, v234
	v_fma_f32 v233, -v233, v236, v235
	s_nop 0
	v_div_fmas_f32 v233, v233, v234, v236
	v_div_fixup_f32 v102, v233, v232, 1.0
	v_sub_f32_e32 v103, 1.0, v102
	v_lshl_add_u32 v104, v101, 8, v100
	v_fmamk_f32 v232, v206, 0x3a000000, v222
	v_mul_f32_e32 v233, 0x4f800000, v232
	v_cmp_gt_f32_e32 vcc, s63, v232
	s_nop 1
	v_cndmask_b32_e32 v232, v232, v233, vcc
	v_sqrt_f32_e32 v233, v232
	s_nop 0
	v_add_u32_e32 v234, -1, v233
	v_add_u32_e32 v235, 1, v233
	v_fma_f32 v236, -v234, v233, v232
	v_fma_f32 v237, -v235, v233, v232
	v_cmp_ge_f32_e64 s[68:69], 0, v236
	s_nop 1
	v_cndmask_b32_e64 v233, v233, v234, s[68:69]
	v_cmp_lt_f32_e64 s[68:69], 0, v237
	s_nop 1
	v_cndmask_b32_e64 v233, v233, v235, s[68:69]
	v_mul_f32_e32 v234, 0x37800000, v233
	v_cndmask_b32_e32 v233, v233, v234, vcc
	v_cmp_class_f32_e32 vcc, v232, v223
	s_nop 1
	v_cndmask_b32_e32 v232, v233, v232, vcc
	v_div_scale_f32 v233, s[68:69], v232, v232, 1.0
	v_rcp_f32_e32 v234, v233
	s_nop 0
	v_fma_f32 v235, -v233, v234, 1.0
	v_fmac_f32_e32 v234, v235, v234
	v_div_scale_f32 v235, vcc, 1.0, v232, 1.0
	v_mul_f32_e32 v236, v235, v234
	v_fma_f32 v237, -v233, v236, v235
	v_fmac_f32_e32 v236, v237, v234
	v_fma_f32 v233, -v233, v236, v235
	s_nop 0
	v_div_fmas_f32 v233, v233, v234, v236
	v_div_fixup_f32 v119, v233, v232, 1.0
	v_mul_f32_e32 v56, v119, v56
	v_mul_f32_e32 v57, v119, v57
	v_mul_f32_e32 v58, v119, v58
	v_mul_f32_e32 v59, v119, v59
	v_mul_f32_e32 v60, v119, v60
	v_mul_f32_e32 v61, v119, v61
	v_mul_f32_e32 v62, v119, v62
	v_mul_f32_e32 v63, v119, v63
	v_mov_b32_e32 v238, v56
	v_mov_b32_e32 v106, 0
	v_cmp_gt_f32_e32 vcc, v57, v238
	s_nop 1
	v_cndmask_b32_e32 v238, v238, v57, vcc
	v_cndmask_b32_e64 v106, v106, 1, vcc
	v_cmp_gt_f32_e32 vcc, v58, v238
	s_nop 1
; __global__ void __launch_bounds__(NTHR, 2) fwd_kernel(Args args) {
;     ...
;                 int i0 = 0; float v0 = lg[0];
; #pragma unroll
;                 for (int e = 1; e < 8; ++e) if (lg[e] > v0) { v0 = lg[e]; i0 = e; }
;                 int i1 = -1; float v1 = -__builtin_inff();
; #pragma unroll
;                 for (int e = 0; e < 8; ++e) if (e != i0 && lg[e] > v1) { v1 = lg[e]; i1 = e; }
;                 if (lane == 0) { const int t = t0 + q; const float w0 = 1.0f / (1.0f + expf(v1 - v0));
;                     tok_e[t] = i0 | (i1 << 8); tok_w[2 * t] = w0; tok_w[2 * t + 1] = 1.0f - w0; rstd3[t] = rs;
;                     atomicAdd((int*)&lcnt[i0], 1); atomicAdd((int*)&lcnt[i1], 1); } }
;             __syncthreads();
;             if (tid < 8) cnt_chunk[c * 8 + tid] = lcnt[tid];
;             __syncthreads();
	v_cndmask_b32_e32 v238, v238, v58, vcc
	v_cndmask_b32_e64 v106, v106, 2, vcc
	v_cmp_gt_f32_e32 vcc, v59, v238
	s_nop 1
	v_cndmask_b32_e32 v238, v238, v59, vcc
	v_cndmask_b32_e64 v106, v106, 3, vcc
	v_cmp_gt_f32_e32 vcc, v60, v238
	s_nop 1
	v_cndmask_b32_e32 v238, v238, v60, vcc
	v_cndmask_b32_e64 v106, v106, 4, vcc
	v_cmp_gt_f32_e32 vcc, v61, v238
	s_nop 1
	v_cndmask_b32_e32 v238, v238, v61, vcc
	v_cndmask_b32_e64 v106, v106, 5, vcc
	v_cmp_gt_f32_e32 vcc, v62, v238
	s_nop 1
	v_cndmask_b32_e32 v238, v238, v62, vcc
	v_cndmask_b32_e64 v106, v106, 6, vcc
	v_cmp_gt_f32_e32 vcc, v63, v238
	s_nop 1
	v_cndmask_b32_e32 v238, v238, v63, vcc
	v_cndmask_b32_e64 v106, v106, 7, vcc
	v_mov_b32_e32 v239, v224
	v_mov_b32_e32 v107, -1
	v_cmp_ne_u32_e64 s[68:69], 0, v106
	v_cmp_gt_f32_e32 vcc, v56, v239
	s_and_b64 vcc, vcc, s[68:69]
	v_cndmask_b32_e32 v239, v239, v56, vcc
	v_cndmask_b32_e64 v107, v107, 0, vcc
	v_cmp_ne_u32_e64 s[68:69], 1, v106
	v_cmp_gt_f32_e32 vcc, v57, v239
	s_and_b64 vcc, vcc, s[68:69]
	v_cndmask_b32_e32 v239, v239, v57, vcc
	v_cndmask_b32_e64 v107, v107, 1, vcc
	v_cmp_ne_u32_e64 s[68:69], 2, v106
	v_cmp_gt_f32_e32 vcc, v58, v239
	s_and_b64 vcc, vcc, s[68:69]
	v_cndmask_b32_e32 v239, v239, v58, vcc
	v_cndmask_b32_e64 v107, v107, 2, vcc
	v_cmp_ne_u32_e64 s[68:69], 3, v106
	v_cmp_gt_f32_e32 vcc, v59, v239
	s_and_b64 vcc, vcc, s[68:69]
	v_cndmask_b32_e32 v239, v239, v59, vcc
	v_cndmask_b32_e64 v107, v107, 3, vcc
	v_cmp_ne_u32_e64 s[68:69], 4, v106
	v_cmp_gt_f32_e32 vcc, v60, v239
	s_and_b64 vcc, vcc, s[68:69]
	v_cndmask_b32_e32 v239, v239, v60, vcc
	v_cndmask_b32_e64 v107, v107, 4, vcc
	v_cmp_ne_u32_e64 s[68:69], 5, v106
	v_cmp_gt_f32_e32 vcc, v61, v239
	s_and_b64 vcc, vcc, s[68:69]
	v_cndmask_b32_e32 v239, v239, v61, vcc
	v_cndmask_b32_e64 v107, v107, 5, vcc
	v_cmp_ne_u32_e64 s[68:69], 6, v106
	v_cmp_gt_f32_e32 vcc, v62, v239
	s_and_b64 vcc, vcc, s[68:69]
	v_cndmask_b32_e32 v239, v239, v62, vcc
	v_cndmask_b32_e64 v107, v107, 6, vcc
	v_cmp_ne_u32_e64 s[68:69], 7, v106
	v_cmp_gt_f32_e32 vcc, v63, v239
	s_and_b64 vcc, vcc, s[68:69]
	v_cndmask_b32_e32 v239, v239, v63, vcc
	v_cndmask_b32_e64 v107, v107, 7, vcc
	v_sub_f32_e32 v232, v239, v238
	v_mul_f32_e32 v233, 0x3fb8aa3b, v232
	v_fma_f32 v234, v232, s65, -v233
	v_rndne_f32_e32 v235, v233
	v_fmac_f32_e32 v234, 0x32a5705f, v232
	v_sub_f32_e32 v233, v233, v235
	v_add_f32_e32 v233, v233, v234
	v_exp_f32_e32 v233, v233
	v_cvt_i32_f32_e32 v234, v235
	v_cmp_ngt_f32_e32 vcc, s66, v232
	v_ldexp_f32 v233, v233, v234
	s_nop 0
	v_cndmask_b32_e32 v233, 0, v233, vcc
	v_cmp_nlt_f32_e32 vcc, s67, v232
	s_nop 1
	v_cndmask_b32_e32 v232, v225, v233, vcc
	v_add_f32_e32 v232, 1.0, v232
	v_div_scale_f32 v233, s[68:69], v232, v232, 1.0
	v_rcp_f32_e32 v234, v233
	s_nop 0
	v_fma_f32 v235, -v233, v234, 1.0
	v_fmac_f32_e32 v234, v235, v234
	v_div_scale_f32 v235, vcc, 1.0, v232, 1.0
	v_mul_f32_e32 v236, v235, v234
	v_fma_f32 v237, -v233, v236, v235
	v_fmac_f32_e32 v236, v237, v234
	v_fma_f32 v233, -v233, v236, v235
	s_nop 0
	v_div_fmas_f32 v233, v233, v234, v236
	v_div_fixup_f32 v108, v233, v232, 1.0
	v_sub_f32_e32 v109, 1.0, v108
	v_lshl_add_u32 v110, v107, 8, v106
	s_lshl_b32 s14, s13, 2
	s_add_u32 s56, s8, s14
	s_addc_u32 s57, s9, 0
	s_lshl_b32 s14, s13, 3
	s_add_u32 s58, s8, s14
	s_addc_u32 s59, s9, 0
	v_cmp_eq_u32_e32 vcc, 63, v210
	s_and_saveexec_b64 s[2:3], vcc
	global_store_dword v226, v68, s[56:57] offset:0
	global_store_dwordx2 v227, v[66:67], s[58:59] offset:0
	global_store_dword v228, v112, s[56:57] offset:0
	v_lshl_add_u32 v232, v64, 2, s20
	v_lshl_add_u32 v233, v65, 2, s20
	ds_add_u32 v232, v221
	ds_add_u32 v233, v221
	global_store_dword v226, v74, s[56:57] offset:4
	global_store_dwordx2 v227, v[72:73], s[58:59] offset:8
	global_store_dword v228, v113, s[56:57] offset:4
	v_lshl_add_u32 v232, v70, 2, s20
	v_lshl_add_u32 v233, v71, 2, s20
	ds_add_u32 v232, v221
	ds_add_u32 v233, v221
	global_store_dword v226, v80, s[56:57] offset:8
	global_store_dwordx2 v227, v[78:79], s[58:59] offset:16
	global_store_dword v228, v114, s[56:57] offset:8
	v_lshl_add_u32 v232, v76, 2, s20
	v_lshl_add_u32 v233, v77, 2, s20
	ds_add_u32 v232, v221
	ds_add_u32 v233, v221
	global_store_dword v226, v86, s[56:57] offset:12
	global_store_dwordx2 v227, v[84:85], s[58:59] offset:24
	global_store_dword v228, v115, s[56:57] offset:12
	v_lshl_add_u32 v232, v82, 2, s20
	v_lshl_add_u32 v233, v83, 2, s20
	ds_add_u32 v232, v221
	ds_add_u32 v233, v221
	global_store_dword v226, v92, s[56:57] offset:16
	global_store_dwordx2 v227, v[90:91], s[58:59] offset:32
	global_store_dword v228, v116, s[56:57] offset:16
	v_lshl_add_u32 v232, v88, 2, s20
	v_lshl_add_u32 v233, v89, 2, s20
	ds_add_u32 v232, v221
	ds_add_u32 v233, v221
	global_store_dword v226, v98, s[56:57] offset:20
	global_store_dwordx2 v227, v[96:97], s[58:59] offset:40
	global_store_dword v228, v117, s[56:57] offset:20
	v_lshl_add_u32 v232, v94, 2, s20
	v_lshl_add_u32 v233, v95, 2, s20
	ds_add_u32 v232, v221
	ds_add_u32 v233, v221
	global_store_dword v226, v104, s[56:57] offset:24
	global_store_dwordx2 v227, v[102:103], s[58:59] offset:48
	global_store_dword v228, v118, s[56:57] offset:24
	v_lshl_add_u32 v232, v100, 2, s20
	v_lshl_add_u32 v233, v101, 2, s20
	ds_add_u32 v232, v221
	ds_add_u32 v233, v221
	global_store_dword v226, v110, s[56:57] offset:28
	global_store_dwordx2 v227, v[108:109], s[58:59] offset:56
	global_store_dword v228, v119, s[56:57] offset:28
	v_lshl_add_u32 v232, v106, 2, s20
	v_lshl_add_u32 v233, v107, 2, s20
	ds_add_u32 v232, v221
	ds_add_u32 v233, v221
	s_mov_b64 exec, s[2:3]
	s_waitcnt lgkmcnt(0)
	s_barrier
	v_cmp_gt_u32_e32 vcc, 8, v211
	s_and_saveexec_b64 s[2:3], vcc
	ds_read_b32 v232, v229
	s_lshl_b32 s14, s12, 5
	v_lshl_add_u32 v233, v211, 2, s14
	v_add_u32_e32 v233, 0x392000, v233
	s_waitcnt lgkmcnt(0)
	global_store_dword v233, v232, s[8:9]
	s_mov_b64 exec, s[2:3]
	s_add_i32 s12, s12, s92
	s_cmpk_lt_i32 s12, 0x100
	s_barrier
	s_cbranch_scc1 .Lr14_chunk
